# one static priority raise for waves 4-7 in every GEMM K loop (P1, P4a x3, P4b, P5, P8, P9), per-segment s_setprio toggles removed
# baseline (speedup 1.0000x reference)
.LBB0_284:
	s_cmp_ge_u32 s86, 4
	s_cbranch_scc0 .Lprio_284
	s_setprio 1
.Lprio_284:
	ds_read_b128 v[130:133], v166
	ds_read_b128 v[134:137], v166 offset:1024
	ds_read_b128 v[138:141], v166 offset:2048
	ds_read_b128 v[142:145], v166 offset:3072
	ds_read_b128 v[152:155], v167
	ds_read_b128 v[172:175], v167 offset:1024
	ds_read_b128 v[176:179], v167 offset:2048
	ds_read_b128 v[180:183], v167 offset:3072
	s_add_u32 s20, s18, 0x100
	s_addc_u32 s21, s19, 0
	s_cmp_eq_u32 s61, 12
	s_cselect_b32 s26, s57, s20
	s_cselect_b32 s27, s11, s21
	s_cselect_b32 s24, s58, s59
	s_cselect_b32 s25, s9, s60
	s_add_u32 s22, s26, 0x80
	s_addc_u32 s23, s27, 0
	ds_read_b128 v[184:187], v168
	ds_read_b128 v[188:191], v168 offset:1024
	ds_read_b128 v[192:195], v168 offset:2048
	ds_read_b128 v[196:199], v168 offset:3072
	ds_read_b128 v[200:203], v168 offset:4096
	ds_read_b128 v[204:207], v168 offset:5120
	ds_read_b128 v[224:227], v168 offset:6144
	ds_read_b128 v[228:231], v168 offset:7168
	s_add_u32 s18, s18, 0x40080
	s_addc_u32 s19, s19, 0
	s_mov_b32 s62, m0
	s_mov_b32 m0, s53
	s_nop 3
	global_load_lds_dwordx4 v151, s[18:19]
	s_mov_b32 m0, s62
	s_add_i32 s62, s31, 0xe000
	s_mov_b32 s63, m0
	s_mov_b32 m0, s62
	s_nop 3
	global_load_lds_dwordx4 v159, s[18:19]
	s_mov_b32 m0, s63
	s_waitcnt vmcnt(8)
	s_waitcnt lgkmcnt(0)
	s_barrier
	s_waitcnt lgkmcnt(7)
	v_mfma_f32_16x16x32_bf16 v[126:129], v[130:133], v[184:187], v[126:129]
	v_mfma_f32_16x16x32_bf16 v[122:125], v[138:141], v[184:187], v[122:125]
	s_waitcnt lgkmcnt(5)
	v_mfma_f32_16x16x32_bf16 v[110:113], v[130:133], v[192:195], v[110:113]
	v_mfma_f32_16x16x32_bf16 v[106:109], v[138:141], v[192:195], v[106:109]
	s_waitcnt lgkmcnt(3)
	v_mfma_f32_16x16x32_bf16 v[94:97], v[130:133], v[200:203], v[94:97]
	v_mfma_f32_16x16x32_bf16 v[90:93], v[138:141], v[200:203], v[90:93]
	s_waitcnt lgkmcnt(1)
	v_mfma_f32_16x16x32_bf16 v[78:81], v[130:133], v[224:227], v[78:81]
	v_mfma_f32_16x16x32_bf16 v[74:77], v[138:141], v[224:227], v[74:77]
	v_mfma_f32_16x16x32_bf16 v[126:129], v[134:137], v[188:191], v[126:129]
	v_mfma_f32_16x16x32_bf16 v[122:125], v[142:145], v[188:191], v[122:125]
	v_mfma_f32_16x16x32_bf16 v[110:113], v[134:137], v[196:199], v[110:113]
	v_mfma_f32_16x16x32_bf16 v[106:109], v[142:145], v[196:199], v[106:109]
	v_mfma_f32_16x16x32_bf16 v[94:97], v[134:137], v[204:207], v[94:97]
	v_mfma_f32_16x16x32_bf16 v[90:93], v[142:145], v[204:207], v[90:93]
	s_waitcnt lgkmcnt(0)
	v_mfma_f32_16x16x32_bf16 v[78:81], v[134:137], v[228:231], v[78:81]
	v_mfma_f32_16x16x32_bf16 v[74:77], v[142:145], v[228:231], v[74:77]
	v_mfma_f32_16x16x32_bf16 v[118:121], v[152:155], v[184:187], v[118:121]
	v_mfma_f32_16x16x32_bf16 v[114:117], v[176:179], v[184:187], v[114:117]
	v_mfma_f32_16x16x32_bf16 v[102:105], v[152:155], v[192:195], v[102:105]
	v_mfma_f32_16x16x32_bf16 v[98:101], v[176:179], v[192:195], v[98:101]
	v_mfma_f32_16x16x32_bf16 v[86:89], v[152:155], v[200:203], v[86:89]
	v_mfma_f32_16x16x32_bf16 v[82:85], v[176:179], v[200:203], v[82:85]
	v_mfma_f32_16x16x32_bf16 v[70:73], v[152:155], v[224:227], v[70:73]
	v_mfma_f32_16x16x32_bf16 v[66:69], v[176:179], v[224:227], v[66:69]
	v_mfma_f32_16x16x32_bf16 v[118:121], v[172:175], v[188:191], v[118:121]
	v_mfma_f32_16x16x32_bf16 v[114:117], v[180:183], v[188:191], v[114:117]
	v_mfma_f32_16x16x32_bf16 v[102:105], v[172:175], v[196:199], v[102:105]
	v_mfma_f32_16x16x32_bf16 v[98:101], v[180:183], v[196:199], v[98:101]
	v_mfma_f32_16x16x32_bf16 v[86:89], v[172:175], v[204:207], v[86:89]
	v_mfma_f32_16x16x32_bf16 v[82:85], v[180:183], v[204:207], v[82:85]
	v_mfma_f32_16x16x32_bf16 v[70:73], v[172:175], v[228:231], v[70:73]
	v_mfma_f32_16x16x32_bf16 v[66:69], v[180:183], v[228:231], v[66:69]
	s_barrier
	ds_read_b128 v[184:187], v168 offset:16384
	ds_read_b128 v[188:191], v168 offset:17408
	ds_read_b128 v[192:195], v168 offset:18432
	ds_read_b128 v[196:199], v168 offset:19456
	ds_read_b128 v[200:203], v168 offset:20480
	ds_read_b128 v[204:207], v168 offset:21504
	ds_read_b128 v[224:227], v168 offset:22528
	ds_read_b128 v[228:231], v168 offset:23552
	s_mov_b32 s18, m0
	s_mov_b32 m0, s33
	s_nop 3
	global_load_lds_dwordx4 v158, s[24:25]
	s_mov_b32 m0, s18
	s_nop 0
	s_mov_b32 s18, m0
	s_mov_b32 m0, s34
	s_nop 3
	global_load_lds_dwordx4 v160, s[24:25]
	s_mov_b32 m0, s18
	s_add_u32 s18, s24, 0x40000
	s_addc_u32 s19, s25, 0
	s_mov_b32 s62, m0
	s_mov_b32 m0, s35
	s_nop 3
	global_load_lds_dwordx4 v158, s[18:19]
	s_mov_b32 m0, s62
	s_nop 0
	s_mov_b32 s62, m0
	s_mov_b32 m0, s36
	s_nop 3
	global_load_lds_dwordx4 v160, s[18:19]
	s_mov_b32 m0, s62
	s_mov_b32 s18, m0
	s_mov_b32 m0, s31
	s_nop 3
	global_load_lds_dwordx4 v151, s[26:27]
	s_mov_b32 m0, s18
	s_nop 0
	s_mov_b32 s18, m0
	s_mov_b32 m0, s37
	s_nop 3
	global_load_lds_dwordx4 v159, s[26:27]
	s_mov_b32 m0, s18
	s_waitcnt vmcnt(8)
	s_waitcnt lgkmcnt(0)
	s_barrier
	s_waitcnt lgkmcnt(7)
	v_mfma_f32_16x16x32_bf16 v[62:65], v[130:133], v[184:187], v[62:65]
	v_mfma_f32_16x16x32_bf16 v[58:61], v[138:141], v[184:187], v[58:61]
	s_waitcnt lgkmcnt(5)
	v_mfma_f32_16x16x32_bf16 v[46:49], v[130:133], v[192:195], v[46:49]
	v_mfma_f32_16x16x32_bf16 v[42:45], v[138:141], v[192:195], v[42:45]
	s_waitcnt lgkmcnt(3)
	v_mfma_f32_16x16x32_bf16 v[30:33], v[130:133], v[200:203], v[30:33]
	v_mfma_f32_16x16x32_bf16 v[26:29], v[138:141], v[200:203], v[26:29]
	s_waitcnt lgkmcnt(1)
	v_mfma_f32_16x16x32_bf16 v[14:17], v[130:133], v[224:227], v[14:17]
	v_mfma_f32_16x16x32_bf16 v[10:13], v[138:141], v[224:227], v[10:13]
	v_mfma_f32_16x16x32_bf16 v[62:65], v[134:137], v[188:191], v[62:65]
	v_mfma_f32_16x16x32_bf16 v[58:61], v[142:145], v[188:191], v[58:61]
	v_mfma_f32_16x16x32_bf16 v[46:49], v[134:137], v[196:199], v[46:49]
	v_mfma_f32_16x16x32_bf16 v[42:45], v[142:145], v[196:199], v[42:45]
	v_mfma_f32_16x16x32_bf16 v[30:33], v[134:137], v[204:207], v[30:33]
	v_mfma_f32_16x16x32_bf16 v[26:29], v[142:145], v[204:207], v[26:29]
	s_waitcnt lgkmcnt(0)
	v_mfma_f32_16x16x32_bf16 v[14:17], v[134:137], v[228:231], v[14:17]
	v_mfma_f32_16x16x32_bf16 v[10:13], v[142:145], v[228:231], v[10:13]
	v_mfma_f32_16x16x32_bf16 v[54:57], v[152:155], v[184:187], v[54:57]
	v_mfma_f32_16x16x32_bf16 v[50:53], v[176:179], v[184:187], v[50:53]
	v_mfma_f32_16x16x32_bf16 v[38:41], v[152:155], v[192:195], v[38:41]
	v_mfma_f32_16x16x32_bf16 v[34:37], v[176:179], v[192:195], v[34:37]
	v_mfma_f32_16x16x32_bf16 v[22:25], v[152:155], v[200:203], v[22:25]
	v_mfma_f32_16x16x32_bf16 v[18:21], v[176:179], v[200:203], v[18:21]
	v_mfma_f32_16x16x32_bf16 v[6:9], v[152:155], v[224:227], v[6:9]
	v_mfma_f32_16x16x32_bf16 v[2:5], v[176:179], v[224:227], v[2:5]
	v_mfma_f32_16x16x32_bf16 v[54:57], v[172:175], v[188:191], v[54:57]
	v_mfma_f32_16x16x32_bf16 v[50:53], v[180:183], v[188:191], v[50:53]
	v_mfma_f32_16x16x32_bf16 v[38:41], v[172:175], v[196:199], v[38:41]
	v_mfma_f32_16x16x32_bf16 v[34:37], v[180:183], v[196:199], v[34:37]
	v_mfma_f32_16x16x32_bf16 v[22:25], v[172:175], v[204:207], v[22:25]
	v_mfma_f32_16x16x32_bf16 v[18:21], v[180:183], v[204:207], v[18:21]
	v_mfma_f32_16x16x32_bf16 v[6:9], v[172:175], v[228:231], v[6:9]
	v_mfma_f32_16x16x32_bf16 v[2:5], v[180:183], v[228:231], v[2:5]
	s_barrier
	ds_read_b128 v[130:133], v169
	ds_read_b128 v[134:137], v169 offset:1024
	ds_read_b128 v[138:141], v169 offset:2048
	ds_read_b128 v[142:145], v169 offset:3072
	ds_read_b128 v[152:155], v170
	ds_read_b128 v[172:175], v170 offset:1024
	ds_read_b128 v[176:179], v170 offset:2048
	ds_read_b128 v[180:183], v170 offset:3072
	ds_read_b128 v[184:187], v168 offset:32768
	ds_read_b128 v[188:191], v168 offset:33792
	ds_read_b128 v[192:195], v168 offset:34816
	ds_read_b128 v[196:199], v168 offset:35840
	ds_read_b128 v[200:203], v168 offset:36864
	ds_read_b128 v[204:207], v168 offset:37888
	ds_read_b128 v[224:227], v168 offset:38912
	ds_read_b128 v[228:231], v168 offset:39936
	s_add_u32 s18, s26, 0x40000
	s_addc_u32 s19, s27, 0
	s_mov_b32 s26, m0
	s_mov_b32 m0, s44
	s_nop 3
	global_load_lds_dwordx4 v151, s[18:19]
	s_mov_b32 m0, s26
	s_nop 0
	s_mov_b32 s26, m0
	s_mov_b32 m0, s45
	s_nop 3
	global_load_lds_dwordx4 v159, s[18:19]
	s_mov_b32 m0, s26
	s_waitcnt vmcnt(8)
	s_waitcnt lgkmcnt(0)
	s_barrier
	s_waitcnt lgkmcnt(7)
	v_mfma_f32_16x16x32_bf16 v[126:129], v[130:133], v[184:187], v[126:129]
	v_mfma_f32_16x16x32_bf16 v[122:125], v[138:141], v[184:187], v[122:125]
	s_waitcnt lgkmcnt(5)
	v_mfma_f32_16x16x32_bf16 v[110:113], v[130:133], v[192:195], v[110:113]
	v_mfma_f32_16x16x32_bf16 v[106:109], v[138:141], v[192:195], v[106:109]
	s_waitcnt lgkmcnt(3)
	v_mfma_f32_16x16x32_bf16 v[94:97], v[130:133], v[200:203], v[94:97]
	v_mfma_f32_16x16x32_bf16 v[90:93], v[138:141], v[200:203], v[90:93]
	s_waitcnt lgkmcnt(1)
	v_mfma_f32_16x16x32_bf16 v[78:81], v[130:133], v[224:227], v[78:81]
	v_mfma_f32_16x16x32_bf16 v[74:77], v[138:141], v[224:227], v[74:77]
	v_mfma_f32_16x16x32_bf16 v[126:129], v[134:137], v[188:191], v[126:129]
	v_mfma_f32_16x16x32_bf16 v[122:125], v[142:145], v[188:191], v[122:125]
	v_mfma_f32_16x16x32_bf16 v[110:113], v[134:137], v[196:199], v[110:113]
	v_mfma_f32_16x16x32_bf16 v[106:109], v[142:145], v[196:199], v[106:109]
	v_mfma_f32_16x16x32_bf16 v[94:97], v[134:137], v[204:207], v[94:97]
	v_mfma_f32_16x16x32_bf16 v[90:93], v[142:145], v[204:207], v[90:93]
	s_waitcnt lgkmcnt(0)
	v_mfma_f32_16x16x32_bf16 v[78:81], v[134:137], v[228:231], v[78:81]
	v_mfma_f32_16x16x32_bf16 v[74:77], v[142:145], v[228:231], v[74:77]
	v_mfma_f32_16x16x32_bf16 v[118:121], v[152:155], v[184:187], v[118:121]
	v_mfma_f32_16x16x32_bf16 v[114:117], v[176:179], v[184:187], v[114:117]
	v_mfma_f32_16x16x32_bf16 v[102:105], v[152:155], v[192:195], v[102:105]
	v_mfma_f32_16x16x32_bf16 v[98:101], v[176:179], v[192:195], v[98:101]
	v_mfma_f32_16x16x32_bf16 v[86:89], v[152:155], v[200:203], v[86:89]
	v_mfma_f32_16x16x32_bf16 v[82:85], v[176:179], v[200:203], v[82:85]
	v_mfma_f32_16x16x32_bf16 v[70:73], v[152:155], v[224:227], v[70:73]
	v_mfma_f32_16x16x32_bf16 v[66:69], v[176:179], v[224:227], v[66:69]
	v_mfma_f32_16x16x32_bf16 v[118:121], v[172:175], v[188:191], v[118:121]
	v_mfma_f32_16x16x32_bf16 v[114:117], v[180:183], v[188:191], v[114:117]
	v_mfma_f32_16x16x32_bf16 v[102:105], v[172:175], v[196:199], v[102:105]
	v_mfma_f32_16x16x32_bf16 v[98:101], v[180:183], v[196:199], v[98:101]
	v_mfma_f32_16x16x32_bf16 v[86:89], v[172:175], v[204:207], v[86:89]
	v_mfma_f32_16x16x32_bf16 v[82:85], v[180:183], v[204:207], v[82:85]
	v_mfma_f32_16x16x32_bf16 v[70:73], v[172:175], v[228:231], v[70:73]
	v_mfma_f32_16x16x32_bf16 v[66:69], v[180:183], v[228:231], v[66:69]
	s_barrier
	ds_read_b128 v[184:187], v168 offset:49152
	ds_read_b128 v[188:191], v168 offset:50176
	ds_read_b128 v[192:195], v168 offset:51200
	ds_read_b128 v[196:199], v168 offset:52224
	ds_read_b128 v[200:203], v168 offset:53248
	ds_read_b128 v[204:207], v168 offset:54272
	ds_read_b128 v[224:227], v168 offset:55296
	ds_read_b128 v[228:231], v168 offset:56320
	s_add_u32 s18, s24, 0x80
	s_addc_u32 s19, s25, 0
	s_mov_b32 s26, m0
	s_mov_b32 m0, s47
	s_nop 3
	global_load_lds_dwordx4 v158, s[18:19]
	s_mov_b32 m0, s26
	s_nop 0
	s_mov_b32 s26, m0
	s_mov_b32 m0, s48
	s_nop 3
	global_load_lds_dwordx4 v160, s[18:19]
	s_mov_b32 m0, s26
	s_add_u32 s18, s24, 0x40080
	s_addc_u32 s19, s25, 0
	s_mov_b32 s24, m0
	s_mov_b32 m0, s51
	s_nop 3
	global_load_lds_dwordx4 v158, s[18:19]
	s_mov_b32 m0, s24
	s_nop 0
	s_mov_b32 s24, m0
	s_mov_b32 m0, s52
	s_nop 3
	global_load_lds_dwordx4 v160, s[18:19]
	s_mov_b32 m0, s24
	s_mov_b32 s18, m0
	s_mov_b32 m0, s49
	s_nop 3
	global_load_lds_dwordx4 v151, s[22:23]
	s_mov_b32 m0, s18
	s_nop 0
	s_mov_b32 s18, m0
	s_mov_b32 m0, s50
	s_nop 3
	global_load_lds_dwordx4 v159, s[22:23]
	s_mov_b32 m0, s18
	s_waitcnt vmcnt(8)
	s_waitcnt lgkmcnt(0)
	s_barrier
	s_waitcnt lgkmcnt(7)
	v_mfma_f32_16x16x32_bf16 v[62:65], v[130:133], v[184:187], v[62:65]
	v_mfma_f32_16x16x32_bf16 v[58:61], v[138:141], v[184:187], v[58:61]
	s_waitcnt lgkmcnt(5)
	v_mfma_f32_16x16x32_bf16 v[46:49], v[130:133], v[192:195], v[46:49]
	v_mfma_f32_16x16x32_bf16 v[42:45], v[138:141], v[192:195], v[42:45]
	s_waitcnt lgkmcnt(3)
	v_mfma_f32_16x16x32_bf16 v[30:33], v[130:133], v[200:203], v[30:33]
	v_mfma_f32_16x16x32_bf16 v[26:29], v[138:141], v[200:203], v[26:29]
	s_waitcnt lgkmcnt(1)
	v_mfma_f32_16x16x32_bf16 v[14:17], v[130:133], v[224:227], v[14:17]
	v_mfma_f32_16x16x32_bf16 v[10:13], v[138:141], v[224:227], v[10:13]
	v_mfma_f32_16x16x32_bf16 v[62:65], v[134:137], v[188:191], v[62:65]
	v_mfma_f32_16x16x32_bf16 v[58:61], v[142:145], v[188:191], v[58:61]
	v_mfma_f32_16x16x32_bf16 v[46:49], v[134:137], v[196:199], v[46:49]
	v_mfma_f32_16x16x32_bf16 v[42:45], v[142:145], v[196:199], v[42:45]
	v_mfma_f32_16x16x32_bf16 v[30:33], v[134:137], v[204:207], v[30:33]
	v_mfma_f32_16x16x32_bf16 v[26:29], v[142:145], v[204:207], v[26:29]
	s_waitcnt lgkmcnt(0)
	v_mfma_f32_16x16x32_bf16 v[14:17], v[134:137], v[228:231], v[14:17]
	v_mfma_f32_16x16x32_bf16 v[10:13], v[142:145], v[228:231], v[10:13]
	v_mfma_f32_16x16x32_bf16 v[54:57], v[152:155], v[184:187], v[54:57]
	v_mfma_f32_16x16x32_bf16 v[50:53], v[176:179], v[184:187], v[50:53]
	v_mfma_f32_16x16x32_bf16 v[38:41], v[152:155], v[192:195], v[38:41]
	v_mfma_f32_16x16x32_bf16 v[34:37], v[176:179], v[192:195], v[34:37]
	v_mfma_f32_16x16x32_bf16 v[22:25], v[152:155], v[200:203], v[22:25]
	v_mfma_f32_16x16x32_bf16 v[18:21], v[176:179], v[200:203], v[18:21]
	v_mfma_f32_16x16x32_bf16 v[6:9], v[152:155], v[224:227], v[6:9]
	v_mfma_f32_16x16x32_bf16 v[2:5], v[176:179], v[224:227], v[2:5]
	v_mfma_f32_16x16x32_bf16 v[54:57], v[172:175], v[188:191], v[54:57]
	v_mfma_f32_16x16x32_bf16 v[50:53], v[180:183], v[188:191], v[50:53]
	v_mfma_f32_16x16x32_bf16 v[38:41], v[172:175], v[196:199], v[38:41]
	v_mfma_f32_16x16x32_bf16 v[34:37], v[180:183], v[196:199], v[34:37]
	v_mfma_f32_16x16x32_bf16 v[22:25], v[172:175], v[204:207], v[22:25]
	v_mfma_f32_16x16x32_bf16 v[18:21], v[180:183], v[204:207], v[18:21]
	v_mfma_f32_16x16x32_bf16 v[6:9], v[172:175], v[228:231], v[6:9]
	v_mfma_f32_16x16x32_bf16 v[2:5], v[180:183], v[228:231], v[2:5]
	s_barrier
	s_add_i32 s61, s61, 2
	s_add_u32 s59, s59, 0x100
	s_addc_u32 s60, s60, 0
	s_cmp_gt_u32 s61, 13
	s_mov_b64 s[18:19], s[20:21]
	s_cbranch_scc0 .LBB0_284
	s_and_b64 vcc, exec, s[6:7]
	s_cbranch_vccz .LBB0_287
	s_barrier
.LBB0_287:
	s_setprio 0
	s_lshl_b32 s9, s56, 8
	s_add_i32 s9, s9, s46
	s_cmp_lt_i32 s55, 4
	s_cselect_b64 vcc, -1, 0
	s_cmp_lt_i32 s55, 5
	s_cselect_b64 s[18:19], -1, 0
	s_cmpk_lt_i32 s56, 0x100
	v_mov_b32_e32 v130, 0x3e38aa3b
	v_or_b32_e32 v0, s9, v161
	v_lshl_or_b32 v148, s55, 8, v165
	s_cselect_b64 s[20:21], -1, 0
	v_cndmask_b32_e32 v150, 1.0, v130, vcc
	v_mov_b64_e32 v[130:131], s[4:5]
	s_movk_i32 s11, 0x2c00
	s_and_b64 s[20:21], s[18:19], s[20:21]
	v_ashrrev_i32_e32 v149, 31, v148
	v_mad_i64_i32 v[130:131], s[18:19], v0, s11, v[130:131]
	v_lshl_add_u64 v[154:155], v[148:149], 1, v[130:131]
	s_mov_b64 s[18:19], -1
	s_and_b64 vcc, exec, s[20:21]
	v_or_b32_e32 v178, 16, v0
	v_lshlrev_b64 v[152:153], 1, v[148:149]
	v_or_b32_e32 v176, 32, v0
	v_or_b32_e32 v175, 48, v0
	v_add_u32_e32 v174, 0x80, v0
	v_add_u32_e32 v173, 0x90, v0
	v_add_u32_e32 v172, 0xa0, v0
	v_add_u32_e32 v171, 0xb0, v0
	s_cbranch_vccnz .LBB0_289
	v_pk_mul_f32 v[132:133], v[150:151], v[128:129] op_sel_hi:[0,1]
	v_pk_mul_f32 v[130:131], v[150:151], v[126:127] op_sel_hi:[0,1]
	v_pk_mul_f32 v[134:135], v[150:151], v[124:125] op_sel_hi:[0,1]
	v_pk_mul_f32 v[136:137], v[150:151], v[122:123] op_sel_hi:[0,1]
	v_cvt_pk_bf16_f32 v130, v130, v131
	v_cvt_pk_bf16_f32 v131, v132, v133
	v_cvt_pk_bf16_f32 v132, v136, v137
	v_cvt_pk_bf16_f32 v133, v134, v135
	global_store_dwordx4 v[154:155], v[130:133], off
	v_pk_mul_f32 v[134:135], v[150:151], v[116:117] op_sel_hi:[0,1]
	v_pk_mul_f32 v[136:137], v[150:151], v[114:115] op_sel_hi:[0,1]
	v_pk_mul_f32 v[132:133], v[150:151], v[120:121] op_sel_hi:[0,1]
	v_pk_mul_f32 v[130:131], v[150:151], v[118:119] op_sel_hi:[0,1]
	v_cvt_pk_bf16_f32 v130, v130, v131
	v_cvt_pk_bf16_f32 v131, v132, v133
	v_cvt_pk_bf16_f32 v132, v136, v137
	v_cvt_pk_bf16_f32 v133, v134, v135
	v_mov_b64_e32 v[136:137], s[4:5]
	global_store_dwordx4 v[154:155], v[130:133], off offset:256
	v_pk_mul_f32 v[138:139], v[150:151], v[108:109] op_sel_hi:[0,1]
	v_pk_mul_f32 v[140:141], v[150:151], v[106:107] op_sel_hi:[0,1]
	v_mad_i64_i32 v[130:131], s[18:19], v178, s11, v[136:137]
	v_lshl_add_u64 v[134:135], v[130:131], 0, v[152:153]
	v_pk_mul_f32 v[132:133], v[150:151], v[112:113] op_sel_hi:[0,1]
	v_pk_mul_f32 v[130:131], v[150:151], v[110:111] op_sel_hi:[0,1]
	v_cvt_pk_bf16_f32 v130, v130, v131
	v_cvt_pk_bf16_f32 v131, v132, v133
	v_cvt_pk_bf16_f32 v132, v140, v141
	v_cvt_pk_bf16_f32 v133, v138, v139
	global_store_dwordx4 v[134:135], v[130:133], off
	v_pk_mul_f32 v[138:139], v[150:151], v[100:101] op_sel_hi:[0,1]
	v_pk_mul_f32 v[140:141], v[150:151], v[98:99] op_sel_hi:[0,1]
	v_pk_mul_f32 v[132:133], v[150:151], v[104:105] op_sel_hi:[0,1]
	v_pk_mul_f32 v[130:131], v[150:151], v[102:103] op_sel_hi:[0,1]
	v_cvt_pk_bf16_f32 v130, v130, v131
	v_cvt_pk_bf16_f32 v131, v132, v133
	v_cvt_pk_bf16_f32 v132, v140, v141
	v_cvt_pk_bf16_f32 v133, v138, v139
	global_store_dwordx4 v[134:135], v[130:133], off offset:256
	v_pk_mul_f32 v[138:139], v[150:151], v[92:93] op_sel_hi:[0,1]
	v_pk_mul_f32 v[140:141], v[150:151], v[90:91] op_sel_hi:[0,1]
	v_mad_i64_i32 v[130:131], s[18:19], v176, s11, v[136:137]
	v_lshl_add_u64 v[134:135], v[130:131], 0, v[152:153]
	v_pk_mul_f32 v[132:133], v[150:151], v[96:97] op_sel_hi:[0,1]
	v_pk_mul_f32 v[130:131], v[150:151], v[94:95] op_sel_hi:[0,1]
	v_cvt_pk_bf16_f32 v130, v130, v131
	v_cvt_pk_bf16_f32 v131, v132, v133
	v_cvt_pk_bf16_f32 v132, v140, v141
	v_cvt_pk_bf16_f32 v133, v138, v139
	global_store_dwordx4 v[134:135], v[130:133], off
	v_pk_mul_f32 v[138:139], v[150:151], v[84:85] op_sel_hi:[0,1]
	v_pk_mul_f32 v[140:141], v[150:151], v[82:83] op_sel_hi:[0,1]
	v_pk_mul_f32 v[132:133], v[150:151], v[88:89] op_sel_hi:[0,1]
	v_pk_mul_f32 v[130:131], v[150:151], v[86:87] op_sel_hi:[0,1]
	v_cvt_pk_bf16_f32 v130, v130, v131
	v_cvt_pk_bf16_f32 v131, v132, v133
	v_cvt_pk_bf16_f32 v132, v140, v141
	v_cvt_pk_bf16_f32 v133, v138, v139
	global_store_dwordx4 v[134:135], v[130:133], off offset:256
	v_pk_mul_f32 v[138:139], v[150:151], v[76:77] op_sel_hi:[0,1]
	v_pk_mul_f32 v[140:141], v[150:151], v[74:75] op_sel_hi:[0,1]
	v_mad_i64_i32 v[130:131], s[18:19], v175, s11, v[136:137]
	v_lshl_add_u64 v[134:135], v[130:131], 0, v[152:153]
	v_pk_mul_f32 v[132:133], v[150:151], v[80:81] op_sel_hi:[0,1]
	v_pk_mul_f32 v[130:131], v[150:151], v[78:79] op_sel_hi:[0,1]
	v_cvt_pk_bf16_f32 v130, v130, v131
	v_cvt_pk_bf16_f32 v131, v132, v133
	v_cvt_pk_bf16_f32 v132, v140, v141
	v_cvt_pk_bf16_f32 v133, v138, v139
	global_store_dwordx4 v[134:135], v[130:133], off
	v_pk_mul_f32 v[138:139], v[150:151], v[68:69] op_sel_hi:[0,1]
	v_pk_mul_f32 v[140:141], v[150:151], v[66:67] op_sel_hi:[0,1]
	v_pk_mul_f32 v[132:133], v[150:151], v[72:73] op_sel_hi:[0,1]
	v_pk_mul_f32 v[130:131], v[150:151], v[70:71] op_sel_hi:[0,1]
	v_cvt_pk_bf16_f32 v130, v130, v131
	v_cvt_pk_bf16_f32 v131, v132, v133
	v_cvt_pk_bf16_f32 v132, v140, v141
	v_cvt_pk_bf16_f32 v133, v138, v139
	global_store_dwordx4 v[134:135], v[130:133], off offset:256
	v_pk_mul_f32 v[138:139], v[150:151], v[60:61] op_sel_hi:[0,1]
	v_pk_mul_f32 v[140:141], v[150:151], v[58:59] op_sel_hi:[0,1]
	v_mad_i64_i32 v[130:131], s[18:19], v174, s11, v[136:137]
	v_lshl_add_u64 v[134:135], v[130:131], 0, v[152:153]
	v_pk_mul_f32 v[132:133], v[150:151], v[64:65] op_sel_hi:[0,1]
	v_pk_mul_f32 v[130:131], v[150:151], v[62:63] op_sel_hi:[0,1]
	v_cvt_pk_bf16_f32 v130, v130, v131
	v_cvt_pk_bf16_f32 v131, v132, v133
	v_cvt_pk_bf16_f32 v132, v140, v141
	v_cvt_pk_bf16_f32 v133, v138, v139
	global_store_dwordx4 v[134:135], v[130:133], off
	v_pk_mul_f32 v[138:139], v[150:151], v[52:53] op_sel_hi:[0,1]
	v_pk_mul_f32 v[140:141], v[150:151], v[50:51] op_sel_hi:[0,1]
	v_pk_mul_f32 v[132:133], v[150:151], v[56:57] op_sel_hi:[0,1]
	v_pk_mul_f32 v[130:131], v[150:151], v[54:55] op_sel_hi:[0,1]
	v_cvt_pk_bf16_f32 v130, v130, v131
	v_cvt_pk_bf16_f32 v131, v132, v133
	v_cvt_pk_bf16_f32 v132, v140, v141
	v_cvt_pk_bf16_f32 v133, v138, v139
	global_store_dwordx4 v[134:135], v[130:133], off offset:256
	v_pk_mul_f32 v[138:139], v[150:151], v[44:45] op_sel_hi:[0,1]
	v_pk_mul_f32 v[140:141], v[150:151], v[42:43] op_sel_hi:[0,1]
	v_mad_i64_i32 v[130:131], s[18:19], v173, s11, v[136:137]
	v_lshl_add_u64 v[134:135], v[130:131], 0, v[152:153]
	v_pk_mul_f32 v[132:133], v[150:151], v[48:49] op_sel_hi:[0,1]
	v_pk_mul_f32 v[130:131], v[150:151], v[46:47] op_sel_hi:[0,1]
	v_cvt_pk_bf16_f32 v130, v130, v131
	v_cvt_pk_bf16_f32 v131, v132, v133
	v_cvt_pk_bf16_f32 v132, v140, v141
	v_cvt_pk_bf16_f32 v133, v138, v139
	global_store_dwordx4 v[134:135], v[130:133], off
	v_pk_mul_f32 v[138:139], v[150:151], v[36:37] op_sel_hi:[0,1]
	v_pk_mul_f32 v[140:141], v[150:151], v[34:35] op_sel_hi:[0,1]
	v_pk_mul_f32 v[132:133], v[150:151], v[40:41] op_sel_hi:[0,1]
	v_pk_mul_f32 v[130:131], v[150:151], v[38:39] op_sel_hi:[0,1]
	v_cvt_pk_bf16_f32 v130, v130, v131
	v_cvt_pk_bf16_f32 v131, v132, v133
	v_cvt_pk_bf16_f32 v132, v140, v141
	v_cvt_pk_bf16_f32 v133, v138, v139
	global_store_dwordx4 v[134:135], v[130:133], off offset:256
	v_pk_mul_f32 v[138:139], v[150:151], v[28:29] op_sel_hi:[0,1]
	v_pk_mul_f32 v[140:141], v[150:151], v[26:27] op_sel_hi:[0,1]
	v_mad_i64_i32 v[130:131], s[18:19], v172, s11, v[136:137]
	v_lshl_add_u64 v[134:135], v[130:131], 0, v[152:153]
	v_pk_mul_f32 v[132:133], v[150:151], v[32:33] op_sel_hi:[0,1]
	v_pk_mul_f32 v[130:131], v[150:151], v[30:31] op_sel_hi:[0,1]
	v_cvt_pk_bf16_f32 v130, v130, v131
	v_cvt_pk_bf16_f32 v131, v132, v133
	v_cvt_pk_bf16_f32 v132, v140, v141
	v_cvt_pk_bf16_f32 v133, v138, v139
	global_store_dwordx4 v[134:135], v[130:133], off
	v_pk_mul_f32 v[138:139], v[150:151], v[20:21] op_sel_hi:[0,1]
	v_pk_mul_f32 v[140:141], v[150:151], v[18:19] op_sel_hi:[0,1]
	v_pk_mul_f32 v[132:133], v[150:151], v[24:25] op_sel_hi:[0,1]
	v_pk_mul_f32 v[130:131], v[150:151], v[22:23] op_sel_hi:[0,1]
	v_cvt_pk_bf16_f32 v130, v130, v131
	v_cvt_pk_bf16_f32 v131, v132, v133
	v_cvt_pk_bf16_f32 v132, v140, v141
	v_cvt_pk_bf16_f32 v133, v138, v139
	global_store_dwordx4 v[134:135], v[130:133], off offset:256
	v_pk_mul_f32 v[138:139], v[150:151], v[12:13] op_sel_hi:[0,1]
	v_pk_mul_f32 v[140:141], v[150:151], v[10:11] op_sel_hi:[0,1]
	v_mad_i64_i32 v[130:131], s[18:19], v171, s11, v[136:137]
	v_lshl_add_u64 v[136:137], v[130:131], 0, v[152:153]
	v_pk_mul_f32 v[132:133], v[150:151], v[16:17] op_sel_hi:[0,1]
	v_pk_mul_f32 v[130:131], v[150:151], v[14:15] op_sel_hi:[0,1]
	v_cvt_pk_bf16_f32 v130, v130, v131
	v_cvt_pk_bf16_f32 v131, v132, v133
	v_cvt_pk_bf16_f32 v132, v140, v141
	v_cvt_pk_bf16_f32 v133, v138, v139
	v_mad_i64_i32 v[134:135], s[18:19], v171, s11, 0
	global_store_dwordx4 v[136:137], v[130:133], off
	v_pk_mul_f32 v[138:139], v[150:151], v[2:3] op_sel_hi:[0,1]
	v_pk_mul_f32 v[136:137], v[150:151], v[4:5] op_sel_hi:[0,1]
	v_pk_mul_f32 v[132:133], v[150:151], v[8:9] op_sel_hi:[0,1]
	v_pk_mul_f32 v[130:131], v[150:151], v[6:7] op_sel_hi:[0,1]
	v_cvt_pk_bf16_f32 v130, v130, v131
	v_cvt_pk_bf16_f32 v131, v132, v133
	v_cvt_pk_bf16_f32 v132, v138, v139
	s_mov_b64 s[18:19], 0

.Lprio_694:
	v_add_u32_e32 v141, 0x10000, v139
	ds_read_b128 v[130:133], v141
	ds_read_b128 v[142:145], v141 offset:1024
	ds_read_b128 v[146:149], v141 offset:2048
	ds_read_b128 v[150:153], v141 offset:3072
	v_add_u32_e32 v141, 0x14000, v139
	ds_read_b128 v[154:157], v141
	ds_read_b128 v[158:161], v141 offset:1024
	ds_read_b128 v[162:165], v141 offset:2048
	ds_read_b128 v[166:169], v141 offset:3072
	s_add_u32 s4, s22, 0x100
	s_addc_u32 s5, s23, 0
	s_cmp_eq_u32 s59, 12
	s_cselect_b32 s28, s16, s4
	s_cselect_b32 s29, s17, s5
	s_cselect_b32 s26, s56, s57
	s_cselect_b32 s27, s13, s58
	s_add_u32 s24, s28, 0x80
	s_addc_u32 s25, s29, 0
	ds_read_b128 v[170:173], v140
	ds_read_b128 v[174:177], v140 offset:1024
	ds_read_b128 v[178:181], v140 offset:2048
	ds_read_b128 v[182:185], v140 offset:3072
	ds_read_b128 v[186:189], v140 offset:4096
	ds_read_b128 v[190:193], v140 offset:5120
	ds_read_b128 v[194:197], v140 offset:6144
	ds_read_b128 v[198:201], v140 offset:7168
	s_add_u32 s22, s22, 0x160080
	s_addc_u32 s23, s23, 0
	s_mov_b32 s60, m0
	s_mov_b32 m0, s52
	s_nop 3
	global_load_lds_dwordx4 v0, s[22:23]
	s_mov_b32 m0, s60
	s_add_i32 s60, s21, 0xe000
	s_mov_b32 s61, m0
	s_mov_b32 m0, s60
	s_nop 3
	global_load_lds_dwordx4 v135, s[22:23]
	s_mov_b32 m0, s61
	s_waitcnt vmcnt(8)
	s_waitcnt lgkmcnt(0)
	s_barrier
	s_waitcnt lgkmcnt(7)
	v_mfma_f32_16x16x32_bf16 v[126:129], v[130:133], v[170:173], v[126:129]
	v_mfma_f32_16x16x32_bf16 v[122:125], v[146:149], v[170:173], v[122:125]
	s_waitcnt lgkmcnt(5)
	v_mfma_f32_16x16x32_bf16 v[118:121], v[130:133], v[178:181], v[118:121]
	v_mfma_f32_16x16x32_bf16 v[110:113], v[146:149], v[178:181], v[110:113]
	s_waitcnt lgkmcnt(3)
	v_mfma_f32_16x16x32_bf16 v[102:105], v[130:133], v[186:189], v[102:105]
	v_mfma_f32_16x16x32_bf16 v[94:97], v[146:149], v[186:189], v[94:97]
	s_waitcnt lgkmcnt(1)
	v_mfma_f32_16x16x32_bf16 v[86:89], v[130:133], v[194:197], v[86:89]
	v_mfma_f32_16x16x32_bf16 v[78:81], v[146:149], v[194:197], v[78:81]
	v_mfma_f32_16x16x32_bf16 v[126:129], v[142:145], v[174:177], v[126:129]
	v_mfma_f32_16x16x32_bf16 v[122:125], v[150:153], v[174:177], v[122:125]
	v_mfma_f32_16x16x32_bf16 v[118:121], v[142:145], v[182:185], v[118:121]
	v_mfma_f32_16x16x32_bf16 v[110:113], v[150:153], v[182:185], v[110:113]
	v_mfma_f32_16x16x32_bf16 v[102:105], v[142:145], v[190:193], v[102:105]
	v_mfma_f32_16x16x32_bf16 v[94:97], v[150:153], v[190:193], v[94:97]
	s_waitcnt lgkmcnt(0)
	v_mfma_f32_16x16x32_bf16 v[86:89], v[142:145], v[198:201], v[86:89]
	v_mfma_f32_16x16x32_bf16 v[78:81], v[150:153], v[198:201], v[78:81]
	v_mfma_f32_16x16x32_bf16 v[114:117], v[154:157], v[170:173], v[114:117]
	v_mfma_f32_16x16x32_bf16 v[106:109], v[162:165], v[170:173], v[106:109]
	v_mfma_f32_16x16x32_bf16 v[98:101], v[154:157], v[178:181], v[98:101]
	v_mfma_f32_16x16x32_bf16 v[90:93], v[162:165], v[178:181], v[90:93]
	v_mfma_f32_16x16x32_bf16 v[82:85], v[154:157], v[186:189], v[82:85]
	v_mfma_f32_16x16x32_bf16 v[74:77], v[162:165], v[186:189], v[74:77]
	v_mfma_f32_16x16x32_bf16 v[70:73], v[154:157], v[194:197], v[70:73]
	v_mfma_f32_16x16x32_bf16 v[66:69], v[162:165], v[194:197], v[66:69]
	v_mfma_f32_16x16x32_bf16 v[114:117], v[158:161], v[174:177], v[114:117]
	v_mfma_f32_16x16x32_bf16 v[106:109], v[166:169], v[174:177], v[106:109]
	v_mfma_f32_16x16x32_bf16 v[98:101], v[158:161], v[182:185], v[98:101]
	v_mfma_f32_16x16x32_bf16 v[90:93], v[166:169], v[182:185], v[90:93]
	v_mfma_f32_16x16x32_bf16 v[82:85], v[158:161], v[190:193], v[82:85]
	v_mfma_f32_16x16x32_bf16 v[74:77], v[166:169], v[190:193], v[74:77]
	v_mfma_f32_16x16x32_bf16 v[70:73], v[158:161], v[198:201], v[70:73]
	v_mfma_f32_16x16x32_bf16 v[66:69], v[166:169], v[198:201], v[66:69]
	s_barrier
	ds_read_b128 v[170:173], v140 offset:16384
	ds_read_b128 v[174:177], v140 offset:17408
	ds_read_b128 v[178:181], v140 offset:18432
	ds_read_b128 v[182:185], v140 offset:19456
	ds_read_b128 v[186:189], v140 offset:20480
	ds_read_b128 v[190:193], v140 offset:21504
	ds_read_b128 v[194:197], v140 offset:22528
	ds_read_b128 v[198:201], v140 offset:23552
	s_mov_b32 s22, m0
	s_mov_b32 m0, s38
	s_nop 3
	global_load_lds_dwordx4 v134, s[26:27]
	s_mov_b32 m0, s22
	s_nop 0
	s_mov_b32 s22, m0
	s_mov_b32 m0, s39
	s_nop 3
	global_load_lds_dwordx4 v136, s[26:27]
	s_mov_b32 m0, s22
	s_add_u32 s22, s26, 0x40000
	s_addc_u32 s23, s27, 0
	s_mov_b32 s60, m0
	s_mov_b32 m0, s40
	s_nop 3
	global_load_lds_dwordx4 v134, s[22:23]
	s_mov_b32 m0, s60
	s_nop 0
	s_mov_b32 s60, m0
	s_mov_b32 m0, s41
	s_nop 3
	global_load_lds_dwordx4 v136, s[22:23]
	s_mov_b32 m0, s60
	s_mov_b32 s22, m0
	s_mov_b32 m0, s21
	s_nop 3
	global_load_lds_dwordx4 v0, s[28:29]
	s_mov_b32 m0, s22
	s_nop 0
	s_mov_b32 s22, m0
	s_mov_b32 m0, s42
	s_nop 3
	global_load_lds_dwordx4 v135, s[28:29]
	s_mov_b32 m0, s22
	s_waitcnt vmcnt(8)
	s_waitcnt lgkmcnt(0)
	s_barrier
	s_waitcnt lgkmcnt(7)
	v_mfma_f32_16x16x32_bf16 v[62:65], v[130:133], v[170:173], v[62:65]
	v_mfma_f32_16x16x32_bf16 v[58:61], v[146:149], v[170:173], v[58:61]
	s_waitcnt lgkmcnt(5)
	v_mfma_f32_16x16x32_bf16 v[54:57], v[130:133], v[178:181], v[54:57]
	v_mfma_f32_16x16x32_bf16 v[46:49], v[146:149], v[178:181], v[46:49]
	s_waitcnt lgkmcnt(3)
	v_mfma_f32_16x16x32_bf16 v[38:41], v[130:133], v[186:189], v[38:41]
	v_mfma_f32_16x16x32_bf16 v[30:33], v[146:149], v[186:189], v[30:33]
	s_waitcnt lgkmcnt(1)
	v_mfma_f32_16x16x32_bf16 v[22:25], v[130:133], v[194:197], v[22:25]
	v_mfma_f32_16x16x32_bf16 v[14:17], v[146:149], v[194:197], v[14:17]
	v_mfma_f32_16x16x32_bf16 v[62:65], v[142:145], v[174:177], v[62:65]
	v_mfma_f32_16x16x32_bf16 v[58:61], v[150:153], v[174:177], v[58:61]
	v_mfma_f32_16x16x32_bf16 v[54:57], v[142:145], v[182:185], v[54:57]
	v_mfma_f32_16x16x32_bf16 v[46:49], v[150:153], v[182:185], v[46:49]
	v_mfma_f32_16x16x32_bf16 v[38:41], v[142:145], v[190:193], v[38:41]
	v_mfma_f32_16x16x32_bf16 v[30:33], v[150:153], v[190:193], v[30:33]
	s_waitcnt lgkmcnt(0)
	v_mfma_f32_16x16x32_bf16 v[22:25], v[142:145], v[198:201], v[22:25]
	v_mfma_f32_16x16x32_bf16 v[14:17], v[150:153], v[198:201], v[14:17]
	v_mfma_f32_16x16x32_bf16 v[50:53], v[154:157], v[170:173], v[50:53]
	v_mfma_f32_16x16x32_bf16 v[42:45], v[162:165], v[170:173], v[42:45]
	v_mfma_f32_16x16x32_bf16 v[34:37], v[154:157], v[178:181], v[34:37]
	v_mfma_f32_16x16x32_bf16 v[26:29], v[162:165], v[178:181], v[26:29]
	v_mfma_f32_16x16x32_bf16 v[18:21], v[154:157], v[186:189], v[18:21]
	v_mfma_f32_16x16x32_bf16 v[10:13], v[162:165], v[186:189], v[10:13]
	v_mfma_f32_16x16x32_bf16 v[6:9], v[154:157], v[194:197], v[6:9]
	v_mfma_f32_16x16x32_bf16 v[2:5], v[162:165], v[194:197], v[2:5]
	v_mfma_f32_16x16x32_bf16 v[50:53], v[158:161], v[174:177], v[50:53]
	v_mfma_f32_16x16x32_bf16 v[42:45], v[166:169], v[174:177], v[42:45]
	v_mfma_f32_16x16x32_bf16 v[34:37], v[158:161], v[182:185], v[34:37]
	v_mfma_f32_16x16x32_bf16 v[26:29], v[166:169], v[182:185], v[26:29]
	v_mfma_f32_16x16x32_bf16 v[18:21], v[158:161], v[190:193], v[18:21]
	v_mfma_f32_16x16x32_bf16 v[10:13], v[166:169], v[190:193], v[10:13]
	v_mfma_f32_16x16x32_bf16 v[6:9], v[158:161], v[198:201], v[6:9]
	v_mfma_f32_16x16x32_bf16 v[2:5], v[166:169], v[198:201], v[2:5]
	s_barrier
	v_add_u32_e32 v141, 0x18000, v139
	ds_read_b128 v[130:133], v141
	ds_read_b128 v[142:145], v141 offset:1024
	ds_read_b128 v[146:149], v141 offset:2048
	ds_read_b128 v[150:153], v141 offset:3072
	v_add_u32_e32 v141, 0x1c000, v139
	ds_read_b128 v[154:157], v141
	ds_read_b128 v[158:161], v141 offset:1024
	ds_read_b128 v[162:165], v141 offset:2048
	ds_read_b128 v[166:169], v141 offset:3072
	ds_read_b128 v[170:173], v140 offset:32768
	ds_read_b128 v[174:177], v140 offset:33792
	ds_read_b128 v[178:181], v140 offset:34816
	ds_read_b128 v[182:185], v140 offset:35840
	ds_read_b128 v[186:189], v140 offset:36864
	ds_read_b128 v[190:193], v140 offset:37888
	ds_read_b128 v[194:197], v140 offset:38912
	ds_read_b128 v[198:201], v140 offset:39936
	s_add_u32 s22, s28, 0x160000
	s_addc_u32 s23, s29, 0
	s_mov_b32 s28, m0
	s_mov_b32 m0, s43
	s_nop 3
	global_load_lds_dwordx4 v0, s[22:23]
	s_mov_b32 m0, s28
	s_nop 0
	s_mov_b32 s28, m0
	s_mov_b32 m0, s44
	s_nop 3
	global_load_lds_dwordx4 v135, s[22:23]
	s_mov_b32 m0, s28
	s_waitcnt vmcnt(8)
	s_waitcnt lgkmcnt(0)
	s_barrier
	s_waitcnt lgkmcnt(7)
	v_mfma_f32_16x16x32_bf16 v[126:129], v[130:133], v[170:173], v[126:129]
	v_mfma_f32_16x16x32_bf16 v[122:125], v[146:149], v[170:173], v[122:125]
	s_waitcnt lgkmcnt(5)
	v_mfma_f32_16x16x32_bf16 v[118:121], v[130:133], v[178:181], v[118:121]
	v_mfma_f32_16x16x32_bf16 v[110:113], v[146:149], v[178:181], v[110:113]
	s_waitcnt lgkmcnt(3)
	v_mfma_f32_16x16x32_bf16 v[102:105], v[130:133], v[186:189], v[102:105]
	v_mfma_f32_16x16x32_bf16 v[94:97], v[146:149], v[186:189], v[94:97]
	s_waitcnt lgkmcnt(1)
	v_mfma_f32_16x16x32_bf16 v[86:89], v[130:133], v[194:197], v[86:89]
	v_mfma_f32_16x16x32_bf16 v[78:81], v[146:149], v[194:197], v[78:81]
	v_mfma_f32_16x16x32_bf16 v[126:129], v[142:145], v[174:177], v[126:129]
	v_mfma_f32_16x16x32_bf16 v[122:125], v[150:153], v[174:177], v[122:125]
	v_mfma_f32_16x16x32_bf16 v[118:121], v[142:145], v[182:185], v[118:121]
	v_mfma_f32_16x16x32_bf16 v[110:113], v[150:153], v[182:185], v[110:113]
	v_mfma_f32_16x16x32_bf16 v[102:105], v[142:145], v[190:193], v[102:105]
	v_mfma_f32_16x16x32_bf16 v[94:97], v[150:153], v[190:193], v[94:97]
	s_waitcnt lgkmcnt(0)
	v_mfma_f32_16x16x32_bf16 v[86:89], v[142:145], v[198:201], v[86:89]
	v_mfma_f32_16x16x32_bf16 v[78:81], v[150:153], v[198:201], v[78:81]
	v_mfma_f32_16x16x32_bf16 v[114:117], v[154:157], v[170:173], v[114:117]
	v_mfma_f32_16x16x32_bf16 v[106:109], v[162:165], v[170:173], v[106:109]
	v_mfma_f32_16x16x32_bf16 v[98:101], v[154:157], v[178:181], v[98:101]
	v_mfma_f32_16x16x32_bf16 v[90:93], v[162:165], v[178:181], v[90:93]
	v_mfma_f32_16x16x32_bf16 v[82:85], v[154:157], v[186:189], v[82:85]
	v_mfma_f32_16x16x32_bf16 v[74:77], v[162:165], v[186:189], v[74:77]
	v_mfma_f32_16x16x32_bf16 v[70:73], v[154:157], v[194:197], v[70:73]
	v_mfma_f32_16x16x32_bf16 v[66:69], v[162:165], v[194:197], v[66:69]
	v_mfma_f32_16x16x32_bf16 v[114:117], v[158:161], v[174:177], v[114:117]
	v_mfma_f32_16x16x32_bf16 v[106:109], v[166:169], v[174:177], v[106:109]
	v_mfma_f32_16x16x32_bf16 v[98:101], v[158:161], v[182:185], v[98:101]
	v_mfma_f32_16x16x32_bf16 v[90:93], v[166:169], v[182:185], v[90:93]
	v_mfma_f32_16x16x32_bf16 v[82:85], v[158:161], v[190:193], v[82:85]
	v_mfma_f32_16x16x32_bf16 v[74:77], v[166:169], v[190:193], v[74:77]
	v_mfma_f32_16x16x32_bf16 v[70:73], v[158:161], v[198:201], v[70:73]
	v_mfma_f32_16x16x32_bf16 v[66:69], v[166:169], v[198:201], v[66:69]
	s_barrier
	ds_read_b128 v[170:173], v140 offset:49152
	ds_read_b128 v[174:177], v140 offset:50176
	ds_read_b128 v[178:181], v140 offset:51200
	ds_read_b128 v[182:185], v140 offset:52224
	ds_read_b128 v[186:189], v140 offset:53248
	ds_read_b128 v[190:193], v140 offset:54272
	ds_read_b128 v[194:197], v140 offset:55296
	ds_read_b128 v[198:201], v140 offset:56320
	s_add_u32 s22, s26, 0x80
	s_addc_u32 s23, s27, 0
	s_mov_b32 s28, m0
	s_mov_b32 m0, s45
	s_nop 3
	global_load_lds_dwordx4 v134, s[22:23]
	s_mov_b32 m0, s28
	s_nop 0
	s_mov_b32 s28, m0
	s_mov_b32 m0, s47
	s_nop 3
	global_load_lds_dwordx4 v136, s[22:23]
	s_mov_b32 m0, s28
	s_add_u32 s22, s26, 0x40080
	s_addc_u32 s23, s27, 0
	s_mov_b32 s26, m0
	s_mov_b32 m0, s50
	s_nop 3
	global_load_lds_dwordx4 v134, s[22:23]
	s_mov_b32 m0, s26
	s_nop 0
	s_mov_b32 s26, m0
	s_mov_b32 m0, s51
	s_nop 3
	global_load_lds_dwordx4 v136, s[22:23]
	s_mov_b32 m0, s26
	s_mov_b32 s22, m0
	s_mov_b32 m0, s48
	s_nop 3
	global_load_lds_dwordx4 v0, s[24:25]
	s_mov_b32 m0, s22
	s_nop 0
	s_mov_b32 s22, m0
	s_mov_b32 m0, s49
	s_nop 3
	global_load_lds_dwordx4 v135, s[24:25]
	s_mov_b32 m0, s22
	s_waitcnt vmcnt(8)
	s_waitcnt lgkmcnt(0)
	s_barrier
	s_waitcnt lgkmcnt(7)
	v_mfma_f32_16x16x32_bf16 v[62:65], v[130:133], v[170:173], v[62:65]
	v_mfma_f32_16x16x32_bf16 v[58:61], v[146:149], v[170:173], v[58:61]
	s_waitcnt lgkmcnt(5)
	v_mfma_f32_16x16x32_bf16 v[54:57], v[130:133], v[178:181], v[54:57]
	v_mfma_f32_16x16x32_bf16 v[46:49], v[146:149], v[178:181], v[46:49]
	s_waitcnt lgkmcnt(3)
	v_mfma_f32_16x16x32_bf16 v[38:41], v[130:133], v[186:189], v[38:41]
	v_mfma_f32_16x16x32_bf16 v[30:33], v[146:149], v[186:189], v[30:33]
	s_waitcnt lgkmcnt(1)
	v_mfma_f32_16x16x32_bf16 v[22:25], v[130:133], v[194:197], v[22:25]
	v_mfma_f32_16x16x32_bf16 v[14:17], v[146:149], v[194:197], v[14:17]
	v_mfma_f32_16x16x32_bf16 v[62:65], v[142:145], v[174:177], v[62:65]
	v_mfma_f32_16x16x32_bf16 v[58:61], v[150:153], v[174:177], v[58:61]
	v_mfma_f32_16x16x32_bf16 v[54:57], v[142:145], v[182:185], v[54:57]
	v_mfma_f32_16x16x32_bf16 v[46:49], v[150:153], v[182:185], v[46:49]
	v_mfma_f32_16x16x32_bf16 v[38:41], v[142:145], v[190:193], v[38:41]
	v_mfma_f32_16x16x32_bf16 v[30:33], v[150:153], v[190:193], v[30:33]
	s_waitcnt lgkmcnt(0)
	v_mfma_f32_16x16x32_bf16 v[22:25], v[142:145], v[198:201], v[22:25]
	v_mfma_f32_16x16x32_bf16 v[14:17], v[150:153], v[198:201], v[14:17]
	v_mfma_f32_16x16x32_bf16 v[50:53], v[154:157], v[170:173], v[50:53]
	v_mfma_f32_16x16x32_bf16 v[42:45], v[162:165], v[170:173], v[42:45]
	v_mfma_f32_16x16x32_bf16 v[34:37], v[154:157], v[178:181], v[34:37]
	v_mfma_f32_16x16x32_bf16 v[26:29], v[162:165], v[178:181], v[26:29]
	v_mfma_f32_16x16x32_bf16 v[18:21], v[154:157], v[186:189], v[18:21]
	v_mfma_f32_16x16x32_bf16 v[10:13], v[162:165], v[186:189], v[10:13]
	v_mfma_f32_16x16x32_bf16 v[6:9], v[154:157], v[194:197], v[6:9]
	v_mfma_f32_16x16x32_bf16 v[2:5], v[162:165], v[194:197], v[2:5]
	v_mfma_f32_16x16x32_bf16 v[50:53], v[158:161], v[174:177], v[50:53]
	v_mfma_f32_16x16x32_bf16 v[42:45], v[166:169], v[174:177], v[42:45]
	v_mfma_f32_16x16x32_bf16 v[34:37], v[158:161], v[182:185], v[34:37]
	v_mfma_f32_16x16x32_bf16 v[26:29], v[166:169], v[182:185], v[26:29]
	v_mfma_f32_16x16x32_bf16 v[18:21], v[158:161], v[190:193], v[18:21]
	v_mfma_f32_16x16x32_bf16 v[10:13], v[166:169], v[190:193], v[10:13]
	v_mfma_f32_16x16x32_bf16 v[6:9], v[158:161], v[198:201], v[6:9]
	v_mfma_f32_16x16x32_bf16 v[2:5], v[166:169], v[198:201], v[2:5]
	s_barrier
	s_add_i32 s59, s59, 2
	s_add_u32 s57, s57, 0x100
	s_addc_u32 s58, s58, 0
	s_cmp_gt_u32 s59, 13
	s_mov_b64 s[22:23], s[4:5]
	s_cbranch_scc0 .LBB0_694
	s_and_b64 vcc, exec, s[10:11]
	v_readlane_b32 s56, v253, 57
	v_readlane_b32 s57, v253, 58
	s_cbranch_vccz .LBB0_697
	s_barrier
.LBB0_697:
	s_setprio 0
	s_lshl_b32 s4, s20, 8
	v_or_b32_e32 v130, s4, v138
	s_bfe_i32 s4, s20, 0x10017
	s_lshr_b32 s4, s4, 22
	v_add_u32_e32 v131, s4, v130
	v_and_b32_e32 v131, 0xfffffc00, v131
	v_sub_u32_e32 v132, v130, v131
	v_lshl_add_u32 v141, s55, 8, v137
	v_ashrrev_i32_e32 v133, 31, v132
	v_mov_b64_e32 v[130:131], s[8:9]
	v_mad_i64_i32 v[142:143], s[4:5], v141, s66, v[130:131]
	v_lshlrev_b64 v[132:133], 1, v[132:133]
	v_pk_add_f32 v[128:129], v[128:129], 0 op_sel_hi:[1,0]
	v_pk_add_f32 v[126:127], v[126:127], 0 op_sel_hi:[1,0]
	v_pk_add_f32 v[144:145], v[124:125], 0 op_sel_hi:[1,0]
	v_pk_add_f32 v[124:125], v[122:123], 0 op_sel_hi:[1,0]
	v_lshl_add_u64 v[142:143], v[142:143], 0, v[132:133]
	v_cvt_pk_bf16_f32 v122, v126, v127
	v_cvt_pk_bf16_f32 v123, v128, v129
	v_cvt_pk_bf16_f32 v124, v124, v125
	v_cvt_pk_bf16_f32 v125, v144, v145
	global_store_dwordx4 v[142:143], v[122:125], off
	v_pk_add_f32 v[116:117], v[116:117], 0 op_sel_hi:[1,0]
	v_pk_add_f32 v[114:115], v[114:115], 0 op_sel_hi:[1,0]
	v_pk_add_f32 v[122:123], v[108:109], 0 op_sel_hi:[1,0]
	v_pk_add_f32 v[108:109], v[106:107], 0 op_sel_hi:[1,0]
	v_cvt_pk_bf16_f32 v106, v114, v115
	v_cvt_pk_bf16_f32 v107, v116, v117
	v_cvt_pk_bf16_f32 v108, v108, v109
	v_cvt_pk_bf16_f32 v109, v122, v123
	global_store_dwordx4 v[142:143], v[106:109], off offset:256
	v_pk_add_f32 v[112:113], v[112:113], 0 op_sel_hi:[1,0]
	v_pk_add_f32 v[110:111], v[110:111], 0 op_sel_hi:[1,0]
	v_or_b32_e32 v106, 16, v141
	v_mad_i64_i32 v[106:107], s[4:5], v106, s66, v[130:131]
	v_lshl_add_u64 v[114:115], v[106:107], 0, v[132:133]
	v_pk_add_f32 v[108:109], v[120:121], 0 op_sel_hi:[1,0]
	v_pk_add_f32 v[106:107], v[118:119], 0 op_sel_hi:[1,0]
	v_pk_add_f32 v[100:101], v[100:101], 0 op_sel_hi:[1,0]
	v_cvt_pk_bf16_f32 v106, v106, v107
	v_cvt_pk_bf16_f32 v107, v108, v109
	v_cvt_pk_bf16_f32 v108, v110, v111
	v_cvt_pk_bf16_f32 v109, v112, v113
	global_store_dwordx4 v[114:115], v[106:109], off
	v_pk_add_f32 v[98:99], v[98:99], 0 op_sel_hi:[1,0]
	v_pk_add_f32 v[96:97], v[96:97], 0 op_sel_hi:[1,0]
	v_pk_add_f32 v[106:107], v[92:93], 0 op_sel_hi:[1,0]
	v_pk_add_f32 v[92:93], v[90:91], 0 op_sel_hi:[1,0]
	v_cvt_pk_bf16_f32 v90, v98, v99
	v_cvt_pk_bf16_f32 v91, v100, v101
	v_cvt_pk_bf16_f32 v92, v92, v93
	v_cvt_pk_bf16_f32 v93, v106, v107
	global_store_dwordx4 v[114:115], v[90:93], off offset:256
	v_pk_add_f32 v[94:95], v[94:95], 0 op_sel_hi:[1,0]
	v_pk_add_f32 v[84:85], v[84:85], 0 op_sel_hi:[1,0]
	v_or_b32_e32 v90, 32, v141
	v_mad_i64_i32 v[90:91], s[4:5], v90, s66, v[130:131]
	v_lshl_add_u64 v[98:99], v[90:91], 0, v[132:133]
	v_pk_add_f32 v[92:93], v[104:105], 0 op_sel_hi:[1,0]
	v_pk_add_f32 v[90:91], v[102:103], 0 op_sel_hi:[1,0]
	v_pk_add_f32 v[82:83], v[82:83], 0 op_sel_hi:[1,0]
	v_cvt_pk_bf16_f32 v90, v90, v91
	v_cvt_pk_bf16_f32 v91, v92, v93
	v_cvt_pk_bf16_f32 v92, v94, v95
	v_cvt_pk_bf16_f32 v93, v96, v97
	global_store_dwordx4 v[98:99], v[90:93], off
	v_pk_add_f32 v[80:81], v[80:81], 0 op_sel_hi:[1,0]
	v_pk_add_f32 v[78:79], v[78:79], 0 op_sel_hi:[1,0]
	v_pk_add_f32 v[90:91], v[76:77], 0 op_sel_hi:[1,0]
	v_pk_add_f32 v[76:77], v[74:75], 0 op_sel_hi:[1,0]
	v_cvt_pk_bf16_f32 v74, v82, v83
	v_cvt_pk_bf16_f32 v75, v84, v85
	v_cvt_pk_bf16_f32 v76, v76, v77
	v_cvt_pk_bf16_f32 v77, v90, v91
	global_store_dwordx4 v[98:99], v[74:77], off offset:256
	v_pk_add_f32 v[72:73], v[72:73], 0 op_sel_hi:[1,0]
	v_pk_add_f32 v[70:71], v[70:71], 0 op_sel_hi:[1,0]
	v_or_b32_e32 v74, 48, v141
	v_mad_i64_i32 v[74:75], s[4:5], v74, s66, v[130:131]
	v_lshl_add_u64 v[82:83], v[74:75], 0, v[132:133]
	v_pk_add_f32 v[76:77], v[88:89], 0 op_sel_hi:[1,0]
	v_pk_add_f32 v[74:75], v[86:87], 0 op_sel_hi:[1,0]
	v_pk_add_f32 v[64:65], v[64:65], 0 op_sel_hi:[1,0]
	v_cvt_pk_bf16_f32 v74, v74, v75
	v_cvt_pk_bf16_f32 v75, v76, v77
	v_cvt_pk_bf16_f32 v76, v78, v79
	v_cvt_pk_bf16_f32 v77, v80, v81
	global_store_dwordx4 v[82:83], v[74:77], off
	v_pk_add_f32 v[62:63], v[62:63], 0 op_sel_hi:[1,0]
	v_pk_add_f32 v[52:53], v[52:53], 0 op_sel_hi:[1,0]
	v_pk_add_f32 v[74:75], v[68:69], 0 op_sel_hi:[1,0]
	v_pk_add_f32 v[68:69], v[66:67], 0 op_sel_hi:[1,0]
	v_cvt_pk_bf16_f32 v66, v70, v71
	v_cvt_pk_bf16_f32 v67, v72, v73
	v_cvt_pk_bf16_f32 v68, v68, v69
	v_cvt_pk_bf16_f32 v69, v74, v75
	global_store_dwordx4 v[82:83], v[66:69], off offset:256
	v_pk_add_f32 v[50:51], v[50:51], 0 op_sel_hi:[1,0]
	v_pk_add_f32 v[48:49], v[48:49], 0 op_sel_hi:[1,0]
	v_add_u32_e32 v66, 0x80, v141
	v_mad_i64_i32 v[66:67], s[4:5], v66, s66, v[130:131]
	v_pk_add_f32 v[68:69], v[60:61], 0 op_sel_hi:[1,0]
	v_pk_add_f32 v[60:61], v[58:59], 0 op_sel_hi:[1,0]
	v_lshl_add_u64 v[66:67], v[66:67], 0, v[132:133]
	v_cvt_pk_bf16_f32 v58, v62, v63
	v_cvt_pk_bf16_f32 v59, v64, v65
	v_cvt_pk_bf16_f32 v60, v60, v61
	v_cvt_pk_bf16_f32 v61, v68, v69
	global_store_dwordx4 v[66:67], v[58:61], off
	v_pk_add_f32 v[46:47], v[46:47], 0 op_sel_hi:[1,0]
	v_pk_add_f32 v[36:37], v[36:37], 0 op_sel_hi:[1,0]
	v_pk_add_f32 v[58:59], v[44:45], 0 op_sel_hi:[1,0]
	v_pk_add_f32 v[44:45], v[42:43], 0 op_sel_hi:[1,0]
	v_cvt_pk_bf16_f32 v42, v50, v51
	v_cvt_pk_bf16_f32 v43, v52, v53
	v_cvt_pk_bf16_f32 v44, v44, v45
	v_cvt_pk_bf16_f32 v45, v58, v59
	global_store_dwordx4 v[66:67], v[42:45], off offset:256
	v_pk_add_f32 v[34:35], v[34:35], 0 op_sel_hi:[1,0]
	v_pk_add_f32 v[32:33], v[32:33], 0 op_sel_hi:[1,0]
	v_add_u32_e32 v42, 0x90, v141
	v_mad_i64_i32 v[42:43], s[4:5], v42, s66, v[130:131]
	v_lshl_add_u64 v[50:51], v[42:43], 0, v[132:133]
	v_pk_add_f32 v[44:45], v[56:57], 0 op_sel_hi:[1,0]
	v_pk_add_f32 v[42:43], v[54:55], 0 op_sel_hi:[1,0]
	v_pk_add_f32 v[30:31], v[30:31], 0 op_sel_hi:[1,0]
	v_cvt_pk_bf16_f32 v42, v42, v43
	v_cvt_pk_bf16_f32 v43, v44, v45
	v_cvt_pk_bf16_f32 v44, v46, v47
	v_cvt_pk_bf16_f32 v45, v48, v49
	global_store_dwordx4 v[50:51], v[42:45], off
	v_pk_add_f32 v[20:21], v[20:21], 0 op_sel_hi:[1,0]
	v_pk_add_f32 v[18:19], v[18:19], 0 op_sel_hi:[1,0]
	v_pk_add_f32 v[42:43], v[28:29], 0 op_sel_hi:[1,0]
	v_pk_add_f32 v[28:29], v[26:27], 0 op_sel_hi:[1,0]
	v_cvt_pk_bf16_f32 v26, v34, v35
	v_cvt_pk_bf16_f32 v27, v36, v37
	v_cvt_pk_bf16_f32 v28, v28, v29
	v_cvt_pk_bf16_f32 v29, v42, v43
	global_store_dwordx4 v[50:51], v[26:29], off offset:256
	v_pk_add_f32 v[16:17], v[16:17], 0 op_sel_hi:[1,0]
	v_pk_add_f32 v[14:15], v[14:15], 0 op_sel_hi:[1,0]
	v_add_u32_e32 v26, 0xa0, v141
	v_mad_i64_i32 v[26:27], s[4:5], v26, s66, v[130:131]
	v_lshl_add_u64 v[34:35], v[26:27], 0, v[132:133]
	v_pk_add_f32 v[28:29], v[40:41], 0 op_sel_hi:[1,0]
	v_pk_add_f32 v[26:27], v[38:39], 0 op_sel_hi:[1,0]
	v_pk_add_f32 v[8:9], v[8:9], 0 op_sel_hi:[1,0]
	v_cvt_pk_bf16_f32 v26, v26, v27
	v_cvt_pk_bf16_f32 v27, v28, v29
	v_cvt_pk_bf16_f32 v28, v30, v31
	v_cvt_pk_bf16_f32 v29, v32, v33
	global_store_dwordx4 v[34:35], v[26:29], off
	v_pk_add_f32 v[6:7], v[6:7], 0 op_sel_hi:[1,0]
	s_and_b64 vcc, exec, s[0:1]
	v_pk_add_f32 v[26:27], v[12:13], 0 op_sel_hi:[1,0]
	v_pk_add_f32 v[12:13], v[10:11], 0 op_sel_hi:[1,0]
	v_cvt_pk_bf16_f32 v10, v18, v19
	v_cvt_pk_bf16_f32 v11, v20, v21
	v_cvt_pk_bf16_f32 v12, v12, v13
	v_cvt_pk_bf16_f32 v13, v26, v27
	global_store_dwordx4 v[34:35], v[10:13], off offset:256
	s_mov_b64 s[0:1], -1
	s_nop 0
	v_add_u32_e32 v10, 0xb0, v141
	v_mad_i64_i32 v[10:11], s[4:5], v10, s66, v[130:131]
	v_lshl_add_u64 v[18:19], v[10:11], 0, v[132:133]
	v_pk_add_f32 v[12:13], v[24:25], 0 op_sel_hi:[1,0]
	v_pk_add_f32 v[10:11], v[22:23], 0 op_sel_hi:[1,0]
	s_nop 0
	v_cvt_pk_bf16_f32 v10, v10, v11
	v_cvt_pk_bf16_f32 v11, v12, v13
	v_cvt_pk_bf16_f32 v12, v14, v15
	v_cvt_pk_bf16_f32 v13, v16, v17
	global_store_dwordx4 v[18:19], v[10:13], off
	s_nop 1
	v_pk_add_f32 v[10:11], v[4:5], 0 op_sel_hi:[1,0]
	v_pk_add_f32 v[4:5], v[2:3], 0 op_sel_hi:[1,0]
	v_cvt_pk_bf16_f32 v2, v6, v7
	v_cvt_pk_bf16_f32 v3, v8, v9
	v_cvt_pk_bf16_f32 v4, v4, v5
	v_cvt_pk_bf16_f32 v5, v10, v11
	global_store_dwordx4 v[18:19], v[2:5], off offset:256
	s_cbranch_vccnz .LBB0_688
	s_andn2_b64 vcc, exec, s[6:7]
	s_cbranch_vccnz .LBB0_687
	s_barrier
	s_branch .LBB0_687

.Lprio_712:
	v_add_u32_e32 v141, 0x10000, v139
	ds_read_b128 v[130:133], v141
	ds_read_b128 v[142:145], v141 offset:1024
	ds_read_b128 v[146:149], v141 offset:2048
	ds_read_b128 v[150:153], v141 offset:3072
	v_add_u32_e32 v141, 0x14000, v139
	ds_read_b128 v[154:157], v141
	ds_read_b128 v[158:161], v141 offset:1024
	ds_read_b128 v[162:165], v141 offset:2048
	ds_read_b128 v[166:169], v141 offset:3072
	s_add_u32 s4, s22, 0x100
	s_addc_u32 s5, s23, 0
	s_cmp_eq_u32 s60, 12
	s_cselect_b32 s28, s16, s4
	s_cselect_b32 s29, s17, s5
	s_cselect_b32 s26, s57, s58
	s_cselect_b32 s27, s13, s59
	s_add_u32 s24, s28, 0x80
	s_addc_u32 s25, s29, 0
	ds_read_b128 v[170:173], v140
	ds_read_b128 v[174:177], v140 offset:1024
	ds_read_b128 v[178:181], v140 offset:2048
	ds_read_b128 v[182:185], v140 offset:3072
	ds_read_b128 v[186:189], v140 offset:4096
	ds_read_b128 v[190:193], v140 offset:5120
	ds_read_b128 v[194:197], v140 offset:6144
	ds_read_b128 v[198:201], v140 offset:7168
	s_add_u32 s22, s22, 0x160080
	s_addc_u32 s23, s23, 0
	s_mov_b32 s61, m0
	s_mov_b32 m0, s53
	s_nop 3
	global_load_lds_dwordx4 v0, s[22:23]
	s_mov_b32 m0, s61
	s_add_i32 s61, s21, 0xe000
	s_mov_b32 s62, m0
	s_mov_b32 m0, s61
	s_nop 3
	global_load_lds_dwordx4 v135, s[22:23]
	s_mov_b32 m0, s62
	s_waitcnt vmcnt(8)
	s_waitcnt lgkmcnt(0)
	s_barrier
	s_waitcnt lgkmcnt(7)
	v_mfma_f32_16x16x32_bf16 v[126:129], v[130:133], v[170:173], v[126:129]
	v_mfma_f32_16x16x32_bf16 v[122:125], v[146:149], v[170:173], v[122:125]
	s_waitcnt lgkmcnt(5)
	v_mfma_f32_16x16x32_bf16 v[118:121], v[130:133], v[178:181], v[118:121]
	v_mfma_f32_16x16x32_bf16 v[110:113], v[146:149], v[178:181], v[110:113]
	s_waitcnt lgkmcnt(3)
	v_mfma_f32_16x16x32_bf16 v[102:105], v[130:133], v[186:189], v[102:105]
	v_mfma_f32_16x16x32_bf16 v[94:97], v[146:149], v[186:189], v[94:97]
	s_waitcnt lgkmcnt(1)
	v_mfma_f32_16x16x32_bf16 v[86:89], v[130:133], v[194:197], v[86:89]
	v_mfma_f32_16x16x32_bf16 v[78:81], v[146:149], v[194:197], v[78:81]
	v_mfma_f32_16x16x32_bf16 v[126:129], v[142:145], v[174:177], v[126:129]
	v_mfma_f32_16x16x32_bf16 v[122:125], v[150:153], v[174:177], v[122:125]
	v_mfma_f32_16x16x32_bf16 v[118:121], v[142:145], v[182:185], v[118:121]
	v_mfma_f32_16x16x32_bf16 v[110:113], v[150:153], v[182:185], v[110:113]
	v_mfma_f32_16x16x32_bf16 v[102:105], v[142:145], v[190:193], v[102:105]
	v_mfma_f32_16x16x32_bf16 v[94:97], v[150:153], v[190:193], v[94:97]
	s_waitcnt lgkmcnt(0)
	v_mfma_f32_16x16x32_bf16 v[86:89], v[142:145], v[198:201], v[86:89]
	v_mfma_f32_16x16x32_bf16 v[78:81], v[150:153], v[198:201], v[78:81]
	v_mfma_f32_16x16x32_bf16 v[114:117], v[154:157], v[170:173], v[114:117]
	v_mfma_f32_16x16x32_bf16 v[106:109], v[162:165], v[170:173], v[106:109]
	v_mfma_f32_16x16x32_bf16 v[98:101], v[154:157], v[178:181], v[98:101]
	v_mfma_f32_16x16x32_bf16 v[90:93], v[162:165], v[178:181], v[90:93]
	v_mfma_f32_16x16x32_bf16 v[82:85], v[154:157], v[186:189], v[82:85]
	v_mfma_f32_16x16x32_bf16 v[74:77], v[162:165], v[186:189], v[74:77]
	v_mfma_f32_16x16x32_bf16 v[70:73], v[154:157], v[194:197], v[70:73]
	v_mfma_f32_16x16x32_bf16 v[66:69], v[162:165], v[194:197], v[66:69]
	v_mfma_f32_16x16x32_bf16 v[114:117], v[158:161], v[174:177], v[114:117]
	v_mfma_f32_16x16x32_bf16 v[106:109], v[166:169], v[174:177], v[106:109]
	v_mfma_f32_16x16x32_bf16 v[98:101], v[158:161], v[182:185], v[98:101]
	v_mfma_f32_16x16x32_bf16 v[90:93], v[166:169], v[182:185], v[90:93]
	v_mfma_f32_16x16x32_bf16 v[82:85], v[158:161], v[190:193], v[82:85]
	v_mfma_f32_16x16x32_bf16 v[74:77], v[166:169], v[190:193], v[74:77]
	v_mfma_f32_16x16x32_bf16 v[70:73], v[158:161], v[198:201], v[70:73]
	v_mfma_f32_16x16x32_bf16 v[66:69], v[166:169], v[198:201], v[66:69]
	s_barrier
	ds_read_b128 v[170:173], v140 offset:16384
	ds_read_b128 v[174:177], v140 offset:17408
	ds_read_b128 v[178:181], v140 offset:18432
	ds_read_b128 v[182:185], v140 offset:19456
	ds_read_b128 v[186:189], v140 offset:20480
	ds_read_b128 v[190:193], v140 offset:21504
	ds_read_b128 v[194:197], v140 offset:22528
	ds_read_b128 v[198:201], v140 offset:23552
	s_mov_b32 s22, m0
	s_mov_b32 m0, s39
	s_nop 3
	global_load_lds_dwordx4 v134, s[26:27]
	s_mov_b32 m0, s22
	s_nop 0
	s_mov_b32 s22, m0
	s_mov_b32 m0, s40
	s_nop 3
	global_load_lds_dwordx4 v136, s[26:27]
	s_mov_b32 m0, s22
	s_add_u32 s22, s26, 0x40000
	s_addc_u32 s23, s27, 0
	s_mov_b32 s61, m0
	s_mov_b32 m0, s41
	s_nop 3
	global_load_lds_dwordx4 v134, s[22:23]
	s_mov_b32 m0, s61
	s_nop 0
	s_mov_b32 s61, m0
	s_mov_b32 m0, s42
	s_nop 3
	global_load_lds_dwordx4 v136, s[22:23]
	s_mov_b32 m0, s61
	s_mov_b32 s22, m0
	s_mov_b32 m0, s21
	s_nop 3
	global_load_lds_dwordx4 v0, s[28:29]
	s_mov_b32 m0, s22
	s_nop 0
	s_mov_b32 s22, m0
	s_mov_b32 m0, s43
	s_nop 3
	global_load_lds_dwordx4 v135, s[28:29]
	s_mov_b32 m0, s22
	s_waitcnt vmcnt(8)
	s_waitcnt lgkmcnt(0)
	s_barrier
	s_waitcnt lgkmcnt(7)
	v_mfma_f32_16x16x32_bf16 v[62:65], v[130:133], v[170:173], v[62:65]
	v_mfma_f32_16x16x32_bf16 v[58:61], v[146:149], v[170:173], v[58:61]
	s_waitcnt lgkmcnt(5)
	v_mfma_f32_16x16x32_bf16 v[54:57], v[130:133], v[178:181], v[54:57]
	v_mfma_f32_16x16x32_bf16 v[46:49], v[146:149], v[178:181], v[46:49]
	s_waitcnt lgkmcnt(3)
	v_mfma_f32_16x16x32_bf16 v[38:41], v[130:133], v[186:189], v[38:41]
	v_mfma_f32_16x16x32_bf16 v[30:33], v[146:149], v[186:189], v[30:33]
	s_waitcnt lgkmcnt(1)
	v_mfma_f32_16x16x32_bf16 v[22:25], v[130:133], v[194:197], v[22:25]
	v_mfma_f32_16x16x32_bf16 v[14:17], v[146:149], v[194:197], v[14:17]
	v_mfma_f32_16x16x32_bf16 v[62:65], v[142:145], v[174:177], v[62:65]
	v_mfma_f32_16x16x32_bf16 v[58:61], v[150:153], v[174:177], v[58:61]
	v_mfma_f32_16x16x32_bf16 v[54:57], v[142:145], v[182:185], v[54:57]
	v_mfma_f32_16x16x32_bf16 v[46:49], v[150:153], v[182:185], v[46:49]
	v_mfma_f32_16x16x32_bf16 v[38:41], v[142:145], v[190:193], v[38:41]
	v_mfma_f32_16x16x32_bf16 v[30:33], v[150:153], v[190:193], v[30:33]
	s_waitcnt lgkmcnt(0)
	v_mfma_f32_16x16x32_bf16 v[22:25], v[142:145], v[198:201], v[22:25]
	v_mfma_f32_16x16x32_bf16 v[14:17], v[150:153], v[198:201], v[14:17]
	v_mfma_f32_16x16x32_bf16 v[50:53], v[154:157], v[170:173], v[50:53]
	v_mfma_f32_16x16x32_bf16 v[42:45], v[162:165], v[170:173], v[42:45]
	v_mfma_f32_16x16x32_bf16 v[34:37], v[154:157], v[178:181], v[34:37]
	v_mfma_f32_16x16x32_bf16 v[26:29], v[162:165], v[178:181], v[26:29]
	v_mfma_f32_16x16x32_bf16 v[18:21], v[154:157], v[186:189], v[18:21]
	v_mfma_f32_16x16x32_bf16 v[10:13], v[162:165], v[186:189], v[10:13]
	v_mfma_f32_16x16x32_bf16 v[6:9], v[154:157], v[194:197], v[6:9]
	v_mfma_f32_16x16x32_bf16 v[2:5], v[162:165], v[194:197], v[2:5]
	v_mfma_f32_16x16x32_bf16 v[50:53], v[158:161], v[174:177], v[50:53]
	v_mfma_f32_16x16x32_bf16 v[42:45], v[166:169], v[174:177], v[42:45]
	v_mfma_f32_16x16x32_bf16 v[34:37], v[158:161], v[182:185], v[34:37]
	v_mfma_f32_16x16x32_bf16 v[26:29], v[166:169], v[182:185], v[26:29]
	v_mfma_f32_16x16x32_bf16 v[18:21], v[158:161], v[190:193], v[18:21]
	v_mfma_f32_16x16x32_bf16 v[10:13], v[166:169], v[190:193], v[10:13]
	v_mfma_f32_16x16x32_bf16 v[6:9], v[158:161], v[198:201], v[6:9]
	v_mfma_f32_16x16x32_bf16 v[2:5], v[166:169], v[198:201], v[2:5]
	s_barrier
	v_add_u32_e32 v141, 0x18000, v139
	ds_read_b128 v[130:133], v141
	ds_read_b128 v[142:145], v141 offset:1024
	ds_read_b128 v[146:149], v141 offset:2048
	ds_read_b128 v[150:153], v141 offset:3072
	v_add_u32_e32 v141, 0x1c000, v139
	ds_read_b128 v[154:157], v141
	ds_read_b128 v[158:161], v141 offset:1024
	ds_read_b128 v[162:165], v141 offset:2048
	ds_read_b128 v[166:169], v141 offset:3072
	ds_read_b128 v[170:173], v140 offset:32768
	ds_read_b128 v[174:177], v140 offset:33792
	ds_read_b128 v[178:181], v140 offset:34816
	ds_read_b128 v[182:185], v140 offset:35840
	ds_read_b128 v[186:189], v140 offset:36864
	ds_read_b128 v[190:193], v140 offset:37888
	ds_read_b128 v[194:197], v140 offset:38912
	ds_read_b128 v[198:201], v140 offset:39936
	s_add_u32 s22, s28, 0x160000
	s_addc_u32 s23, s29, 0
	s_mov_b32 s28, m0
	s_mov_b32 m0, s44
	s_nop 3
	global_load_lds_dwordx4 v0, s[22:23]
	s_mov_b32 m0, s28
	s_nop 0
	s_mov_b32 s28, m0
	s_mov_b32 m0, s45
	s_nop 3
	global_load_lds_dwordx4 v135, s[22:23]
	s_mov_b32 m0, s28
	s_waitcnt vmcnt(8)
	s_waitcnt lgkmcnt(0)
	s_barrier
	s_waitcnt lgkmcnt(7)
	v_mfma_f32_16x16x32_bf16 v[126:129], v[130:133], v[170:173], v[126:129]
	v_mfma_f32_16x16x32_bf16 v[122:125], v[146:149], v[170:173], v[122:125]
	s_waitcnt lgkmcnt(5)
	v_mfma_f32_16x16x32_bf16 v[118:121], v[130:133], v[178:181], v[118:121]
	v_mfma_f32_16x16x32_bf16 v[110:113], v[146:149], v[178:181], v[110:113]
	s_waitcnt lgkmcnt(3)
	v_mfma_f32_16x16x32_bf16 v[102:105], v[130:133], v[186:189], v[102:105]
	v_mfma_f32_16x16x32_bf16 v[94:97], v[146:149], v[186:189], v[94:97]
	s_waitcnt lgkmcnt(1)
	v_mfma_f32_16x16x32_bf16 v[86:89], v[130:133], v[194:197], v[86:89]
	v_mfma_f32_16x16x32_bf16 v[78:81], v[146:149], v[194:197], v[78:81]
	v_mfma_f32_16x16x32_bf16 v[126:129], v[142:145], v[174:177], v[126:129]
	v_mfma_f32_16x16x32_bf16 v[122:125], v[150:153], v[174:177], v[122:125]
	v_mfma_f32_16x16x32_bf16 v[118:121], v[142:145], v[182:185], v[118:121]
	v_mfma_f32_16x16x32_bf16 v[110:113], v[150:153], v[182:185], v[110:113]
	v_mfma_f32_16x16x32_bf16 v[102:105], v[142:145], v[190:193], v[102:105]
	v_mfma_f32_16x16x32_bf16 v[94:97], v[150:153], v[190:193], v[94:97]
	s_waitcnt lgkmcnt(0)
	v_mfma_f32_16x16x32_bf16 v[86:89], v[142:145], v[198:201], v[86:89]
	v_mfma_f32_16x16x32_bf16 v[78:81], v[150:153], v[198:201], v[78:81]
	v_mfma_f32_16x16x32_bf16 v[114:117], v[154:157], v[170:173], v[114:117]
	v_mfma_f32_16x16x32_bf16 v[106:109], v[162:165], v[170:173], v[106:109]
	v_mfma_f32_16x16x32_bf16 v[98:101], v[154:157], v[178:181], v[98:101]
	v_mfma_f32_16x16x32_bf16 v[90:93], v[162:165], v[178:181], v[90:93]
	v_mfma_f32_16x16x32_bf16 v[82:85], v[154:157], v[186:189], v[82:85]
	v_mfma_f32_16x16x32_bf16 v[74:77], v[162:165], v[186:189], v[74:77]
	v_mfma_f32_16x16x32_bf16 v[70:73], v[154:157], v[194:197], v[70:73]
	v_mfma_f32_16x16x32_bf16 v[66:69], v[162:165], v[194:197], v[66:69]
	v_mfma_f32_16x16x32_bf16 v[114:117], v[158:161], v[174:177], v[114:117]
	v_mfma_f32_16x16x32_bf16 v[106:109], v[166:169], v[174:177], v[106:109]
	v_mfma_f32_16x16x32_bf16 v[98:101], v[158:161], v[182:185], v[98:101]
	v_mfma_f32_16x16x32_bf16 v[90:93], v[166:169], v[182:185], v[90:93]
	v_mfma_f32_16x16x32_bf16 v[82:85], v[158:161], v[190:193], v[82:85]
	v_mfma_f32_16x16x32_bf16 v[74:77], v[166:169], v[190:193], v[74:77]
	v_mfma_f32_16x16x32_bf16 v[70:73], v[158:161], v[198:201], v[70:73]
	v_mfma_f32_16x16x32_bf16 v[66:69], v[166:169], v[198:201], v[66:69]
	s_barrier
	ds_read_b128 v[170:173], v140 offset:49152
	ds_read_b128 v[174:177], v140 offset:50176
	ds_read_b128 v[178:181], v140 offset:51200
	ds_read_b128 v[182:185], v140 offset:52224
	ds_read_b128 v[186:189], v140 offset:53248
	ds_read_b128 v[190:193], v140 offset:54272
	ds_read_b128 v[194:197], v140 offset:55296
	ds_read_b128 v[198:201], v140 offset:56320
	s_add_u32 s22, s26, 0x80
	s_addc_u32 s23, s27, 0
	s_mov_b32 s28, m0
	s_mov_b32 m0, s47
	s_nop 3
	global_load_lds_dwordx4 v134, s[22:23]
	s_mov_b32 m0, s28
	s_nop 0
	s_mov_b32 s28, m0
	s_mov_b32 m0, s48
	s_nop 3
	global_load_lds_dwordx4 v136, s[22:23]
	s_mov_b32 m0, s28
	s_add_u32 s22, s26, 0x40080
	s_addc_u32 s23, s27, 0
	s_mov_b32 s26, m0
	s_mov_b32 m0, s51
	s_nop 3
	global_load_lds_dwordx4 v134, s[22:23]
	s_mov_b32 m0, s26
	s_nop 0
	s_mov_b32 s26, m0
	s_mov_b32 m0, s52
	s_nop 3
	global_load_lds_dwordx4 v136, s[22:23]
	s_mov_b32 m0, s26
	s_mov_b32 s22, m0
	s_mov_b32 m0, s49
	s_nop 3
	global_load_lds_dwordx4 v0, s[24:25]
	s_mov_b32 m0, s22
	s_nop 0
	s_mov_b32 s22, m0
	s_mov_b32 m0, s50
	s_nop 3
	global_load_lds_dwordx4 v135, s[24:25]
	s_mov_b32 m0, s22
	s_waitcnt vmcnt(8)
	s_waitcnt lgkmcnt(0)
	s_barrier
	s_waitcnt lgkmcnt(7)
	v_mfma_f32_16x16x32_bf16 v[62:65], v[130:133], v[170:173], v[62:65]
	v_mfma_f32_16x16x32_bf16 v[58:61], v[146:149], v[170:173], v[58:61]
	s_waitcnt lgkmcnt(5)
	v_mfma_f32_16x16x32_bf16 v[54:57], v[130:133], v[178:181], v[54:57]
	v_mfma_f32_16x16x32_bf16 v[46:49], v[146:149], v[178:181], v[46:49]
	s_waitcnt lgkmcnt(3)
	v_mfma_f32_16x16x32_bf16 v[38:41], v[130:133], v[186:189], v[38:41]
	v_mfma_f32_16x16x32_bf16 v[30:33], v[146:149], v[186:189], v[30:33]
	s_waitcnt lgkmcnt(1)
	v_mfma_f32_16x16x32_bf16 v[22:25], v[130:133], v[194:197], v[22:25]
	v_mfma_f32_16x16x32_bf16 v[14:17], v[146:149], v[194:197], v[14:17]
	v_mfma_f32_16x16x32_bf16 v[62:65], v[142:145], v[174:177], v[62:65]
	v_mfma_f32_16x16x32_bf16 v[58:61], v[150:153], v[174:177], v[58:61]
	v_mfma_f32_16x16x32_bf16 v[54:57], v[142:145], v[182:185], v[54:57]
	v_mfma_f32_16x16x32_bf16 v[46:49], v[150:153], v[182:185], v[46:49]
	v_mfma_f32_16x16x32_bf16 v[38:41], v[142:145], v[190:193], v[38:41]
	v_mfma_f32_16x16x32_bf16 v[30:33], v[150:153], v[190:193], v[30:33]
	s_waitcnt lgkmcnt(0)
	v_mfma_f32_16x16x32_bf16 v[22:25], v[142:145], v[198:201], v[22:25]
	v_mfma_f32_16x16x32_bf16 v[14:17], v[150:153], v[198:201], v[14:17]
	v_mfma_f32_16x16x32_bf16 v[50:53], v[154:157], v[170:173], v[50:53]
	v_mfma_f32_16x16x32_bf16 v[42:45], v[162:165], v[170:173], v[42:45]
	v_mfma_f32_16x16x32_bf16 v[34:37], v[154:157], v[178:181], v[34:37]
	v_mfma_f32_16x16x32_bf16 v[26:29], v[162:165], v[178:181], v[26:29]
	v_mfma_f32_16x16x32_bf16 v[18:21], v[154:157], v[186:189], v[18:21]
	v_mfma_f32_16x16x32_bf16 v[10:13], v[162:165], v[186:189], v[10:13]
	v_mfma_f32_16x16x32_bf16 v[6:9], v[154:157], v[194:197], v[6:9]
	v_mfma_f32_16x16x32_bf16 v[2:5], v[162:165], v[194:197], v[2:5]
	v_mfma_f32_16x16x32_bf16 v[50:53], v[158:161], v[174:177], v[50:53]
	v_mfma_f32_16x16x32_bf16 v[42:45], v[166:169], v[174:177], v[42:45]
	v_mfma_f32_16x16x32_bf16 v[34:37], v[158:161], v[182:185], v[34:37]
	v_mfma_f32_16x16x32_bf16 v[26:29], v[166:169], v[182:185], v[26:29]
	v_mfma_f32_16x16x32_bf16 v[18:21], v[158:161], v[190:193], v[18:21]
	v_mfma_f32_16x16x32_bf16 v[10:13], v[166:169], v[190:193], v[10:13]
	v_mfma_f32_16x16x32_bf16 v[6:9], v[158:161], v[198:201], v[6:9]
	v_mfma_f32_16x16x32_bf16 v[2:5], v[166:169], v[198:201], v[2:5]
	s_barrier
	s_add_i32 s60, s60, 2
	s_add_u32 s58, s58, 0x100
	s_addc_u32 s59, s59, 0
	s_cmp_gt_u32 s60, 13
	s_mov_b64 s[22:23], s[4:5]
	s_cbranch_scc0 .LBB0_712
	s_and_b64 vcc, exec, s[10:11]
	s_cbranch_vccz .LBB0_715
	s_barrier
.LBB0_715:
	s_setprio 0
	s_lshl_b32 s4, s20, 8
	v_or_b32_e32 v130, s4, v138
	s_bfe_i32 s4, s20, 0x10017
	s_lshr_b32 s4, s4, 22
	v_add_u32_e32 v131, s4, v130
	v_and_b32_e32 v131, 0xfffffc00, v131
	v_sub_u32_e32 v132, v130, v131
	v_lshl_add_u32 v141, s56, 8, v137
	v_ashrrev_i32_e32 v133, 31, v132
	v_mov_b64_e32 v[130:131], s[8:9]
	v_mad_i64_i32 v[142:143], s[4:5], v141, s66, v[130:131]
	v_lshlrev_b64 v[132:133], 1, v[132:133]
	v_pk_add_f32 v[128:129], v[128:129], 0 op_sel_hi:[1,0]
	v_pk_add_f32 v[126:127], v[126:127], 0 op_sel_hi:[1,0]
	v_pk_add_f32 v[144:145], v[124:125], 0 op_sel_hi:[1,0]
	v_pk_add_f32 v[124:125], v[122:123], 0 op_sel_hi:[1,0]
	v_lshl_add_u64 v[142:143], v[142:143], 0, v[132:133]
	v_cvt_pk_bf16_f32 v122, v126, v127
	v_cvt_pk_bf16_f32 v123, v128, v129
	v_cvt_pk_bf16_f32 v124, v124, v125
	v_cvt_pk_bf16_f32 v125, v144, v145
	global_store_dwordx4 v[142:143], v[122:125], off
	v_pk_add_f32 v[116:117], v[116:117], 0 op_sel_hi:[1,0]
	v_pk_add_f32 v[114:115], v[114:115], 0 op_sel_hi:[1,0]
	v_pk_add_f32 v[122:123], v[108:109], 0 op_sel_hi:[1,0]
	v_pk_add_f32 v[108:109], v[106:107], 0 op_sel_hi:[1,0]
	v_cvt_pk_bf16_f32 v106, v114, v115
	v_cvt_pk_bf16_f32 v107, v116, v117
	v_cvt_pk_bf16_f32 v108, v108, v109
	v_cvt_pk_bf16_f32 v109, v122, v123
	global_store_dwordx4 v[142:143], v[106:109], off offset:256
	v_pk_add_f32 v[112:113], v[112:113], 0 op_sel_hi:[1,0]
	v_pk_add_f32 v[110:111], v[110:111], 0 op_sel_hi:[1,0]
	v_or_b32_e32 v106, 16, v141
	v_mad_i64_i32 v[106:107], s[4:5], v106, s66, v[130:131]
	v_lshl_add_u64 v[114:115], v[106:107], 0, v[132:133]
	v_pk_add_f32 v[108:109], v[120:121], 0 op_sel_hi:[1,0]
	v_pk_add_f32 v[106:107], v[118:119], 0 op_sel_hi:[1,0]
	v_pk_add_f32 v[100:101], v[100:101], 0 op_sel_hi:[1,0]
	v_cvt_pk_bf16_f32 v106, v106, v107
	v_cvt_pk_bf16_f32 v107, v108, v109
	v_cvt_pk_bf16_f32 v108, v110, v111
	v_cvt_pk_bf16_f32 v109, v112, v113
	global_store_dwordx4 v[114:115], v[106:109], off
	v_pk_add_f32 v[98:99], v[98:99], 0 op_sel_hi:[1,0]
	v_pk_add_f32 v[96:97], v[96:97], 0 op_sel_hi:[1,0]
	v_pk_add_f32 v[106:107], v[92:93], 0 op_sel_hi:[1,0]
	v_pk_add_f32 v[92:93], v[90:91], 0 op_sel_hi:[1,0]
	v_cvt_pk_bf16_f32 v90, v98, v99
	v_cvt_pk_bf16_f32 v91, v100, v101
	v_cvt_pk_bf16_f32 v92, v92, v93
	v_cvt_pk_bf16_f32 v93, v106, v107
	global_store_dwordx4 v[114:115], v[90:93], off offset:256
	v_pk_add_f32 v[94:95], v[94:95], 0 op_sel_hi:[1,0]
	v_pk_add_f32 v[84:85], v[84:85], 0 op_sel_hi:[1,0]
	v_or_b32_e32 v90, 32, v141
	v_mad_i64_i32 v[90:91], s[4:5], v90, s66, v[130:131]
	v_lshl_add_u64 v[98:99], v[90:91], 0, v[132:133]
	v_pk_add_f32 v[92:93], v[104:105], 0 op_sel_hi:[1,0]
	v_pk_add_f32 v[90:91], v[102:103], 0 op_sel_hi:[1,0]
	v_pk_add_f32 v[82:83], v[82:83], 0 op_sel_hi:[1,0]
	v_cvt_pk_bf16_f32 v90, v90, v91
	v_cvt_pk_bf16_f32 v91, v92, v93
	v_cvt_pk_bf16_f32 v92, v94, v95
	v_cvt_pk_bf16_f32 v93, v96, v97
	global_store_dwordx4 v[98:99], v[90:93], off
	v_pk_add_f32 v[80:81], v[80:81], 0 op_sel_hi:[1,0]
	v_pk_add_f32 v[78:79], v[78:79], 0 op_sel_hi:[1,0]
	v_pk_add_f32 v[90:91], v[76:77], 0 op_sel_hi:[1,0]
	v_pk_add_f32 v[76:77], v[74:75], 0 op_sel_hi:[1,0]
	v_cvt_pk_bf16_f32 v74, v82, v83
	v_cvt_pk_bf16_f32 v75, v84, v85
	v_cvt_pk_bf16_f32 v76, v76, v77
	v_cvt_pk_bf16_f32 v77, v90, v91
	global_store_dwordx4 v[98:99], v[74:77], off offset:256
	v_pk_add_f32 v[72:73], v[72:73], 0 op_sel_hi:[1,0]
	v_pk_add_f32 v[70:71], v[70:71], 0 op_sel_hi:[1,0]
	v_or_b32_e32 v74, 48, v141
	v_mad_i64_i32 v[74:75], s[4:5], v74, s66, v[130:131]
	v_lshl_add_u64 v[82:83], v[74:75], 0, v[132:133]
	v_pk_add_f32 v[76:77], v[88:89], 0 op_sel_hi:[1,0]
	v_pk_add_f32 v[74:75], v[86:87], 0 op_sel_hi:[1,0]
	v_pk_add_f32 v[64:65], v[64:65], 0 op_sel_hi:[1,0]
	v_cvt_pk_bf16_f32 v74, v74, v75
	v_cvt_pk_bf16_f32 v75, v76, v77
	v_cvt_pk_bf16_f32 v76, v78, v79
	v_cvt_pk_bf16_f32 v77, v80, v81
	global_store_dwordx4 v[82:83], v[74:77], off
	v_pk_add_f32 v[62:63], v[62:63], 0 op_sel_hi:[1,0]
	v_pk_add_f32 v[52:53], v[52:53], 0 op_sel_hi:[1,0]
	v_pk_add_f32 v[74:75], v[68:69], 0 op_sel_hi:[1,0]
	v_pk_add_f32 v[68:69], v[66:67], 0 op_sel_hi:[1,0]
	v_cvt_pk_bf16_f32 v66, v70, v71
	v_cvt_pk_bf16_f32 v67, v72, v73
	v_cvt_pk_bf16_f32 v68, v68, v69
	v_cvt_pk_bf16_f32 v69, v74, v75
	global_store_dwordx4 v[82:83], v[66:69], off offset:256
	v_pk_add_f32 v[50:51], v[50:51], 0 op_sel_hi:[1,0]
	v_pk_add_f32 v[48:49], v[48:49], 0 op_sel_hi:[1,0]
	v_add_u32_e32 v66, 0x80, v141
	v_mad_i64_i32 v[66:67], s[4:5], v66, s66, v[130:131]
	v_pk_add_f32 v[68:69], v[60:61], 0 op_sel_hi:[1,0]
	v_pk_add_f32 v[60:61], v[58:59], 0 op_sel_hi:[1,0]
	v_lshl_add_u64 v[66:67], v[66:67], 0, v[132:133]
	v_cvt_pk_bf16_f32 v58, v62, v63
	v_cvt_pk_bf16_f32 v59, v64, v65
	v_cvt_pk_bf16_f32 v60, v60, v61
	v_cvt_pk_bf16_f32 v61, v68, v69
	global_store_dwordx4 v[66:67], v[58:61], off
	v_pk_add_f32 v[46:47], v[46:47], 0 op_sel_hi:[1,0]
	v_pk_add_f32 v[36:37], v[36:37], 0 op_sel_hi:[1,0]
	v_pk_add_f32 v[58:59], v[44:45], 0 op_sel_hi:[1,0]
	v_pk_add_f32 v[44:45], v[42:43], 0 op_sel_hi:[1,0]
	v_cvt_pk_bf16_f32 v42, v50, v51
	v_cvt_pk_bf16_f32 v43, v52, v53
	v_cvt_pk_bf16_f32 v44, v44, v45
	v_cvt_pk_bf16_f32 v45, v58, v59
	global_store_dwordx4 v[66:67], v[42:45], off offset:256
	v_pk_add_f32 v[34:35], v[34:35], 0 op_sel_hi:[1,0]
	v_pk_add_f32 v[32:33], v[32:33], 0 op_sel_hi:[1,0]
	v_add_u32_e32 v42, 0x90, v141
	v_mad_i64_i32 v[42:43], s[4:5], v42, s66, v[130:131]
	v_lshl_add_u64 v[50:51], v[42:43], 0, v[132:133]
	v_pk_add_f32 v[44:45], v[56:57], 0 op_sel_hi:[1,0]
	v_pk_add_f32 v[42:43], v[54:55], 0 op_sel_hi:[1,0]
	v_pk_add_f32 v[30:31], v[30:31], 0 op_sel_hi:[1,0]
	v_cvt_pk_bf16_f32 v42, v42, v43
	v_cvt_pk_bf16_f32 v43, v44, v45
	v_cvt_pk_bf16_f32 v44, v46, v47
	v_cvt_pk_bf16_f32 v45, v48, v49
	global_store_dwordx4 v[50:51], v[42:45], off
	v_pk_add_f32 v[20:21], v[20:21], 0 op_sel_hi:[1,0]
	v_pk_add_f32 v[18:19], v[18:19], 0 op_sel_hi:[1,0]
	v_pk_add_f32 v[42:43], v[28:29], 0 op_sel_hi:[1,0]
	v_pk_add_f32 v[28:29], v[26:27], 0 op_sel_hi:[1,0]
	v_cvt_pk_bf16_f32 v26, v34, v35
	v_cvt_pk_bf16_f32 v27, v36, v37
	v_cvt_pk_bf16_f32 v28, v28, v29
	v_cvt_pk_bf16_f32 v29, v42, v43
	global_store_dwordx4 v[50:51], v[26:29], off offset:256
	v_pk_add_f32 v[16:17], v[16:17], 0 op_sel_hi:[1,0]
	v_pk_add_f32 v[14:15], v[14:15], 0 op_sel_hi:[1,0]
	v_add_u32_e32 v26, 0xa0, v141
	v_mad_i64_i32 v[26:27], s[4:5], v26, s66, v[130:131]
	v_lshl_add_u64 v[34:35], v[26:27], 0, v[132:133]
	v_pk_add_f32 v[28:29], v[40:41], 0 op_sel_hi:[1,0]
	v_pk_add_f32 v[26:27], v[38:39], 0 op_sel_hi:[1,0]
	v_pk_add_f32 v[8:9], v[8:9], 0 op_sel_hi:[1,0]
	v_cvt_pk_bf16_f32 v26, v26, v27
	v_cvt_pk_bf16_f32 v27, v28, v29
	v_cvt_pk_bf16_f32 v28, v30, v31
	v_cvt_pk_bf16_f32 v29, v32, v33
	global_store_dwordx4 v[34:35], v[26:29], off
	v_pk_add_f32 v[6:7], v[6:7], 0 op_sel_hi:[1,0]
	s_and_b64 vcc, exec, s[0:1]
	v_pk_add_f32 v[26:27], v[12:13], 0 op_sel_hi:[1,0]
	v_pk_add_f32 v[12:13], v[10:11], 0 op_sel_hi:[1,0]
	v_cvt_pk_bf16_f32 v10, v18, v19
	v_cvt_pk_bf16_f32 v11, v20, v21
	v_cvt_pk_bf16_f32 v12, v12, v13
	v_cvt_pk_bf16_f32 v13, v26, v27
	global_store_dwordx4 v[34:35], v[10:13], off offset:256
	s_mov_b64 s[0:1], -1
	s_nop 0
	v_add_u32_e32 v10, 0xb0, v141
	v_mad_i64_i32 v[10:11], s[4:5], v10, s66, v[130:131]
	v_lshl_add_u64 v[18:19], v[10:11], 0, v[132:133]
	v_pk_add_f32 v[12:13], v[24:25], 0 op_sel_hi:[1,0]
	v_pk_add_f32 v[10:11], v[22:23], 0 op_sel_hi:[1,0]
	s_nop 0
	v_cvt_pk_bf16_f32 v10, v10, v11
	v_cvt_pk_bf16_f32 v11, v12, v13
	v_cvt_pk_bf16_f32 v12, v14, v15
	v_cvt_pk_bf16_f32 v13, v16, v17
	global_store_dwordx4 v[18:19], v[10:13], off
	s_nop 1
	v_pk_add_f32 v[10:11], v[4:5], 0 op_sel_hi:[1,0]
	v_pk_add_f32 v[4:5], v[2:3], 0 op_sel_hi:[1,0]
	v_cvt_pk_bf16_f32 v2, v6, v7
	v_cvt_pk_bf16_f32 v3, v8, v9
	v_cvt_pk_bf16_f32 v4, v4, v5
	v_cvt_pk_bf16_f32 v5, v10, v11
	global_store_dwordx4 v[18:19], v[2:5], off offset:256
	s_cbranch_vccnz .LBB0_706
	s_andn2_b64 vcc, exec, s[6:7]
	s_cbranch_vccnz .LBB0_705
	s_barrier
	s_branch .LBB0_705

.Lprio_730:
	v_add_u32_e32 v141, 0x10000, v139
	ds_read_b128 v[130:133], v141
	ds_read_b128 v[142:145], v141 offset:1024
	ds_read_b128 v[146:149], v141 offset:2048
	ds_read_b128 v[150:153], v141 offset:3072
	v_add_u32_e32 v141, 0x14000, v139
	ds_read_b128 v[154:157], v141
	ds_read_b128 v[158:161], v141 offset:1024
	ds_read_b128 v[162:165], v141 offset:2048
	ds_read_b128 v[166:169], v141 offset:3072
	s_add_u32 s4, s22, 0x100
	s_addc_u32 s5, s23, 0
	s_cmp_eq_u32 s58, 12
	s_cselect_b32 s28, s16, s4
	s_cselect_b32 s29, s17, s5
	s_cselect_b32 s26, s55, s56
	s_cselect_b32 s27, s13, s57
	s_add_u32 s24, s28, 0x80
	s_addc_u32 s25, s29, 0
	ds_read_b128 v[170:173], v140
	ds_read_b128 v[174:177], v140 offset:1024
	ds_read_b128 v[178:181], v140 offset:2048
	ds_read_b128 v[182:185], v140 offset:3072
	ds_read_b128 v[186:189], v140 offset:4096
	ds_read_b128 v[190:193], v140 offset:5120
	ds_read_b128 v[194:197], v140 offset:6144
	ds_read_b128 v[198:201], v140 offset:7168
	s_add_u32 s22, s22, 0x160080
	s_addc_u32 s23, s23, 0
	s_mov_b32 s59, m0
	s_mov_b32 m0, s51
	s_nop 3
	global_load_lds_dwordx4 v0, s[22:23]
	s_mov_b32 m0, s59
	s_add_i32 s59, s21, 0xe000
	s_mov_b32 s60, m0
	s_mov_b32 m0, s59
	s_nop 3
	global_load_lds_dwordx4 v135, s[22:23]
	s_mov_b32 m0, s60
	s_waitcnt vmcnt(8)
	s_waitcnt lgkmcnt(0)
	s_barrier
	s_waitcnt lgkmcnt(7)
	v_mfma_f32_16x16x32_bf16 v[126:129], v[130:133], v[170:173], v[126:129]
	v_mfma_f32_16x16x32_bf16 v[122:125], v[146:149], v[170:173], v[122:125]
	s_waitcnt lgkmcnt(5)
	v_mfma_f32_16x16x32_bf16 v[118:121], v[130:133], v[178:181], v[118:121]
	v_mfma_f32_16x16x32_bf16 v[110:113], v[146:149], v[178:181], v[110:113]
	s_waitcnt lgkmcnt(3)
	v_mfma_f32_16x16x32_bf16 v[102:105], v[130:133], v[186:189], v[102:105]
	v_mfma_f32_16x16x32_bf16 v[94:97], v[146:149], v[186:189], v[94:97]
	s_waitcnt lgkmcnt(1)
	v_mfma_f32_16x16x32_bf16 v[86:89], v[130:133], v[194:197], v[86:89]
	v_mfma_f32_16x16x32_bf16 v[78:81], v[146:149], v[194:197], v[78:81]
	v_mfma_f32_16x16x32_bf16 v[126:129], v[142:145], v[174:177], v[126:129]
	v_mfma_f32_16x16x32_bf16 v[122:125], v[150:153], v[174:177], v[122:125]
	v_mfma_f32_16x16x32_bf16 v[118:121], v[142:145], v[182:185], v[118:121]
	v_mfma_f32_16x16x32_bf16 v[110:113], v[150:153], v[182:185], v[110:113]
	v_mfma_f32_16x16x32_bf16 v[102:105], v[142:145], v[190:193], v[102:105]
	v_mfma_f32_16x16x32_bf16 v[94:97], v[150:153], v[190:193], v[94:97]
	s_waitcnt lgkmcnt(0)
	v_mfma_f32_16x16x32_bf16 v[86:89], v[142:145], v[198:201], v[86:89]
	v_mfma_f32_16x16x32_bf16 v[78:81], v[150:153], v[198:201], v[78:81]
	v_mfma_f32_16x16x32_bf16 v[114:117], v[154:157], v[170:173], v[114:117]
	v_mfma_f32_16x16x32_bf16 v[106:109], v[162:165], v[170:173], v[106:109]
	v_mfma_f32_16x16x32_bf16 v[98:101], v[154:157], v[178:181], v[98:101]
	v_mfma_f32_16x16x32_bf16 v[90:93], v[162:165], v[178:181], v[90:93]
	v_mfma_f32_16x16x32_bf16 v[82:85], v[154:157], v[186:189], v[82:85]
	v_mfma_f32_16x16x32_bf16 v[74:77], v[162:165], v[186:189], v[74:77]
	v_mfma_f32_16x16x32_bf16 v[70:73], v[154:157], v[194:197], v[70:73]
	v_mfma_f32_16x16x32_bf16 v[66:69], v[162:165], v[194:197], v[66:69]
	v_mfma_f32_16x16x32_bf16 v[114:117], v[158:161], v[174:177], v[114:117]
	v_mfma_f32_16x16x32_bf16 v[106:109], v[166:169], v[174:177], v[106:109]
	v_mfma_f32_16x16x32_bf16 v[98:101], v[158:161], v[182:185], v[98:101]
	v_mfma_f32_16x16x32_bf16 v[90:93], v[166:169], v[182:185], v[90:93]
	v_mfma_f32_16x16x32_bf16 v[82:85], v[158:161], v[190:193], v[82:85]
	v_mfma_f32_16x16x32_bf16 v[74:77], v[166:169], v[190:193], v[74:77]
	v_mfma_f32_16x16x32_bf16 v[70:73], v[158:161], v[198:201], v[70:73]
	v_mfma_f32_16x16x32_bf16 v[66:69], v[166:169], v[198:201], v[66:69]
	s_barrier
	ds_read_b128 v[170:173], v140 offset:16384
	ds_read_b128 v[174:177], v140 offset:17408
	ds_read_b128 v[178:181], v140 offset:18432
	ds_read_b128 v[182:185], v140 offset:19456
	ds_read_b128 v[186:189], v140 offset:20480
	ds_read_b128 v[190:193], v140 offset:21504
	ds_read_b128 v[194:197], v140 offset:22528
	ds_read_b128 v[198:201], v140 offset:23552
	s_mov_b32 s22, m0
	s_mov_b32 m0, s34
	s_nop 3
	global_load_lds_dwordx4 v134, s[26:27]
	s_mov_b32 m0, s22
	s_nop 0
	s_mov_b32 s22, m0
	s_mov_b32 m0, s38
	s_nop 3
	global_load_lds_dwordx4 v136, s[26:27]
	s_mov_b32 m0, s22
	s_add_u32 s22, s26, 0x40000
	s_addc_u32 s23, s27, 0
	s_mov_b32 s59, m0
	s_mov_b32 m0, s39
	s_nop 3
	global_load_lds_dwordx4 v134, s[22:23]
	s_mov_b32 m0, s59
	s_nop 0
	s_mov_b32 s59, m0
	s_mov_b32 m0, s40
	s_nop 3
	global_load_lds_dwordx4 v136, s[22:23]
	s_mov_b32 m0, s59
	s_mov_b32 s22, m0
	s_mov_b32 m0, s21
	s_nop 3
	global_load_lds_dwordx4 v0, s[28:29]
	s_mov_b32 m0, s22
	s_nop 0
	s_mov_b32 s22, m0
	s_mov_b32 m0, s41
	s_nop 3
	global_load_lds_dwordx4 v135, s[28:29]
	s_mov_b32 m0, s22
	s_waitcnt vmcnt(8)
	s_waitcnt lgkmcnt(0)
	s_barrier
	s_waitcnt lgkmcnt(7)
	v_mfma_f32_16x16x32_bf16 v[62:65], v[130:133], v[170:173], v[62:65]
	v_mfma_f32_16x16x32_bf16 v[58:61], v[146:149], v[170:173], v[58:61]
	s_waitcnt lgkmcnt(5)
	v_mfma_f32_16x16x32_bf16 v[54:57], v[130:133], v[178:181], v[54:57]
	v_mfma_f32_16x16x32_bf16 v[46:49], v[146:149], v[178:181], v[46:49]
	s_waitcnt lgkmcnt(3)
	v_mfma_f32_16x16x32_bf16 v[38:41], v[130:133], v[186:189], v[38:41]
	v_mfma_f32_16x16x32_bf16 v[30:33], v[146:149], v[186:189], v[30:33]
	s_waitcnt lgkmcnt(1)
	v_mfma_f32_16x16x32_bf16 v[22:25], v[130:133], v[194:197], v[22:25]
	v_mfma_f32_16x16x32_bf16 v[14:17], v[146:149], v[194:197], v[14:17]
	v_mfma_f32_16x16x32_bf16 v[62:65], v[142:145], v[174:177], v[62:65]
	v_mfma_f32_16x16x32_bf16 v[58:61], v[150:153], v[174:177], v[58:61]
	v_mfma_f32_16x16x32_bf16 v[54:57], v[142:145], v[182:185], v[54:57]
	v_mfma_f32_16x16x32_bf16 v[46:49], v[150:153], v[182:185], v[46:49]
	v_mfma_f32_16x16x32_bf16 v[38:41], v[142:145], v[190:193], v[38:41]
	v_mfma_f32_16x16x32_bf16 v[30:33], v[150:153], v[190:193], v[30:33]
	s_waitcnt lgkmcnt(0)
	v_mfma_f32_16x16x32_bf16 v[22:25], v[142:145], v[198:201], v[22:25]
	v_mfma_f32_16x16x32_bf16 v[14:17], v[150:153], v[198:201], v[14:17]
	v_mfma_f32_16x16x32_bf16 v[50:53], v[154:157], v[170:173], v[50:53]
	v_mfma_f32_16x16x32_bf16 v[42:45], v[162:165], v[170:173], v[42:45]
	v_mfma_f32_16x16x32_bf16 v[34:37], v[154:157], v[178:181], v[34:37]
	v_mfma_f32_16x16x32_bf16 v[26:29], v[162:165], v[178:181], v[26:29]
	v_mfma_f32_16x16x32_bf16 v[18:21], v[154:157], v[186:189], v[18:21]
	v_mfma_f32_16x16x32_bf16 v[10:13], v[162:165], v[186:189], v[10:13]
	v_mfma_f32_16x16x32_bf16 v[6:9], v[154:157], v[194:197], v[6:9]
	v_mfma_f32_16x16x32_bf16 v[2:5], v[162:165], v[194:197], v[2:5]
	v_mfma_f32_16x16x32_bf16 v[50:53], v[158:161], v[174:177], v[50:53]
	v_mfma_f32_16x16x32_bf16 v[42:45], v[166:169], v[174:177], v[42:45]
	v_mfma_f32_16x16x32_bf16 v[34:37], v[158:161], v[182:185], v[34:37]
	v_mfma_f32_16x16x32_bf16 v[26:29], v[166:169], v[182:185], v[26:29]
	v_mfma_f32_16x16x32_bf16 v[18:21], v[158:161], v[190:193], v[18:21]
	v_mfma_f32_16x16x32_bf16 v[10:13], v[166:169], v[190:193], v[10:13]
	v_mfma_f32_16x16x32_bf16 v[6:9], v[158:161], v[198:201], v[6:9]
	v_mfma_f32_16x16x32_bf16 v[2:5], v[166:169], v[198:201], v[2:5]
	s_barrier
	v_add_u32_e32 v141, 0x18000, v139
	ds_read_b128 v[130:133], v141
	ds_read_b128 v[142:145], v141 offset:1024
	ds_read_b128 v[146:149], v141 offset:2048
	ds_read_b128 v[150:153], v141 offset:3072
	v_add_u32_e32 v141, 0x1c000, v139
	ds_read_b128 v[154:157], v141
	ds_read_b128 v[158:161], v141 offset:1024
	ds_read_b128 v[162:165], v141 offset:2048
	ds_read_b128 v[166:169], v141 offset:3072
	ds_read_b128 v[170:173], v140 offset:32768
	ds_read_b128 v[174:177], v140 offset:33792
	ds_read_b128 v[178:181], v140 offset:34816
	ds_read_b128 v[182:185], v140 offset:35840
	ds_read_b128 v[186:189], v140 offset:36864
	ds_read_b128 v[190:193], v140 offset:37888
	ds_read_b128 v[194:197], v140 offset:38912
	ds_read_b128 v[198:201], v140 offset:39936
	s_add_u32 s22, s28, 0x160000
	s_addc_u32 s23, s29, 0
	s_mov_b32 s28, m0
	s_mov_b32 m0, s42
	s_nop 3
	global_load_lds_dwordx4 v0, s[22:23]
	s_mov_b32 m0, s28
	s_nop 0
	s_mov_b32 s28, m0
	s_mov_b32 m0, s43
	s_nop 3
	global_load_lds_dwordx4 v135, s[22:23]
	s_mov_b32 m0, s28
	s_waitcnt vmcnt(8)
	s_waitcnt lgkmcnt(0)
	s_barrier
	s_waitcnt lgkmcnt(7)
	v_mfma_f32_16x16x32_bf16 v[126:129], v[130:133], v[170:173], v[126:129]
	v_mfma_f32_16x16x32_bf16 v[122:125], v[146:149], v[170:173], v[122:125]
	s_waitcnt lgkmcnt(5)
	v_mfma_f32_16x16x32_bf16 v[118:121], v[130:133], v[178:181], v[118:121]
	v_mfma_f32_16x16x32_bf16 v[110:113], v[146:149], v[178:181], v[110:113]
	s_waitcnt lgkmcnt(3)
	v_mfma_f32_16x16x32_bf16 v[102:105], v[130:133], v[186:189], v[102:105]
	v_mfma_f32_16x16x32_bf16 v[94:97], v[146:149], v[186:189], v[94:97]
	s_waitcnt lgkmcnt(1)
	v_mfma_f32_16x16x32_bf16 v[86:89], v[130:133], v[194:197], v[86:89]
	v_mfma_f32_16x16x32_bf16 v[78:81], v[146:149], v[194:197], v[78:81]
	v_mfma_f32_16x16x32_bf16 v[126:129], v[142:145], v[174:177], v[126:129]
	v_mfma_f32_16x16x32_bf16 v[122:125], v[150:153], v[174:177], v[122:125]
	v_mfma_f32_16x16x32_bf16 v[118:121], v[142:145], v[182:185], v[118:121]
	v_mfma_f32_16x16x32_bf16 v[110:113], v[150:153], v[182:185], v[110:113]
	v_mfma_f32_16x16x32_bf16 v[102:105], v[142:145], v[190:193], v[102:105]
	v_mfma_f32_16x16x32_bf16 v[94:97], v[150:153], v[190:193], v[94:97]
	s_waitcnt lgkmcnt(0)
	v_mfma_f32_16x16x32_bf16 v[86:89], v[142:145], v[198:201], v[86:89]
	v_mfma_f32_16x16x32_bf16 v[78:81], v[150:153], v[198:201], v[78:81]
	v_mfma_f32_16x16x32_bf16 v[114:117], v[154:157], v[170:173], v[114:117]
	v_mfma_f32_16x16x32_bf16 v[106:109], v[162:165], v[170:173], v[106:109]
	v_mfma_f32_16x16x32_bf16 v[98:101], v[154:157], v[178:181], v[98:101]
	v_mfma_f32_16x16x32_bf16 v[90:93], v[162:165], v[178:181], v[90:93]
	v_mfma_f32_16x16x32_bf16 v[82:85], v[154:157], v[186:189], v[82:85]
	v_mfma_f32_16x16x32_bf16 v[74:77], v[162:165], v[186:189], v[74:77]
	v_mfma_f32_16x16x32_bf16 v[70:73], v[154:157], v[194:197], v[70:73]
	v_mfma_f32_16x16x32_bf16 v[66:69], v[162:165], v[194:197], v[66:69]
	v_mfma_f32_16x16x32_bf16 v[114:117], v[158:161], v[174:177], v[114:117]
	v_mfma_f32_16x16x32_bf16 v[106:109], v[166:169], v[174:177], v[106:109]
	v_mfma_f32_16x16x32_bf16 v[98:101], v[158:161], v[182:185], v[98:101]
	v_mfma_f32_16x16x32_bf16 v[90:93], v[166:169], v[182:185], v[90:93]
	v_mfma_f32_16x16x32_bf16 v[82:85], v[158:161], v[190:193], v[82:85]
	v_mfma_f32_16x16x32_bf16 v[74:77], v[166:169], v[190:193], v[74:77]
	v_mfma_f32_16x16x32_bf16 v[70:73], v[158:161], v[198:201], v[70:73]
	v_mfma_f32_16x16x32_bf16 v[66:69], v[166:169], v[198:201], v[66:69]
	s_barrier
	ds_read_b128 v[170:173], v140 offset:49152
	ds_read_b128 v[174:177], v140 offset:50176
	ds_read_b128 v[178:181], v140 offset:51200
	ds_read_b128 v[182:185], v140 offset:52224
	ds_read_b128 v[186:189], v140 offset:53248
	ds_read_b128 v[190:193], v140 offset:54272
	ds_read_b128 v[194:197], v140 offset:55296
	ds_read_b128 v[198:201], v140 offset:56320
	s_add_u32 s22, s26, 0x80
	s_addc_u32 s23, s27, 0
	s_mov_b32 s28, m0
	s_mov_b32 m0, s44
	s_nop 3
	global_load_lds_dwordx4 v134, s[22:23]
	s_mov_b32 m0, s28
	s_nop 0
	s_mov_b32 s28, m0
	s_mov_b32 m0, s45
	s_nop 3
	global_load_lds_dwordx4 v136, s[22:23]
	s_mov_b32 m0, s28
	s_add_u32 s22, s26, 0x40080
	s_addc_u32 s23, s27, 0
	s_mov_b32 s26, m0
	s_mov_b32 m0, s49
	s_nop 3
	global_load_lds_dwordx4 v134, s[22:23]
	s_mov_b32 m0, s26
	s_nop 0
	s_mov_b32 s26, m0
	s_mov_b32 m0, s50
	s_nop 3
	global_load_lds_dwordx4 v136, s[22:23]
	s_mov_b32 m0, s26
	s_mov_b32 s22, m0
	s_mov_b32 m0, s47
	s_nop 3
	global_load_lds_dwordx4 v0, s[24:25]
	s_mov_b32 m0, s22
	s_nop 0
	s_mov_b32 s22, m0
	s_mov_b32 m0, s48
	s_nop 3
	global_load_lds_dwordx4 v135, s[24:25]
	s_mov_b32 m0, s22
	s_waitcnt vmcnt(8)
	s_waitcnt lgkmcnt(0)
	s_barrier
	s_waitcnt lgkmcnt(7)
	v_mfma_f32_16x16x32_bf16 v[62:65], v[130:133], v[170:173], v[62:65]
	v_mfma_f32_16x16x32_bf16 v[58:61], v[146:149], v[170:173], v[58:61]
	s_waitcnt lgkmcnt(5)
	v_mfma_f32_16x16x32_bf16 v[54:57], v[130:133], v[178:181], v[54:57]
	v_mfma_f32_16x16x32_bf16 v[46:49], v[146:149], v[178:181], v[46:49]
	s_waitcnt lgkmcnt(3)
	v_mfma_f32_16x16x32_bf16 v[38:41], v[130:133], v[186:189], v[38:41]
	v_mfma_f32_16x16x32_bf16 v[30:33], v[146:149], v[186:189], v[30:33]
	s_waitcnt lgkmcnt(1)
	v_mfma_f32_16x16x32_bf16 v[22:25], v[130:133], v[194:197], v[22:25]
	v_mfma_f32_16x16x32_bf16 v[14:17], v[146:149], v[194:197], v[14:17]
	v_mfma_f32_16x16x32_bf16 v[62:65], v[142:145], v[174:177], v[62:65]
	v_mfma_f32_16x16x32_bf16 v[58:61], v[150:153], v[174:177], v[58:61]
	v_mfma_f32_16x16x32_bf16 v[54:57], v[142:145], v[182:185], v[54:57]
	v_mfma_f32_16x16x32_bf16 v[46:49], v[150:153], v[182:185], v[46:49]
	v_mfma_f32_16x16x32_bf16 v[38:41], v[142:145], v[190:193], v[38:41]
	v_mfma_f32_16x16x32_bf16 v[30:33], v[150:153], v[190:193], v[30:33]
	s_waitcnt lgkmcnt(0)
	v_mfma_f32_16x16x32_bf16 v[22:25], v[142:145], v[198:201], v[22:25]
	v_mfma_f32_16x16x32_bf16 v[14:17], v[150:153], v[198:201], v[14:17]
	v_mfma_f32_16x16x32_bf16 v[50:53], v[154:157], v[170:173], v[50:53]
	v_mfma_f32_16x16x32_bf16 v[42:45], v[162:165], v[170:173], v[42:45]
	v_mfma_f32_16x16x32_bf16 v[34:37], v[154:157], v[178:181], v[34:37]
	v_mfma_f32_16x16x32_bf16 v[26:29], v[162:165], v[178:181], v[26:29]
	v_mfma_f32_16x16x32_bf16 v[18:21], v[154:157], v[186:189], v[18:21]
	v_mfma_f32_16x16x32_bf16 v[10:13], v[162:165], v[186:189], v[10:13]
	v_mfma_f32_16x16x32_bf16 v[6:9], v[154:157], v[194:197], v[6:9]
	v_mfma_f32_16x16x32_bf16 v[2:5], v[162:165], v[194:197], v[2:5]
	v_mfma_f32_16x16x32_bf16 v[50:53], v[158:161], v[174:177], v[50:53]
	v_mfma_f32_16x16x32_bf16 v[42:45], v[166:169], v[174:177], v[42:45]
	v_mfma_f32_16x16x32_bf16 v[34:37], v[158:161], v[182:185], v[34:37]
	v_mfma_f32_16x16x32_bf16 v[26:29], v[166:169], v[182:185], v[26:29]
	v_mfma_f32_16x16x32_bf16 v[18:21], v[158:161], v[190:193], v[18:21]
	v_mfma_f32_16x16x32_bf16 v[10:13], v[166:169], v[190:193], v[10:13]
	v_mfma_f32_16x16x32_bf16 v[6:9], v[158:161], v[198:201], v[6:9]
	v_mfma_f32_16x16x32_bf16 v[2:5], v[166:169], v[198:201], v[2:5]
	s_barrier
	s_add_i32 s58, s58, 2
	s_add_u32 s56, s56, 0x100
	s_addc_u32 s57, s57, 0
	s_cmp_gt_u32 s58, 13
	s_mov_b64 s[22:23], s[4:5]
	s_cbranch_scc0 .LBB0_730
	s_and_b64 vcc, exec, s[10:11]
	v_readlane_b32 s56, v253, 57
	v_readlane_b32 s57, v253, 58
	s_cbranch_vccz .LBB0_733
	s_barrier
.LBB0_733:
	s_setprio 0
	s_lshl_b32 s4, s20, 8
	v_or_b32_e32 v130, s4, v138
	s_bfe_i32 s4, s20, 0x10017
	s_lshr_b32 s4, s4, 22
	v_add_u32_e32 v131, s4, v130
	v_and_b32_e32 v131, 0xfffffc00, v131
	v_sub_u32_e32 v132, v130, v131
	v_lshl_add_u32 v141, s54, 8, v137
	v_ashrrev_i32_e32 v133, 31, v132
	v_mov_b64_e32 v[130:131], s[8:9]
	v_mad_i64_i32 v[142:143], s[4:5], v141, s66, v[130:131]
	v_lshlrev_b64 v[132:133], 1, v[132:133]
	v_pk_add_f32 v[128:129], v[128:129], 0 op_sel_hi:[1,0]
	v_pk_add_f32 v[126:127], v[126:127], 0 op_sel_hi:[1,0]
	v_pk_add_f32 v[144:145], v[124:125], 0 op_sel_hi:[1,0]
	v_pk_add_f32 v[124:125], v[122:123], 0 op_sel_hi:[1,0]
	v_lshl_add_u64 v[142:143], v[142:143], 0, v[132:133]
	v_cvt_pk_bf16_f32 v122, v126, v127
	v_cvt_pk_bf16_f32 v123, v128, v129
	v_cvt_pk_bf16_f32 v124, v124, v125
	v_cvt_pk_bf16_f32 v125, v144, v145
	global_store_dwordx4 v[142:143], v[122:125], off
	v_pk_add_f32 v[116:117], v[116:117], 0 op_sel_hi:[1,0]
	v_pk_add_f32 v[114:115], v[114:115], 0 op_sel_hi:[1,0]
	v_pk_add_f32 v[122:123], v[108:109], 0 op_sel_hi:[1,0]
	v_pk_add_f32 v[108:109], v[106:107], 0 op_sel_hi:[1,0]
	v_cvt_pk_bf16_f32 v106, v114, v115
	v_cvt_pk_bf16_f32 v107, v116, v117
	v_cvt_pk_bf16_f32 v108, v108, v109
	v_cvt_pk_bf16_f32 v109, v122, v123
	global_store_dwordx4 v[142:143], v[106:109], off offset:256
	v_pk_add_f32 v[112:113], v[112:113], 0 op_sel_hi:[1,0]
	v_pk_add_f32 v[110:111], v[110:111], 0 op_sel_hi:[1,0]
	v_or_b32_e32 v106, 16, v141
	v_mad_i64_i32 v[106:107], s[4:5], v106, s66, v[130:131]
	v_lshl_add_u64 v[114:115], v[106:107], 0, v[132:133]
	v_pk_add_f32 v[108:109], v[120:121], 0 op_sel_hi:[1,0]
	v_pk_add_f32 v[106:107], v[118:119], 0 op_sel_hi:[1,0]
	v_pk_add_f32 v[100:101], v[100:101], 0 op_sel_hi:[1,0]
	v_cvt_pk_bf16_f32 v106, v106, v107
	v_cvt_pk_bf16_f32 v107, v108, v109
	v_cvt_pk_bf16_f32 v108, v110, v111
	v_cvt_pk_bf16_f32 v109, v112, v113
	global_store_dwordx4 v[114:115], v[106:109], off
	v_pk_add_f32 v[98:99], v[98:99], 0 op_sel_hi:[1,0]
	v_pk_add_f32 v[96:97], v[96:97], 0 op_sel_hi:[1,0]
	v_pk_add_f32 v[106:107], v[92:93], 0 op_sel_hi:[1,0]
	v_pk_add_f32 v[92:93], v[90:91], 0 op_sel_hi:[1,0]
	v_cvt_pk_bf16_f32 v90, v98, v99
	v_cvt_pk_bf16_f32 v91, v100, v101
	v_cvt_pk_bf16_f32 v92, v92, v93
	v_cvt_pk_bf16_f32 v93, v106, v107
	global_store_dwordx4 v[114:115], v[90:93], off offset:256
	v_pk_add_f32 v[94:95], v[94:95], 0 op_sel_hi:[1,0]
	v_pk_add_f32 v[84:85], v[84:85], 0 op_sel_hi:[1,0]
	v_or_b32_e32 v90, 32, v141
	v_mad_i64_i32 v[90:91], s[4:5], v90, s66, v[130:131]
	v_lshl_add_u64 v[98:99], v[90:91], 0, v[132:133]
	v_pk_add_f32 v[92:93], v[104:105], 0 op_sel_hi:[1,0]
	v_pk_add_f32 v[90:91], v[102:103], 0 op_sel_hi:[1,0]
	v_pk_add_f32 v[82:83], v[82:83], 0 op_sel_hi:[1,0]
	v_cvt_pk_bf16_f32 v90, v90, v91
	v_cvt_pk_bf16_f32 v91, v92, v93
	v_cvt_pk_bf16_f32 v92, v94, v95
	v_cvt_pk_bf16_f32 v93, v96, v97
	global_store_dwordx4 v[98:99], v[90:93], off
	v_pk_add_f32 v[80:81], v[80:81], 0 op_sel_hi:[1,0]
	v_pk_add_f32 v[78:79], v[78:79], 0 op_sel_hi:[1,0]
	v_pk_add_f32 v[90:91], v[76:77], 0 op_sel_hi:[1,0]
	v_pk_add_f32 v[76:77], v[74:75], 0 op_sel_hi:[1,0]
	v_cvt_pk_bf16_f32 v74, v82, v83
	v_cvt_pk_bf16_f32 v75, v84, v85
	v_cvt_pk_bf16_f32 v76, v76, v77
	v_cvt_pk_bf16_f32 v77, v90, v91
	global_store_dwordx4 v[98:99], v[74:77], off offset:256
	v_pk_add_f32 v[72:73], v[72:73], 0 op_sel_hi:[1,0]
	v_pk_add_f32 v[70:71], v[70:71], 0 op_sel_hi:[1,0]
	v_or_b32_e32 v74, 48, v141
	v_mad_i64_i32 v[74:75], s[4:5], v74, s66, v[130:131]
	v_lshl_add_u64 v[82:83], v[74:75], 0, v[132:133]
	v_pk_add_f32 v[76:77], v[88:89], 0 op_sel_hi:[1,0]
	v_pk_add_f32 v[74:75], v[86:87], 0 op_sel_hi:[1,0]
	v_pk_add_f32 v[64:65], v[64:65], 0 op_sel_hi:[1,0]
	v_cvt_pk_bf16_f32 v74, v74, v75
	v_cvt_pk_bf16_f32 v75, v76, v77
	v_cvt_pk_bf16_f32 v76, v78, v79
	v_cvt_pk_bf16_f32 v77, v80, v81
	global_store_dwordx4 v[82:83], v[74:77], off
	v_pk_add_f32 v[62:63], v[62:63], 0 op_sel_hi:[1,0]
	v_pk_add_f32 v[52:53], v[52:53], 0 op_sel_hi:[1,0]
	v_pk_add_f32 v[74:75], v[68:69], 0 op_sel_hi:[1,0]
	v_pk_add_f32 v[68:69], v[66:67], 0 op_sel_hi:[1,0]
	v_cvt_pk_bf16_f32 v66, v70, v71
	v_cvt_pk_bf16_f32 v67, v72, v73
	v_cvt_pk_bf16_f32 v68, v68, v69
	v_cvt_pk_bf16_f32 v69, v74, v75
	global_store_dwordx4 v[82:83], v[66:69], off offset:256
	v_pk_add_f32 v[50:51], v[50:51], 0 op_sel_hi:[1,0]
	v_pk_add_f32 v[48:49], v[48:49], 0 op_sel_hi:[1,0]
	v_add_u32_e32 v66, 0x80, v141
	v_mad_i64_i32 v[66:67], s[4:5], v66, s66, v[130:131]
	v_pk_add_f32 v[68:69], v[60:61], 0 op_sel_hi:[1,0]
	v_pk_add_f32 v[60:61], v[58:59], 0 op_sel_hi:[1,0]
	v_lshl_add_u64 v[66:67], v[66:67], 0, v[132:133]
	v_cvt_pk_bf16_f32 v58, v62, v63
	v_cvt_pk_bf16_f32 v59, v64, v65
	v_cvt_pk_bf16_f32 v60, v60, v61
	v_cvt_pk_bf16_f32 v61, v68, v69
	global_store_dwordx4 v[66:67], v[58:61], off
	v_pk_add_f32 v[46:47], v[46:47], 0 op_sel_hi:[1,0]
	v_pk_add_f32 v[36:37], v[36:37], 0 op_sel_hi:[1,0]
	v_pk_add_f32 v[58:59], v[44:45], 0 op_sel_hi:[1,0]
	v_pk_add_f32 v[44:45], v[42:43], 0 op_sel_hi:[1,0]
	v_cvt_pk_bf16_f32 v42, v50, v51
	v_cvt_pk_bf16_f32 v43, v52, v53
	v_cvt_pk_bf16_f32 v44, v44, v45
	v_cvt_pk_bf16_f32 v45, v58, v59
	global_store_dwordx4 v[66:67], v[42:45], off offset:256
	v_pk_add_f32 v[34:35], v[34:35], 0 op_sel_hi:[1,0]
	v_pk_add_f32 v[32:33], v[32:33], 0 op_sel_hi:[1,0]
	v_add_u32_e32 v42, 0x90, v141
	v_mad_i64_i32 v[42:43], s[4:5], v42, s66, v[130:131]
	v_lshl_add_u64 v[50:51], v[42:43], 0, v[132:133]
	v_pk_add_f32 v[44:45], v[56:57], 0 op_sel_hi:[1,0]
	v_pk_add_f32 v[42:43], v[54:55], 0 op_sel_hi:[1,0]
	v_pk_add_f32 v[30:31], v[30:31], 0 op_sel_hi:[1,0]
	v_cvt_pk_bf16_f32 v42, v42, v43
	v_cvt_pk_bf16_f32 v43, v44, v45
	v_cvt_pk_bf16_f32 v44, v46, v47
	v_cvt_pk_bf16_f32 v45, v48, v49
	global_store_dwordx4 v[50:51], v[42:45], off
	v_pk_add_f32 v[20:21], v[20:21], 0 op_sel_hi:[1,0]
	v_pk_add_f32 v[18:19], v[18:19], 0 op_sel_hi:[1,0]
	v_pk_add_f32 v[42:43], v[28:29], 0 op_sel_hi:[1,0]
	v_pk_add_f32 v[28:29], v[26:27], 0 op_sel_hi:[1,0]
	v_cvt_pk_bf16_f32 v26, v34, v35
	v_cvt_pk_bf16_f32 v27, v36, v37
	v_cvt_pk_bf16_f32 v28, v28, v29
	v_cvt_pk_bf16_f32 v29, v42, v43
	global_store_dwordx4 v[50:51], v[26:29], off offset:256
	v_pk_add_f32 v[16:17], v[16:17], 0 op_sel_hi:[1,0]
	v_pk_add_f32 v[14:15], v[14:15], 0 op_sel_hi:[1,0]
	v_add_u32_e32 v26, 0xa0, v141
	v_mad_i64_i32 v[26:27], s[4:5], v26, s66, v[130:131]
	v_lshl_add_u64 v[34:35], v[26:27], 0, v[132:133]
	v_pk_add_f32 v[28:29], v[40:41], 0 op_sel_hi:[1,0]
	v_pk_add_f32 v[26:27], v[38:39], 0 op_sel_hi:[1,0]
	v_pk_add_f32 v[8:9], v[8:9], 0 op_sel_hi:[1,0]
	v_cvt_pk_bf16_f32 v26, v26, v27
	v_cvt_pk_bf16_f32 v27, v28, v29
	v_cvt_pk_bf16_f32 v28, v30, v31
	v_cvt_pk_bf16_f32 v29, v32, v33
	global_store_dwordx4 v[34:35], v[26:29], off
	v_pk_add_f32 v[6:7], v[6:7], 0 op_sel_hi:[1,0]
	s_and_b64 vcc, exec, s[0:1]
	v_pk_add_f32 v[26:27], v[12:13], 0 op_sel_hi:[1,0]
	v_pk_add_f32 v[12:13], v[10:11], 0 op_sel_hi:[1,0]
	v_cvt_pk_bf16_f32 v10, v18, v19
	v_cvt_pk_bf16_f32 v11, v20, v21
	v_cvt_pk_bf16_f32 v12, v12, v13
	v_cvt_pk_bf16_f32 v13, v26, v27
	global_store_dwordx4 v[34:35], v[10:13], off offset:256
	s_mov_b64 s[0:1], -1
	s_nop 0
	v_add_u32_e32 v10, 0xb0, v141
	v_mad_i64_i32 v[10:11], s[4:5], v10, s66, v[130:131]
	v_lshl_add_u64 v[18:19], v[10:11], 0, v[132:133]
	v_pk_add_f32 v[12:13], v[24:25], 0 op_sel_hi:[1,0]
	v_pk_add_f32 v[10:11], v[22:23], 0 op_sel_hi:[1,0]
	s_nop 0
	v_cvt_pk_bf16_f32 v10, v10, v11
	v_cvt_pk_bf16_f32 v11, v12, v13
	v_cvt_pk_bf16_f32 v12, v14, v15
	v_cvt_pk_bf16_f32 v13, v16, v17
	global_store_dwordx4 v[18:19], v[10:13], off
	s_nop 1
	v_pk_add_f32 v[10:11], v[4:5], 0 op_sel_hi:[1,0]
	v_pk_add_f32 v[4:5], v[2:3], 0 op_sel_hi:[1,0]
	v_cvt_pk_bf16_f32 v2, v6, v7
	v_cvt_pk_bf16_f32 v3, v8, v9
	v_cvt_pk_bf16_f32 v4, v4, v5
	v_cvt_pk_bf16_f32 v5, v10, v11
	global_store_dwordx4 v[18:19], v[2:5], off offset:256
	s_cbranch_vccnz .LBB0_724
	s_andn2_b64 vcc, exec, s[6:7]
	s_cbranch_vccnz .LBB0_723
	s_barrier
	s_branch .LBB0_723

.Lprio_799:
	v_add_u32_e32 v0, 0x10000, v192
	ds_read_b128 v[26:29], v0
	ds_read_b128 v[30:33], v0 offset:1024
	s_waitcnt vmcnt(2)
	ds_read_b128 v[18:21], v0 offset:2048
	s_waitcnt vmcnt(1)
	ds_read_b128 v[22:25], v0 offset:3072
	v_add_u32_e32 v0, 0x14000, v192
	ds_read_b128 v[10:13], v0
	ds_read_b128 v[14:17], v0 offset:1024
	ds_read_b128 v[2:5], v0 offset:2048
	ds_read_b128 v[6:9], v0 offset:3072
	s_add_u32 s26, s36, 0x100
	s_addc_u32 s27, s37, 0
	s_cmp_eq_u32 s68, 4
	s_cselect_b32 s40, s21, s26
	s_cselect_b32 s41, s1, s27
	s_cselect_b32 s34, s29, s66
	s_cselect_b32 s35, s19, s67
	s_add_u32 s30, s40, 0x80
	s_addc_u32 s31, s41, 0
	s_waitcnt vmcnt(0)
	ds_read_b128 v[162:165], v193
	ds_read_b128 v[166:169], v193 offset:1024
	ds_read_b128 v[170:173], v193 offset:2048
	ds_read_b128 v[174:177], v193 offset:3072
	ds_read_b128 v[194:197], v193 offset:4096
	ds_read_b128 v[198:201], v193 offset:5120
	ds_read_b128 v[202:205], v193 offset:6144
	ds_read_b128 v[206:209], v193 offset:7168
	s_add_u32 s36, s36, 0x20080
	s_addc_u32 s37, s37, 0
	s_mov_b32 s69, m0
	s_mov_b32 m0, s64
	s_nop 3
	global_load_lds_dwordx4 v184, s[36:37]
	s_mov_b32 m0, s69
	s_add_i32 s69, s48, 0xe000
	s_mov_b32 s70, m0
	s_mov_b32 m0, s69
	s_nop 3
	global_load_lds_dwordx4 v186, s[36:37]
	s_mov_b32 m0, s70
	s_waitcnt vmcnt(8)
	s_waitcnt lgkmcnt(0)
	s_barrier
	s_waitcnt lgkmcnt(6)
	v_mfma_scale_f32_16x16x128_f8f6f4 v[158:161], v[26:33], v[162:169], v[158:161], v188, v189 op_sel_hi:[0,0,0]
	v_mfma_scale_f32_16x16x128_f8f6f4 v[154:157], v[18:25], v[162:169], v[154:157], v188, v189 op_sel_hi:[0,0,0]
	s_waitcnt lgkmcnt(4)
	v_mfma_scale_f32_16x16x128_f8f6f4 v[142:145], v[26:33], v[170:177], v[142:145], v188, v189 op_sel_hi:[0,0,0]
	v_mfma_scale_f32_16x16x128_f8f6f4 v[138:141], v[18:25], v[170:177], v[138:141], v188, v189 op_sel_hi:[0,0,0]
	s_waitcnt lgkmcnt(2)
	v_mfma_scale_f32_16x16x128_f8f6f4 v[126:129], v[26:33], v[194:201], v[126:129], v188, v189 op_sel_hi:[0,0,0]
	v_mfma_scale_f32_16x16x128_f8f6f4 v[122:125], v[18:25], v[194:201], v[122:125], v188, v189 op_sel_hi:[0,0,0]
	s_waitcnt lgkmcnt(0)
	v_mfma_scale_f32_16x16x128_f8f6f4 v[110:113], v[26:33], v[202:209], v[110:113], v188, v189 op_sel_hi:[0,0,0]
	v_mfma_scale_f32_16x16x128_f8f6f4 v[106:109], v[18:25], v[202:209], v[106:109], v188, v189 op_sel_hi:[0,0,0]
	v_mfma_scale_f32_16x16x128_f8f6f4 v[150:153], v[10:17], v[162:169], v[150:153], v188, v189 op_sel_hi:[0,0,0]
	v_mfma_scale_f32_16x16x128_f8f6f4 v[146:149], v[2:9], v[162:169], v[146:149], v188, v189 op_sel_hi:[0,0,0]
	v_mfma_scale_f32_16x16x128_f8f6f4 v[134:137], v[10:17], v[170:177], v[134:137], v188, v189 op_sel_hi:[0,0,0]
	v_mfma_scale_f32_16x16x128_f8f6f4 v[130:133], v[2:9], v[170:177], v[130:133], v188, v189 op_sel_hi:[0,0,0]
	v_mfma_scale_f32_16x16x128_f8f6f4 v[118:121], v[10:17], v[194:201], v[118:121], v188, v189 op_sel_hi:[0,0,0]
	v_mfma_scale_f32_16x16x128_f8f6f4 v[114:117], v[2:9], v[194:201], v[114:117], v188, v189 op_sel_hi:[0,0,0]
	v_mfma_scale_f32_16x16x128_f8f6f4 v[102:105], v[10:17], v[202:209], v[102:105], v188, v189 op_sel_hi:[0,0,0]
	v_mfma_scale_f32_16x16x128_f8f6f4 v[98:101], v[2:9], v[202:209], v[98:101], v188, v189 op_sel_hi:[0,0,0]
	s_barrier
	ds_read_b128 v[162:165], v193 offset:16384
	ds_read_b128 v[166:169], v193 offset:17408
	ds_read_b128 v[170:173], v193 offset:18432
	ds_read_b128 v[174:177], v193 offset:19456
	ds_read_b128 v[194:197], v193 offset:20480
	ds_read_b128 v[198:201], v193 offset:21504
	ds_read_b128 v[202:205], v193 offset:22528
	ds_read_b128 v[206:209], v193 offset:23552
	s_mov_b32 s36, m0
	s_mov_b32 m0, s49
	s_nop 3
	global_load_lds_dwordx4 v185, s[34:35]
	s_mov_b32 m0, s36
	s_nop 0
	s_mov_b32 s36, m0
	s_mov_b32 m0, s50
	s_nop 3
	global_load_lds_dwordx4 v187, s[34:35]
	s_mov_b32 m0, s36
	s_add_u32 s36, s34, 0x20000
	s_addc_u32 s37, s35, 0
	s_mov_b32 s69, m0
	s_mov_b32 m0, s51
	s_nop 3
	global_load_lds_dwordx4 v185, s[36:37]
	s_mov_b32 m0, s69
	s_nop 0
	s_mov_b32 s69, m0
	s_mov_b32 m0, s52
	s_nop 3
	global_load_lds_dwordx4 v187, s[36:37]
	s_mov_b32 m0, s69
	s_mov_b32 s36, m0
	s_mov_b32 m0, s48
	s_nop 3
	global_load_lds_dwordx4 v184, s[40:41]
	s_mov_b32 m0, s36
	s_nop 0
	s_mov_b32 s36, m0
	s_mov_b32 m0, s53
	s_nop 3
	global_load_lds_dwordx4 v186, s[40:41]
	s_mov_b32 m0, s36
	s_waitcnt vmcnt(8)
	s_waitcnt lgkmcnt(0)
	s_barrier
	s_waitcnt lgkmcnt(6)
	v_mfma_scale_f32_16x16x128_f8f6f4 v[94:97], v[26:33], v[162:169], v[94:97], v188, v189 op_sel_hi:[0,0,0]
	v_mfma_scale_f32_16x16x128_f8f6f4 v[90:93], v[18:25], v[162:169], v[90:93], v188, v189 op_sel_hi:[0,0,0]
	s_waitcnt lgkmcnt(4)
	v_mfma_scale_f32_16x16x128_f8f6f4 v[78:81], v[26:33], v[170:177], v[78:81], v188, v189 op_sel_hi:[0,0,0]
	v_mfma_scale_f32_16x16x128_f8f6f4 v[74:77], v[18:25], v[170:177], v[74:77], v188, v189 op_sel_hi:[0,0,0]
	s_waitcnt lgkmcnt(2)
	v_mfma_scale_f32_16x16x128_f8f6f4 v[62:65], v[26:33], v[194:201], v[62:65], v188, v189 op_sel_hi:[0,0,0]
	v_mfma_scale_f32_16x16x128_f8f6f4 v[58:61], v[18:25], v[194:201], v[58:61], v188, v189 op_sel_hi:[0,0,0]
	s_waitcnt lgkmcnt(0)
	v_mfma_scale_f32_16x16x128_f8f6f4 v[46:49], v[26:33], v[202:209], v[46:49], v188, v189 op_sel_hi:[0,0,0]
	v_mfma_scale_f32_16x16x128_f8f6f4 v[42:45], v[18:25], v[202:209], v[42:45], v188, v189 op_sel_hi:[0,0,0]
	v_mfma_scale_f32_16x16x128_f8f6f4 v[86:89], v[10:17], v[162:169], v[86:89], v188, v189 op_sel_hi:[0,0,0]
	v_mfma_scale_f32_16x16x128_f8f6f4 v[82:85], v[2:9], v[162:169], v[82:85], v188, v189 op_sel_hi:[0,0,0]
	v_mfma_scale_f32_16x16x128_f8f6f4 v[70:73], v[10:17], v[170:177], v[70:73], v188, v189 op_sel_hi:[0,0,0]
	v_mfma_scale_f32_16x16x128_f8f6f4 v[66:69], v[2:9], v[170:177], v[66:69], v188, v189 op_sel_hi:[0,0,0]
	v_mfma_scale_f32_16x16x128_f8f6f4 v[54:57], v[10:17], v[194:201], v[54:57], v188, v189 op_sel_hi:[0,0,0]
	v_mfma_scale_f32_16x16x128_f8f6f4 v[50:53], v[2:9], v[194:201], v[50:53], v188, v189 op_sel_hi:[0,0,0]
	v_mfma_scale_f32_16x16x128_f8f6f4 v[38:41], v[10:17], v[202:209], v[38:41], v188, v189 op_sel_hi:[0,0,0]
	v_mfma_scale_f32_16x16x128_f8f6f4 v[34:37], v[2:9], v[202:209], v[34:37], v188, v189 op_sel_hi:[0,0,0]
	s_barrier
	v_add_u32_e32 v0, 0x18000, v192
	ds_read_b128 v[26:29], v0
	ds_read_b128 v[30:33], v0 offset:1024
	ds_read_b128 v[18:21], v0 offset:2048
	ds_read_b128 v[22:25], v0 offset:3072
	v_add_u32_e32 v0, 0x1c000, v192
	ds_read_b128 v[10:13], v0
	ds_read_b128 v[14:17], v0 offset:1024
	ds_read_b128 v[2:5], v0 offset:2048
	ds_read_b128 v[6:9], v0 offset:3072
	ds_read_b128 v[162:165], v193 offset:32768
	ds_read_b128 v[166:169], v193 offset:33792
	ds_read_b128 v[170:173], v193 offset:34816
	ds_read_b128 v[174:177], v193 offset:35840
	ds_read_b128 v[194:197], v193 offset:36864
	ds_read_b128 v[198:201], v193 offset:37888
	ds_read_b128 v[202:205], v193 offset:38912
	ds_read_b128 v[206:209], v193 offset:39936
	s_add_u32 s36, s40, 0x20000
	s_addc_u32 s37, s41, 0
	s_mov_b32 s40, m0
	s_mov_b32 m0, s54
	s_nop 3
	global_load_lds_dwordx4 v184, s[36:37]
	s_mov_b32 m0, s40
	s_nop 0
	s_mov_b32 s40, m0
	s_mov_b32 m0, s55
	s_nop 3
	global_load_lds_dwordx4 v186, s[36:37]
	s_mov_b32 m0, s40
	s_waitcnt vmcnt(8)
	s_waitcnt lgkmcnt(0)
	s_barrier
	s_waitcnt lgkmcnt(6)
	v_mfma_scale_f32_16x16x128_f8f6f4 v[158:161], v[26:33], v[162:169], v[158:161], v188, v189 op_sel_hi:[0,0,0]
	v_mfma_scale_f32_16x16x128_f8f6f4 v[154:157], v[18:25], v[162:169], v[154:157], v188, v189 op_sel_hi:[0,0,0]
	s_waitcnt lgkmcnt(4)
	v_mfma_scale_f32_16x16x128_f8f6f4 v[142:145], v[26:33], v[170:177], v[142:145], v188, v189 op_sel_hi:[0,0,0]
	v_mfma_scale_f32_16x16x128_f8f6f4 v[138:141], v[18:25], v[170:177], v[138:141], v188, v189 op_sel_hi:[0,0,0]
	s_waitcnt lgkmcnt(2)
	v_mfma_scale_f32_16x16x128_f8f6f4 v[126:129], v[26:33], v[194:201], v[126:129], v188, v189 op_sel_hi:[0,0,0]
	v_mfma_scale_f32_16x16x128_f8f6f4 v[122:125], v[18:25], v[194:201], v[122:125], v188, v189 op_sel_hi:[0,0,0]
	s_waitcnt lgkmcnt(0)
	v_mfma_scale_f32_16x16x128_f8f6f4 v[110:113], v[26:33], v[202:209], v[110:113], v188, v189 op_sel_hi:[0,0,0]
	v_mfma_scale_f32_16x16x128_f8f6f4 v[106:109], v[18:25], v[202:209], v[106:109], v188, v189 op_sel_hi:[0,0,0]
	v_mfma_scale_f32_16x16x128_f8f6f4 v[150:153], v[10:17], v[162:169], v[150:153], v188, v189 op_sel_hi:[0,0,0]
	v_mfma_scale_f32_16x16x128_f8f6f4 v[146:149], v[2:9], v[162:169], v[146:149], v188, v189 op_sel_hi:[0,0,0]
	v_mfma_scale_f32_16x16x128_f8f6f4 v[134:137], v[10:17], v[170:177], v[134:137], v188, v189 op_sel_hi:[0,0,0]
	v_mfma_scale_f32_16x16x128_f8f6f4 v[130:133], v[2:9], v[170:177], v[130:133], v188, v189 op_sel_hi:[0,0,0]
	v_mfma_scale_f32_16x16x128_f8f6f4 v[118:121], v[10:17], v[194:201], v[118:121], v188, v189 op_sel_hi:[0,0,0]
	v_mfma_scale_f32_16x16x128_f8f6f4 v[114:117], v[2:9], v[194:201], v[114:117], v188, v189 op_sel_hi:[0,0,0]
	v_mfma_scale_f32_16x16x128_f8f6f4 v[102:105], v[10:17], v[202:209], v[102:105], v188, v189 op_sel_hi:[0,0,0]
	v_mfma_scale_f32_16x16x128_f8f6f4 v[98:101], v[2:9], v[202:209], v[98:101], v188, v189 op_sel_hi:[0,0,0]
	s_barrier
	ds_read_b128 v[162:165], v193 offset:49152
	ds_read_b128 v[166:169], v193 offset:50176
	ds_read_b128 v[170:173], v193 offset:51200
	ds_read_b128 v[174:177], v193 offset:52224
	ds_read_b128 v[194:197], v193 offset:53248
	ds_read_b128 v[198:201], v193 offset:54272
	ds_read_b128 v[202:205], v193 offset:55296
	ds_read_b128 v[206:209], v193 offset:56320
	s_add_u32 s36, s34, 0x80
	s_addc_u32 s37, s35, 0
	s_mov_b32 s40, m0
	s_mov_b32 m0, s58
	s_nop 3
	global_load_lds_dwordx4 v185, s[36:37]
	s_mov_b32 m0, s40
	s_add_u32 s34, s34, 0x20080
	s_mov_b32 s40, m0
	s_mov_b32 m0, s59
	s_nop 3
	global_load_lds_dwordx4 v187, s[36:37]
	s_mov_b32 m0, s40
	s_addc_u32 s35, s35, 0
	s_mov_b32 s36, m0
	s_mov_b32 m0, s62
	s_nop 3
	global_load_lds_dwordx4 v185, s[34:35]
	s_mov_b32 m0, s36
	s_nop 0
	s_mov_b32 s36, m0
	s_mov_b32 m0, s63
	s_nop 3
	global_load_lds_dwordx4 v187, s[34:35]
	s_mov_b32 m0, s36
	s_mov_b32 s34, m0
	s_mov_b32 m0, s60
	s_nop 3
	global_load_lds_dwordx4 v184, s[30:31]
	s_mov_b32 m0, s34
	s_nop 0
	s_mov_b32 s34, m0
	s_mov_b32 m0, s61
	s_nop 3
	global_load_lds_dwordx4 v186, s[30:31]
	s_mov_b32 m0, s34
	s_waitcnt vmcnt(8)
	s_waitcnt lgkmcnt(0)
	s_barrier
	s_waitcnt lgkmcnt(6)
	v_mfma_scale_f32_16x16x128_f8f6f4 v[94:97], v[26:33], v[162:169], v[94:97], v188, v189 op_sel_hi:[0,0,0]
	v_mfma_scale_f32_16x16x128_f8f6f4 v[90:93], v[18:25], v[162:169], v[90:93], v188, v189 op_sel_hi:[0,0,0]
	s_waitcnt lgkmcnt(4)
	v_mfma_scale_f32_16x16x128_f8f6f4 v[78:81], v[26:33], v[170:177], v[78:81], v188, v189 op_sel_hi:[0,0,0]
	v_mfma_scale_f32_16x16x128_f8f6f4 v[74:77], v[18:25], v[170:177], v[74:77], v188, v189 op_sel_hi:[0,0,0]
	s_waitcnt lgkmcnt(2)
	v_mfma_scale_f32_16x16x128_f8f6f4 v[62:65], v[26:33], v[194:201], v[62:65], v188, v189 op_sel_hi:[0,0,0]
	v_mfma_scale_f32_16x16x128_f8f6f4 v[58:61], v[18:25], v[194:201], v[58:61], v188, v189 op_sel_hi:[0,0,0]
	s_waitcnt lgkmcnt(0)
	v_mfma_scale_f32_16x16x128_f8f6f4 v[46:49], v[26:33], v[202:209], v[46:49], v188, v189 op_sel_hi:[0,0,0]
	v_mfma_scale_f32_16x16x128_f8f6f4 v[42:45], v[18:25], v[202:209], v[42:45], v188, v189 op_sel_hi:[0,0,0]
	v_mfma_scale_f32_16x16x128_f8f6f4 v[86:89], v[10:17], v[162:169], v[86:89], v188, v189 op_sel_hi:[0,0,0]
	v_mfma_scale_f32_16x16x128_f8f6f4 v[82:85], v[2:9], v[162:169], v[82:85], v188, v189 op_sel_hi:[0,0,0]
	v_mfma_scale_f32_16x16x128_f8f6f4 v[70:73], v[10:17], v[170:177], v[70:73], v188, v189 op_sel_hi:[0,0,0]
	v_mfma_scale_f32_16x16x128_f8f6f4 v[66:69], v[2:9], v[170:177], v[66:69], v188, v189 op_sel_hi:[0,0,0]
	v_mfma_scale_f32_16x16x128_f8f6f4 v[54:57], v[10:17], v[194:201], v[54:57], v188, v189 op_sel_hi:[0,0,0]
	v_mfma_scale_f32_16x16x128_f8f6f4 v[50:53], v[2:9], v[194:201], v[50:53], v188, v189 op_sel_hi:[0,0,0]
	v_mfma_scale_f32_16x16x128_f8f6f4 v[38:41], v[10:17], v[202:209], v[38:41], v188, v189 op_sel_hi:[0,0,0]
	v_mfma_scale_f32_16x16x128_f8f6f4 v[34:37], v[2:9], v[202:209], v[34:37], v188, v189 op_sel_hi:[0,0,0]
	s_barrier
	s_add_i32 s68, s68, 2
	s_add_u32 s66, s66, 0x100
	s_addc_u32 s67, s67, 0
	s_cmp_gt_u32 s68, 5
	s_mov_b64 s[36:37], s[26:27]
	s_cbranch_scc0 .LBB0_799
	s_and_b64 vcc, exec, s[16:17]
	s_cbranch_vccz .LBB0_802
	s_barrier
.LBB0_802:
	s_setprio 0
	s_cmp_gt_u32 s0, 7
	s_cselect_b64 s[34:35], -1, 0
	s_lshl_b32 s1, s0, 8
	s_and_b32 s26, s1, 0xfffffc00
	s_ashr_i32 s27, s26, 31
	s_and_b32 s19, s1, 0x300
	s_lshl_b64 s[30:31], s[26:27], 2
	v_or_b32_e32 v0, s19, v191
	s_add_u32 s30, s56, s30
	v_lshl_add_u32 v162, s28, 8, v190
	v_mov_b64_e32 v[18:19], s[12:13]
	s_movk_i32 s66, 0x1800
	s_addc_u32 s31, s57, s31
	v_lshlrev_b32_e32 v6, 2, v0
	v_mad_i64_i32 v[18:19], s[28:29], v162, s66, v[18:19]
	s_nop 15
	s_nop 3
	global_load_dwordx4 v[10:13], v6, s[30:31] offset:16
	global_load_dwordx4 v[14:17], v6, s[30:31]
	global_load_dwordx4 v[2:5], v6, s[30:31] offset:528
	s_nop 0
	global_load_dwordx4 v[6:9], v6, s[30:31] offset:512
	v_lshl_add_u64 v[18:19], s[26:27], 1, v[18:19]
	v_lshlrev_b32_e32 v0, 1, v0
	v_lshl_add_u64 v[18:19], v[18:19], 0, v[0:1]
	s_mov_b32 s37, 0
	global_load_dwordx4 v[24:27], v[18:19], off
	global_load_dwordx4 v[28:31], v[18:19], off offset:256
	s_mov_b32 s36, 0x18000
	v_lshl_add_u64 v[22:23], v[18:19], 0, s[36:37]
	global_load_dwordx4 v[164:167], v[22:23], off
	global_load_dwordx4 v[168:171], v[22:23], off offset:256
	v_ashrrev_i32_e32 v163, 31, v162
	s_cmp_gt_u32 s0, 3
	s_cselect_b64 s[28:29], -1, 0
	v_lshlrev_b64 v[20:21], 11, v[162:163]
	v_readlane_b32 s68, v253, 41
	v_lshl_add_u64 v[178:179], s[10:11], 0, v[20:21]
	v_readlane_b32 s69, v253, 42
	v_readlane_b32 s67, v253, 52
	s_not_b64 s[0:1], s[28:29]
	s_mov_b32 s70, 0xe000
	v_lshl_add_u64 v[20:21], v[178:179], 0, v[0:1]
	v_lshl_add_u32 v222, s86, 6, v213
	v_lshlrev_b32_e32 v222, 4, v222
	v_add_u32_e32 v222, 0x200c0, v222
	s_mov_b32 s30, 0xbfb8aa3b
	s_waitcnt vmcnt(4)
	v_pk_add_f32 v[158:159], v[158:159], v[14:15]
	v_pk_add_f32 v[160:161], v[160:161], v[16:17]
	v_pk_add_f32 v[154:155], v[154:155], v[10:11]
	v_pk_add_f32 v[156:157], v[156:157], v[12:13]
	v_pk_mul_f32 v[172:173], v[158:159], s[30:31] op_sel_hi:[1,0]
	v_pk_mul_f32 v[174:175], v[160:161], s[30:31] op_sel_hi:[1,0]
	v_pk_mul_f32 v[176:177], v[154:155], s[30:31] op_sel_hi:[1,0]
	v_pk_mul_f32 v[180:181], v[156:157], s[30:31] op_sel_hi:[1,0]
	v_exp_f32_e32 v172, v172
	v_exp_f32_e32 v173, v173
	v_exp_f32_e32 v174, v174
	v_exp_f32_e32 v175, v175
	v_exp_f32_e32 v176, v176
	v_exp_f32_e32 v177, v177
	v_exp_f32_e32 v180, v180
	v_exp_f32_e32 v181, v181
	v_pk_add_f32 v[172:173], v[172:173], 1.0 op_sel_hi:[1,0]
	v_pk_add_f32 v[174:175], v[174:175], 1.0 op_sel_hi:[1,0]
	v_pk_add_f32 v[176:177], v[176:177], 1.0 op_sel_hi:[1,0]
	v_pk_add_f32 v[180:181], v[180:181], 1.0 op_sel_hi:[1,0]
	v_rcp_f32_e32 v158, v172
	v_rcp_f32_e32 v159, v173
	v_rcp_f32_e32 v160, v174
	v_rcp_f32_e32 v161, v175
	v_rcp_f32_e32 v154, v176
	v_rcp_f32_e32 v155, v177
	v_rcp_f32_e32 v156, v180
	v_rcp_f32_e32 v157, v181
	v_pk_add_f32 v[150:151], v[150:151], v[6:7]
	v_pk_add_f32 v[152:153], v[152:153], v[8:9]
	v_pk_add_f32 v[146:147], v[146:147], v[2:3]
	v_pk_add_f32 v[148:149], v[148:149], v[4:5]
	v_pk_mul_f32 v[172:173], v[150:151], s[30:31] op_sel_hi:[1,0]
	v_pk_mul_f32 v[174:175], v[152:153], s[30:31] op_sel_hi:[1,0]
	v_pk_mul_f32 v[176:177], v[146:147], s[30:31] op_sel_hi:[1,0]
	v_pk_mul_f32 v[180:181], v[148:149], s[30:31] op_sel_hi:[1,0]
	v_exp_f32_e32 v172, v172
	v_exp_f32_e32 v173, v173
	v_exp_f32_e32 v174, v174
	v_exp_f32_e32 v175, v175
	v_exp_f32_e32 v176, v176
	v_exp_f32_e32 v177, v177
	v_exp_f32_e32 v180, v180
	v_exp_f32_e32 v181, v181
	v_pk_add_f32 v[172:173], v[172:173], 1.0 op_sel_hi:[1,0]
	v_pk_add_f32 v[174:175], v[174:175], 1.0 op_sel_hi:[1,0]
	v_pk_add_f32 v[176:177], v[176:177], 1.0 op_sel_hi:[1,0]
	v_pk_add_f32 v[180:181], v[180:181], 1.0 op_sel_hi:[1,0]
	v_rcp_f32_e32 v150, v172
	v_rcp_f32_e32 v151, v173
	v_rcp_f32_e32 v152, v174
	v_rcp_f32_e32 v153, v175
	v_rcp_f32_e32 v146, v176
	v_rcp_f32_e32 v147, v177
	v_rcp_f32_e32 v148, v180
	v_rcp_f32_e32 v149, v181
	v_pk_add_f32 v[142:143], v[142:143], v[14:15]
	v_pk_add_f32 v[144:145], v[144:145], v[16:17]
	v_pk_add_f32 v[138:139], v[138:139], v[10:11]
	v_pk_add_f32 v[140:141], v[140:141], v[12:13]
	v_pk_mul_f32 v[172:173], v[142:143], s[30:31] op_sel_hi:[1,0]
	v_pk_mul_f32 v[174:175], v[144:145], s[30:31] op_sel_hi:[1,0]
	v_pk_mul_f32 v[176:177], v[138:139], s[30:31] op_sel_hi:[1,0]
	v_pk_mul_f32 v[180:181], v[140:141], s[30:31] op_sel_hi:[1,0]
	v_exp_f32_e32 v172, v172
	v_exp_f32_e32 v173, v173
	v_exp_f32_e32 v174, v174
	v_exp_f32_e32 v175, v175
	v_exp_f32_e32 v176, v176
	v_exp_f32_e32 v177, v177
	v_exp_f32_e32 v180, v180
	v_exp_f32_e32 v181, v181
	v_pk_add_f32 v[172:173], v[172:173], 1.0 op_sel_hi:[1,0]
	v_pk_add_f32 v[174:175], v[174:175], 1.0 op_sel_hi:[1,0]
	v_pk_add_f32 v[176:177], v[176:177], 1.0 op_sel_hi:[1,0]
	v_pk_add_f32 v[180:181], v[180:181], 1.0 op_sel_hi:[1,0]
	v_rcp_f32_e32 v142, v172
	v_rcp_f32_e32 v143, v173
	v_rcp_f32_e32 v144, v174
	v_rcp_f32_e32 v145, v175
	v_rcp_f32_e32 v138, v176
	v_rcp_f32_e32 v139, v177
	v_rcp_f32_e32 v140, v180
	v_rcp_f32_e32 v141, v181
	v_pk_add_f32 v[134:135], v[134:135], v[6:7]
	v_pk_add_f32 v[136:137], v[136:137], v[8:9]
	v_pk_add_f32 v[130:131], v[130:131], v[2:3]
	v_pk_add_f32 v[132:133], v[132:133], v[4:5]
	v_pk_mul_f32 v[172:173], v[134:135], s[30:31] op_sel_hi:[1,0]
	v_pk_mul_f32 v[174:175], v[136:137], s[30:31] op_sel_hi:[1,0]
	v_pk_mul_f32 v[176:177], v[130:131], s[30:31] op_sel_hi:[1,0]
	v_pk_mul_f32 v[180:181], v[132:133], s[30:31] op_sel_hi:[1,0]
	v_exp_f32_e32 v172, v172
	v_exp_f32_e32 v173, v173
	v_exp_f32_e32 v174, v174
	v_exp_f32_e32 v175, v175
	v_exp_f32_e32 v176, v176
	v_exp_f32_e32 v177, v177
	v_exp_f32_e32 v180, v180
	v_exp_f32_e32 v181, v181
	v_pk_add_f32 v[172:173], v[172:173], 1.0 op_sel_hi:[1,0]
	v_pk_add_f32 v[174:175], v[174:175], 1.0 op_sel_hi:[1,0]
	v_pk_add_f32 v[176:177], v[176:177], 1.0 op_sel_hi:[1,0]
	v_pk_add_f32 v[180:181], v[180:181], 1.0 op_sel_hi:[1,0]
	v_rcp_f32_e32 v134, v172
	v_rcp_f32_e32 v135, v173
	v_rcp_f32_e32 v136, v174
	v_rcp_f32_e32 v137, v175
	v_rcp_f32_e32 v130, v176
	v_rcp_f32_e32 v131, v177
	v_rcp_f32_e32 v132, v180
	v_rcp_f32_e32 v133, v181
	v_pk_add_f32 v[126:127], v[126:127], v[14:15]
	v_pk_add_f32 v[128:129], v[128:129], v[16:17]
	v_pk_add_f32 v[122:123], v[122:123], v[10:11]
	v_pk_add_f32 v[124:125], v[124:125], v[12:13]
	v_pk_mul_f32 v[172:173], v[126:127], s[30:31] op_sel_hi:[1,0]
	v_pk_mul_f32 v[174:175], v[128:129], s[30:31] op_sel_hi:[1,0]
	v_pk_mul_f32 v[176:177], v[122:123], s[30:31] op_sel_hi:[1,0]
	v_pk_mul_f32 v[180:181], v[124:125], s[30:31] op_sel_hi:[1,0]
	v_exp_f32_e32 v172, v172
	v_exp_f32_e32 v173, v173
	v_exp_f32_e32 v174, v174
	v_exp_f32_e32 v175, v175
	v_exp_f32_e32 v176, v176
	v_exp_f32_e32 v177, v177
	v_exp_f32_e32 v180, v180
	v_exp_f32_e32 v181, v181
	v_pk_add_f32 v[172:173], v[172:173], 1.0 op_sel_hi:[1,0]
	v_pk_add_f32 v[174:175], v[174:175], 1.0 op_sel_hi:[1,0]
	v_pk_add_f32 v[176:177], v[176:177], 1.0 op_sel_hi:[1,0]
	v_pk_add_f32 v[180:181], v[180:181], 1.0 op_sel_hi:[1,0]
	v_rcp_f32_e32 v126, v172
	v_rcp_f32_e32 v127, v173
	v_rcp_f32_e32 v128, v174
	v_rcp_f32_e32 v129, v175
	v_rcp_f32_e32 v122, v176
	v_rcp_f32_e32 v123, v177
	v_rcp_f32_e32 v124, v180
	v_rcp_f32_e32 v125, v181
	v_pk_add_f32 v[118:119], v[118:119], v[6:7]
	v_pk_add_f32 v[120:121], v[120:121], v[8:9]
	v_pk_add_f32 v[114:115], v[114:115], v[2:3]
	v_pk_add_f32 v[116:117], v[116:117], v[4:5]
	v_pk_mul_f32 v[172:173], v[118:119], s[30:31] op_sel_hi:[1,0]
	v_pk_mul_f32 v[174:175], v[120:121], s[30:31] op_sel_hi:[1,0]
	v_pk_mul_f32 v[176:177], v[114:115], s[30:31] op_sel_hi:[1,0]
	v_pk_mul_f32 v[180:181], v[116:117], s[30:31] op_sel_hi:[1,0]
	v_exp_f32_e32 v172, v172
	v_exp_f32_e32 v173, v173
	v_exp_f32_e32 v174, v174
	v_exp_f32_e32 v175, v175
	v_exp_f32_e32 v176, v176
	v_exp_f32_e32 v177, v177
	v_exp_f32_e32 v180, v180
	v_exp_f32_e32 v181, v181
	v_pk_add_f32 v[172:173], v[172:173], 1.0 op_sel_hi:[1,0]
	v_pk_add_f32 v[174:175], v[174:175], 1.0 op_sel_hi:[1,0]
	v_pk_add_f32 v[176:177], v[176:177], 1.0 op_sel_hi:[1,0]
	v_pk_add_f32 v[180:181], v[180:181], 1.0 op_sel_hi:[1,0]
	v_rcp_f32_e32 v118, v172
	v_rcp_f32_e32 v119, v173
	v_rcp_f32_e32 v120, v174
	v_rcp_f32_e32 v121, v175
	v_rcp_f32_e32 v114, v176
	v_rcp_f32_e32 v115, v177
	v_rcp_f32_e32 v116, v180
	v_rcp_f32_e32 v117, v181
	v_pk_add_f32 v[110:111], v[110:111], v[14:15]
	v_pk_add_f32 v[112:113], v[112:113], v[16:17]
	v_pk_add_f32 v[106:107], v[106:107], v[10:11]
	v_pk_add_f32 v[108:109], v[108:109], v[12:13]
	v_pk_mul_f32 v[172:173], v[110:111], s[30:31] op_sel_hi:[1,0]
	v_pk_mul_f32 v[174:175], v[112:113], s[30:31] op_sel_hi:[1,0]
	v_pk_mul_f32 v[176:177], v[106:107], s[30:31] op_sel_hi:[1,0]
	v_pk_mul_f32 v[180:181], v[108:109], s[30:31] op_sel_hi:[1,0]
	v_exp_f32_e32 v172, v172
	v_exp_f32_e32 v173, v173
	v_exp_f32_e32 v174, v174
	v_exp_f32_e32 v175, v175
	v_exp_f32_e32 v176, v176
	v_exp_f32_e32 v177, v177
	v_exp_f32_e32 v180, v180
	v_exp_f32_e32 v181, v181
	v_pk_add_f32 v[172:173], v[172:173], 1.0 op_sel_hi:[1,0]
	v_pk_add_f32 v[174:175], v[174:175], 1.0 op_sel_hi:[1,0]
	v_pk_add_f32 v[176:177], v[176:177], 1.0 op_sel_hi:[1,0]
	v_pk_add_f32 v[180:181], v[180:181], 1.0 op_sel_hi:[1,0]
	v_rcp_f32_e32 v110, v172
	v_rcp_f32_e32 v111, v173
	v_rcp_f32_e32 v112, v174
	v_rcp_f32_e32 v113, v175
	v_rcp_f32_e32 v106, v176
	v_rcp_f32_e32 v107, v177
	v_rcp_f32_e32 v108, v180
	v_rcp_f32_e32 v109, v181
	v_pk_add_f32 v[102:103], v[102:103], v[6:7]
	v_pk_add_f32 v[104:105], v[104:105], v[8:9]
	v_pk_add_f32 v[98:99], v[98:99], v[2:3]
	v_pk_add_f32 v[100:101], v[100:101], v[4:5]
	v_pk_mul_f32 v[172:173], v[102:103], s[30:31] op_sel_hi:[1,0]
	v_pk_mul_f32 v[174:175], v[104:105], s[30:31] op_sel_hi:[1,0]
	v_pk_mul_f32 v[176:177], v[98:99], s[30:31] op_sel_hi:[1,0]
	v_pk_mul_f32 v[180:181], v[100:101], s[30:31] op_sel_hi:[1,0]
	v_exp_f32_e32 v172, v172
	v_exp_f32_e32 v173, v173
	v_exp_f32_e32 v174, v174
	v_exp_f32_e32 v175, v175
	v_exp_f32_e32 v176, v176
	v_exp_f32_e32 v177, v177
	v_exp_f32_e32 v180, v180
	v_exp_f32_e32 v181, v181
	v_pk_add_f32 v[172:173], v[172:173], 1.0 op_sel_hi:[1,0]
	v_pk_add_f32 v[174:175], v[174:175], 1.0 op_sel_hi:[1,0]
	v_pk_add_f32 v[176:177], v[176:177], 1.0 op_sel_hi:[1,0]
	v_pk_add_f32 v[180:181], v[180:181], 1.0 op_sel_hi:[1,0]
	v_rcp_f32_e32 v102, v172
	v_rcp_f32_e32 v103, v173
	v_rcp_f32_e32 v104, v174
	v_rcp_f32_e32 v105, v175
	v_rcp_f32_e32 v98, v176
	v_rcp_f32_e32 v99, v177
	v_rcp_f32_e32 v100, v180
	v_rcp_f32_e32 v101, v181
	v_pk_add_f32 v[94:95], v[94:95], v[14:15]
	v_pk_add_f32 v[96:97], v[96:97], v[16:17]
	v_pk_add_f32 v[90:91], v[90:91], v[10:11]
	v_pk_add_f32 v[92:93], v[92:93], v[12:13]
	v_pk_mul_f32 v[172:173], v[94:95], s[30:31] op_sel_hi:[1,0]
	v_pk_mul_f32 v[174:175], v[96:97], s[30:31] op_sel_hi:[1,0]
	v_pk_mul_f32 v[176:177], v[90:91], s[30:31] op_sel_hi:[1,0]
	v_pk_mul_f32 v[180:181], v[92:93], s[30:31] op_sel_hi:[1,0]
	v_exp_f32_e32 v172, v172
	v_exp_f32_e32 v173, v173
	v_exp_f32_e32 v174, v174
	v_exp_f32_e32 v175, v175
	v_exp_f32_e32 v176, v176
	v_exp_f32_e32 v177, v177
	v_exp_f32_e32 v180, v180
	v_exp_f32_e32 v181, v181
	v_pk_add_f32 v[172:173], v[172:173], 1.0 op_sel_hi:[1,0]
	v_pk_add_f32 v[174:175], v[174:175], 1.0 op_sel_hi:[1,0]
	v_pk_add_f32 v[176:177], v[176:177], 1.0 op_sel_hi:[1,0]
	v_pk_add_f32 v[180:181], v[180:181], 1.0 op_sel_hi:[1,0]
	v_rcp_f32_e32 v94, v172
	v_rcp_f32_e32 v95, v173
	v_rcp_f32_e32 v96, v174
	v_rcp_f32_e32 v97, v175
	v_rcp_f32_e32 v90, v176
	v_rcp_f32_e32 v91, v177
	v_rcp_f32_e32 v92, v180
	v_rcp_f32_e32 v93, v181
	v_pk_add_f32 v[86:87], v[86:87], v[6:7]
	v_pk_add_f32 v[88:89], v[88:89], v[8:9]
	v_pk_add_f32 v[82:83], v[82:83], v[2:3]
	v_pk_add_f32 v[84:85], v[84:85], v[4:5]
	v_pk_mul_f32 v[172:173], v[86:87], s[30:31] op_sel_hi:[1,0]
	v_pk_mul_f32 v[174:175], v[88:89], s[30:31] op_sel_hi:[1,0]
	v_pk_mul_f32 v[176:177], v[82:83], s[30:31] op_sel_hi:[1,0]
	v_pk_mul_f32 v[180:181], v[84:85], s[30:31] op_sel_hi:[1,0]
	v_exp_f32_e32 v172, v172
	v_exp_f32_e32 v173, v173
	v_exp_f32_e32 v174, v174
	v_exp_f32_e32 v175, v175
	v_exp_f32_e32 v176, v176
	v_exp_f32_e32 v177, v177
	v_exp_f32_e32 v180, v180
	v_exp_f32_e32 v181, v181
	v_pk_add_f32 v[172:173], v[172:173], 1.0 op_sel_hi:[1,0]
	v_pk_add_f32 v[174:175], v[174:175], 1.0 op_sel_hi:[1,0]
	v_pk_add_f32 v[176:177], v[176:177], 1.0 op_sel_hi:[1,0]
	v_pk_add_f32 v[180:181], v[180:181], 1.0 op_sel_hi:[1,0]
	v_rcp_f32_e32 v86, v172
	v_rcp_f32_e32 v87, v173
	v_rcp_f32_e32 v88, v174
	v_rcp_f32_e32 v89, v175
	v_rcp_f32_e32 v82, v176
	v_rcp_f32_e32 v83, v177
	v_rcp_f32_e32 v84, v180
	v_rcp_f32_e32 v85, v181
	v_pk_add_f32 v[78:79], v[78:79], v[14:15]
	v_pk_add_f32 v[80:81], v[80:81], v[16:17]
	v_pk_add_f32 v[74:75], v[74:75], v[10:11]
	v_pk_add_f32 v[76:77], v[76:77], v[12:13]
	v_pk_mul_f32 v[172:173], v[78:79], s[30:31] op_sel_hi:[1,0]
	v_pk_mul_f32 v[174:175], v[80:81], s[30:31] op_sel_hi:[1,0]
	v_pk_mul_f32 v[176:177], v[74:75], s[30:31] op_sel_hi:[1,0]
	v_pk_mul_f32 v[180:181], v[76:77], s[30:31] op_sel_hi:[1,0]
	v_exp_f32_e32 v172, v172
	v_exp_f32_e32 v173, v173
	v_exp_f32_e32 v174, v174
	v_exp_f32_e32 v175, v175
	v_exp_f32_e32 v176, v176
	v_exp_f32_e32 v177, v177
	v_exp_f32_e32 v180, v180
	v_exp_f32_e32 v181, v181
	v_pk_add_f32 v[172:173], v[172:173], 1.0 op_sel_hi:[1,0]
	v_pk_add_f32 v[174:175], v[174:175], 1.0 op_sel_hi:[1,0]
	v_pk_add_f32 v[176:177], v[176:177], 1.0 op_sel_hi:[1,0]
	v_pk_add_f32 v[180:181], v[180:181], 1.0 op_sel_hi:[1,0]
	v_rcp_f32_e32 v78, v172
	v_rcp_f32_e32 v79, v173
	v_rcp_f32_e32 v80, v174
	v_rcp_f32_e32 v81, v175
	v_rcp_f32_e32 v74, v176
	v_rcp_f32_e32 v75, v177
	v_rcp_f32_e32 v76, v180
	v_rcp_f32_e32 v77, v181
	v_pk_add_f32 v[70:71], v[70:71], v[6:7]
	v_pk_add_f32 v[72:73], v[72:73], v[8:9]
	v_pk_add_f32 v[66:67], v[66:67], v[2:3]
	v_pk_add_f32 v[68:69], v[68:69], v[4:5]
	v_pk_mul_f32 v[172:173], v[70:71], s[30:31] op_sel_hi:[1,0]
	v_pk_mul_f32 v[174:175], v[72:73], s[30:31] op_sel_hi:[1,0]
	v_pk_mul_f32 v[176:177], v[66:67], s[30:31] op_sel_hi:[1,0]
	v_pk_mul_f32 v[180:181], v[68:69], s[30:31] op_sel_hi:[1,0]
	v_exp_f32_e32 v172, v172
	v_exp_f32_e32 v173, v173
	v_exp_f32_e32 v174, v174
	v_exp_f32_e32 v175, v175
	v_exp_f32_e32 v176, v176
	v_exp_f32_e32 v177, v177
	v_exp_f32_e32 v180, v180
	v_exp_f32_e32 v181, v181
	v_pk_add_f32 v[172:173], v[172:173], 1.0 op_sel_hi:[1,0]
	v_pk_add_f32 v[174:175], v[174:175], 1.0 op_sel_hi:[1,0]
	v_pk_add_f32 v[176:177], v[176:177], 1.0 op_sel_hi:[1,0]
	v_pk_add_f32 v[180:181], v[180:181], 1.0 op_sel_hi:[1,0]
	v_rcp_f32_e32 v70, v172
	v_rcp_f32_e32 v71, v173
	v_rcp_f32_e32 v72, v174
	v_rcp_f32_e32 v73, v175
	v_rcp_f32_e32 v66, v176
	v_rcp_f32_e32 v67, v177
	v_rcp_f32_e32 v68, v180
	v_rcp_f32_e32 v69, v181
	v_pk_add_f32 v[62:63], v[62:63], v[14:15]
	v_pk_add_f32 v[64:65], v[64:65], v[16:17]
	v_pk_add_f32 v[58:59], v[58:59], v[10:11]
	v_pk_add_f32 v[60:61], v[60:61], v[12:13]
	v_pk_mul_f32 v[172:173], v[62:63], s[30:31] op_sel_hi:[1,0]
	v_pk_mul_f32 v[174:175], v[64:65], s[30:31] op_sel_hi:[1,0]
	v_pk_mul_f32 v[176:177], v[58:59], s[30:31] op_sel_hi:[1,0]
	v_pk_mul_f32 v[180:181], v[60:61], s[30:31] op_sel_hi:[1,0]
	v_exp_f32_e32 v172, v172
	v_exp_f32_e32 v173, v173
	v_exp_f32_e32 v174, v174
	v_exp_f32_e32 v175, v175
	v_exp_f32_e32 v176, v176
	v_exp_f32_e32 v177, v177
	v_exp_f32_e32 v180, v180
	v_exp_f32_e32 v181, v181
	v_pk_add_f32 v[172:173], v[172:173], 1.0 op_sel_hi:[1,0]
	v_pk_add_f32 v[174:175], v[174:175], 1.0 op_sel_hi:[1,0]
	v_pk_add_f32 v[176:177], v[176:177], 1.0 op_sel_hi:[1,0]
	v_pk_add_f32 v[180:181], v[180:181], 1.0 op_sel_hi:[1,0]
	v_rcp_f32_e32 v62, v172
	v_rcp_f32_e32 v63, v173
	v_rcp_f32_e32 v64, v174
	v_rcp_f32_e32 v65, v175
	v_rcp_f32_e32 v58, v176
	v_rcp_f32_e32 v59, v177
	v_rcp_f32_e32 v60, v180
	v_rcp_f32_e32 v61, v181
	v_pk_add_f32 v[54:55], v[54:55], v[6:7]
	v_pk_add_f32 v[56:57], v[56:57], v[8:9]
	v_pk_add_f32 v[50:51], v[50:51], v[2:3]
	v_pk_add_f32 v[52:53], v[52:53], v[4:5]
	v_pk_mul_f32 v[172:173], v[54:55], s[30:31] op_sel_hi:[1,0]
	v_pk_mul_f32 v[174:175], v[56:57], s[30:31] op_sel_hi:[1,0]
	v_pk_mul_f32 v[176:177], v[50:51], s[30:31] op_sel_hi:[1,0]
	v_pk_mul_f32 v[180:181], v[52:53], s[30:31] op_sel_hi:[1,0]
	v_exp_f32_e32 v172, v172
	v_exp_f32_e32 v173, v173
	v_exp_f32_e32 v174, v174
	v_exp_f32_e32 v175, v175
	v_exp_f32_e32 v176, v176
	v_exp_f32_e32 v177, v177
	v_exp_f32_e32 v180, v180
	v_exp_f32_e32 v181, v181
	v_pk_add_f32 v[172:173], v[172:173], 1.0 op_sel_hi:[1,0]
	v_pk_add_f32 v[174:175], v[174:175], 1.0 op_sel_hi:[1,0]
	v_pk_add_f32 v[176:177], v[176:177], 1.0 op_sel_hi:[1,0]
	v_pk_add_f32 v[180:181], v[180:181], 1.0 op_sel_hi:[1,0]
	v_rcp_f32_e32 v54, v172
	v_rcp_f32_e32 v55, v173
	v_rcp_f32_e32 v56, v174
	v_rcp_f32_e32 v57, v175
	v_rcp_f32_e32 v50, v176
	v_rcp_f32_e32 v51, v177
	v_rcp_f32_e32 v52, v180
	v_rcp_f32_e32 v53, v181
	v_pk_add_f32 v[46:47], v[46:47], v[14:15]
	v_pk_add_f32 v[48:49], v[48:49], v[16:17]
	v_pk_add_f32 v[42:43], v[42:43], v[10:11]
	v_pk_add_f32 v[44:45], v[44:45], v[12:13]
	v_pk_mul_f32 v[172:173], v[46:47], s[30:31] op_sel_hi:[1,0]
	v_pk_mul_f32 v[174:175], v[48:49], s[30:31] op_sel_hi:[1,0]
	v_pk_mul_f32 v[176:177], v[42:43], s[30:31] op_sel_hi:[1,0]
	v_pk_mul_f32 v[180:181], v[44:45], s[30:31] op_sel_hi:[1,0]
	v_exp_f32_e32 v172, v172
	v_exp_f32_e32 v173, v173
	v_exp_f32_e32 v174, v174
	v_exp_f32_e32 v175, v175
	v_exp_f32_e32 v176, v176
	v_exp_f32_e32 v177, v177
	v_exp_f32_e32 v180, v180
	v_exp_f32_e32 v181, v181
	v_pk_add_f32 v[172:173], v[172:173], 1.0 op_sel_hi:[1,0]
	v_pk_add_f32 v[174:175], v[174:175], 1.0 op_sel_hi:[1,0]
	v_pk_add_f32 v[176:177], v[176:177], 1.0 op_sel_hi:[1,0]
	v_pk_add_f32 v[180:181], v[180:181], 1.0 op_sel_hi:[1,0]
	v_rcp_f32_e32 v46, v172
	v_rcp_f32_e32 v47, v173
	v_rcp_f32_e32 v48, v174
	v_rcp_f32_e32 v49, v175
	v_rcp_f32_e32 v42, v176
	v_rcp_f32_e32 v43, v177
	v_rcp_f32_e32 v44, v180
	v_rcp_f32_e32 v45, v181
	v_pk_add_f32 v[38:39], v[38:39], v[6:7]
	v_pk_add_f32 v[40:41], v[40:41], v[8:9]
	v_pk_add_f32 v[34:35], v[34:35], v[2:3]
	v_pk_add_f32 v[36:37], v[36:37], v[4:5]
	v_pk_mul_f32 v[172:173], v[38:39], s[30:31] op_sel_hi:[1,0]
	v_pk_mul_f32 v[174:175], v[40:41], s[30:31] op_sel_hi:[1,0]
	v_pk_mul_f32 v[176:177], v[34:35], s[30:31] op_sel_hi:[1,0]
	v_pk_mul_f32 v[180:181], v[36:37], s[30:31] op_sel_hi:[1,0]
	v_exp_f32_e32 v172, v172
	v_exp_f32_e32 v173, v173
	v_exp_f32_e32 v174, v174
	v_exp_f32_e32 v175, v175
	v_exp_f32_e32 v176, v176
	v_exp_f32_e32 v177, v177
	v_exp_f32_e32 v180, v180
	v_exp_f32_e32 v181, v181
	v_pk_add_f32 v[172:173], v[172:173], 1.0 op_sel_hi:[1,0]
	v_pk_add_f32 v[174:175], v[174:175], 1.0 op_sel_hi:[1,0]
	v_pk_add_f32 v[176:177], v[176:177], 1.0 op_sel_hi:[1,0]
	v_pk_add_f32 v[180:181], v[180:181], 1.0 op_sel_hi:[1,0]
	v_rcp_f32_e32 v38, v172
	v_rcp_f32_e32 v39, v173
	v_rcp_f32_e32 v40, v174
	v_rcp_f32_e32 v41, v175
	v_rcp_f32_e32 v34, v176
	v_rcp_f32_e32 v35, v177
	v_rcp_f32_e32 v36, v180
	v_rcp_f32_e32 v37, v181
	v_mov_b32_e32 v2, 0
	v_mov_b32_e32 v3, 0
	v_mov_b32_e32 v4, 0
	v_mov_b32_e32 v5, 0
	v_mov_b32_e32 v6, 0
	v_mov_b32_e32 v7, 0
	v_mov_b32_e32 v8, 0
	v_mov_b32_e32 v9, 0
	s_and_b64 vcc, exec, s[0:1]
	s_cbranch_vccnz .Lmg_m0
	v_mov_b32_e32 v2, v224
	v_mov_b32_e32 v3, v225
	v_mov_b32_e32 v4, v226
	v_mov_b32_e32 v5, v227
	v_mov_b32_e32 v6, v228
	v_mov_b32_e32 v7, v229
	v_mov_b32_e32 v8, v230
	v_mov_b32_e32 v9, v231

.Lprio_909:
	v_add_u32_e32 v78, 0x10000, v161
	v_add_u32_e32 v154, 0x14000, v161
	ds_read_b128 v[66:69], v78
	ds_read_b128 v[70:73], v78 offset:1024
	ds_read_b128 v[74:77], v78 offset:2048
	ds_read_b128 v[78:81], v78 offset:3072
	ds_read_b128 v[146:149], v154
	ds_read_b128 v[150:153], v154 offset:1024
	ds_read_b128 v[164:167], v154 offset:2048
	ds_read_b128 v[168:171], v154 offset:3072
	s_add_u32 s36, s34, 0x100
	s_addc_u32 s37, s35, 0
	s_cmp_eq_u32 s73, 12
	s_cselect_b32 s44, s29, s36
	s_cselect_b32 s45, s23, s37
	s_cselect_b32 s42, s70, s71
	s_cselect_b32 s43, s21, s72
	s_add_u32 s40, s44, 0x80
	s_addc_u32 s41, s45, 0
	ds_read_b128 v[172:175], v162
	ds_read_b128 v[176:179], v162 offset:1024
	ds_read_b128 v[180:183], v162 offset:2048
	ds_read_b128 v[184:187], v162 offset:3072
	ds_read_b128 v[188:191], v162 offset:4096
	ds_read_b128 v[192:195], v162 offset:5120
	ds_read_b128 v[196:199], v162 offset:6144
	ds_read_b128 v[200:203], v162 offset:7168
	s_add_u32 s34, s34, 0x40080
	s_addc_u32 s35, s35, 0
	s_mov_b32 s74, m0
	s_mov_b32 m0, s68
	s_nop 3
	global_load_lds_dwordx4 v0, s[34:35]
	s_mov_b32 m0, s74
	s_add_i32 s74, s31, 0xe000
	s_mov_b32 s75, m0
	s_mov_b32 m0, s74
	s_nop 3
	global_load_lds_dwordx4 v157, s[34:35]
	s_mov_b32 m0, s75
	s_waitcnt vmcnt(8)
	s_waitcnt lgkmcnt(0)
	s_barrier
	s_waitcnt lgkmcnt(7)
	v_mfma_f32_16x16x32_bf16 v[142:145], v[66:69], v[172:175], v[142:145]
	v_mfma_f32_16x16x32_bf16 v[138:141], v[74:77], v[172:175], v[138:141]
	s_waitcnt lgkmcnt(5)
	v_mfma_f32_16x16x32_bf16 v[126:129], v[66:69], v[180:183], v[126:129]
	v_mfma_f32_16x16x32_bf16 v[122:125], v[74:77], v[180:183], v[122:125]
	s_waitcnt lgkmcnt(3)
	v_mfma_f32_16x16x32_bf16 v[110:113], v[66:69], v[188:191], v[110:113]
	v_mfma_f32_16x16x32_bf16 v[106:109], v[74:77], v[188:191], v[106:109]
	s_waitcnt lgkmcnt(1)
	v_mfma_f32_16x16x32_bf16 v[94:97], v[66:69], v[196:199], v[94:97]
	v_mfma_f32_16x16x32_bf16 v[90:93], v[74:77], v[196:199], v[90:93]
	v_mfma_f32_16x16x32_bf16 v[142:145], v[70:73], v[176:179], v[142:145]
	v_mfma_f32_16x16x32_bf16 v[138:141], v[78:81], v[176:179], v[138:141]
	v_mfma_f32_16x16x32_bf16 v[126:129], v[70:73], v[184:187], v[126:129]
	v_mfma_f32_16x16x32_bf16 v[122:125], v[78:81], v[184:187], v[122:125]
	v_mfma_f32_16x16x32_bf16 v[110:113], v[70:73], v[192:195], v[110:113]
	v_mfma_f32_16x16x32_bf16 v[106:109], v[78:81], v[192:195], v[106:109]
	s_waitcnt lgkmcnt(0)
	v_mfma_f32_16x16x32_bf16 v[94:97], v[70:73], v[200:203], v[94:97]
	v_mfma_f32_16x16x32_bf16 v[90:93], v[78:81], v[200:203], v[90:93]
	v_mfma_f32_16x16x32_bf16 v[134:137], v[146:149], v[172:175], v[134:137]
	v_mfma_f32_16x16x32_bf16 v[130:133], v[164:167], v[172:175], v[130:133]
	v_mfma_f32_16x16x32_bf16 v[118:121], v[146:149], v[180:183], v[118:121]
	v_mfma_f32_16x16x32_bf16 v[114:117], v[164:167], v[180:183], v[114:117]
	v_mfma_f32_16x16x32_bf16 v[102:105], v[146:149], v[188:191], v[102:105]
	v_mfma_f32_16x16x32_bf16 v[98:101], v[164:167], v[188:191], v[98:101]
	v_mfma_f32_16x16x32_bf16 v[86:89], v[146:149], v[196:199], v[86:89]
	v_mfma_f32_16x16x32_bf16 v[82:85], v[164:167], v[196:199], v[82:85]
	v_mfma_f32_16x16x32_bf16 v[134:137], v[150:153], v[176:179], v[134:137]
	v_mfma_f32_16x16x32_bf16 v[130:133], v[168:171], v[176:179], v[130:133]
	v_mfma_f32_16x16x32_bf16 v[118:121], v[150:153], v[184:187], v[118:121]
	v_mfma_f32_16x16x32_bf16 v[114:117], v[168:171], v[184:187], v[114:117]
	v_mfma_f32_16x16x32_bf16 v[102:105], v[150:153], v[192:195], v[102:105]
	v_mfma_f32_16x16x32_bf16 v[98:101], v[168:171], v[192:195], v[98:101]
	v_mfma_f32_16x16x32_bf16 v[86:89], v[150:153], v[200:203], v[86:89]
	v_mfma_f32_16x16x32_bf16 v[82:85], v[168:171], v[200:203], v[82:85]
	s_barrier
	ds_read_b128 v[172:175], v162 offset:16384
	ds_read_b128 v[176:179], v162 offset:17408
	ds_read_b128 v[180:183], v162 offset:18432
	ds_read_b128 v[184:187], v162 offset:19456
	ds_read_b128 v[188:191], v162 offset:20480
	ds_read_b128 v[192:195], v162 offset:21504
	ds_read_b128 v[196:199], v162 offset:22528
	ds_read_b128 v[200:203], v162 offset:23552
	s_mov_b32 s34, m0
	s_mov_b32 m0, s53
	s_nop 3
	global_load_lds_dwordx4 v156, s[42:43]
	s_mov_b32 m0, s34
	s_nop 0
	s_mov_b32 s34, m0
	s_mov_b32 m0, s54
	s_nop 3
	global_load_lds_dwordx4 v158, s[42:43]
	s_mov_b32 m0, s34
	s_add_u32 s34, s42, 0x40000
	s_addc_u32 s35, s43, 0
	s_mov_b32 s74, m0
	s_mov_b32 m0, s55
	s_nop 3
	global_load_lds_dwordx4 v156, s[34:35]
	s_mov_b32 m0, s74
	s_nop 0
	s_mov_b32 s74, m0
	s_mov_b32 m0, s56
	s_nop 3
	global_load_lds_dwordx4 v158, s[34:35]
	s_mov_b32 m0, s74
	s_mov_b32 s34, m0
	s_mov_b32 m0, s31
	s_nop 3
	global_load_lds_dwordx4 v0, s[44:45]
	s_mov_b32 m0, s34
	s_nop 0
	s_mov_b32 s34, m0
	s_mov_b32 m0, s57
	s_nop 3
	global_load_lds_dwordx4 v157, s[44:45]
	s_mov_b32 m0, s34
	s_waitcnt vmcnt(8)
	s_waitcnt lgkmcnt(0)
	s_barrier
	s_waitcnt lgkmcnt(7)
	v_mfma_f32_16x16x32_bf16 v[62:65], v[66:69], v[172:175], v[62:65]
	v_mfma_f32_16x16x32_bf16 v[58:61], v[74:77], v[172:175], v[58:61]
	s_waitcnt lgkmcnt(5)
	v_mfma_f32_16x16x32_bf16 v[46:49], v[66:69], v[180:183], v[46:49]
	v_mfma_f32_16x16x32_bf16 v[42:45], v[74:77], v[180:183], v[42:45]
	s_waitcnt lgkmcnt(3)
	v_mfma_f32_16x16x32_bf16 v[30:33], v[66:69], v[188:191], v[30:33]
	v_mfma_f32_16x16x32_bf16 v[26:29], v[74:77], v[188:191], v[26:29]
	s_waitcnt lgkmcnt(1)
	v_mfma_f32_16x16x32_bf16 v[22:25], v[66:69], v[196:199], v[22:25]
	v_mfma_f32_16x16x32_bf16 v[18:21], v[74:77], v[196:199], v[18:21]
	v_mfma_f32_16x16x32_bf16 v[62:65], v[70:73], v[176:179], v[62:65]
	v_mfma_f32_16x16x32_bf16 v[58:61], v[78:81], v[176:179], v[58:61]
	v_mfma_f32_16x16x32_bf16 v[46:49], v[70:73], v[184:187], v[46:49]
	v_mfma_f32_16x16x32_bf16 v[42:45], v[78:81], v[184:187], v[42:45]
	v_mfma_f32_16x16x32_bf16 v[30:33], v[70:73], v[192:195], v[30:33]
	v_mfma_f32_16x16x32_bf16 v[26:29], v[78:81], v[192:195], v[26:29]
	s_waitcnt lgkmcnt(0)
	v_mfma_f32_16x16x32_bf16 v[22:25], v[70:73], v[200:203], v[22:25]
	v_mfma_f32_16x16x32_bf16 v[18:21], v[78:81], v[200:203], v[18:21]
	v_mfma_f32_16x16x32_bf16 v[54:57], v[146:149], v[172:175], v[54:57]
	v_mfma_f32_16x16x32_bf16 v[50:53], v[164:167], v[172:175], v[50:53]
	v_mfma_f32_16x16x32_bf16 v[38:41], v[146:149], v[180:183], v[38:41]
	v_mfma_f32_16x16x32_bf16 v[34:37], v[164:167], v[180:183], v[34:37]
	v_mfma_f32_16x16x32_bf16 v[14:17], v[146:149], v[188:191], v[14:17]
	v_mfma_f32_16x16x32_bf16 v[10:13], v[164:167], v[188:191], v[10:13]
	v_mfma_f32_16x16x32_bf16 v[6:9], v[146:149], v[196:199], v[6:9]
	v_mfma_f32_16x16x32_bf16 v[2:5], v[164:167], v[196:199], v[2:5]
	v_mfma_f32_16x16x32_bf16 v[54:57], v[150:153], v[176:179], v[54:57]
	v_mfma_f32_16x16x32_bf16 v[50:53], v[168:171], v[176:179], v[50:53]
	v_mfma_f32_16x16x32_bf16 v[38:41], v[150:153], v[184:187], v[38:41]
	v_mfma_f32_16x16x32_bf16 v[34:37], v[168:171], v[184:187], v[34:37]
	v_mfma_f32_16x16x32_bf16 v[14:17], v[150:153], v[192:195], v[14:17]
	v_mfma_f32_16x16x32_bf16 v[10:13], v[168:171], v[192:195], v[10:13]
	v_mfma_f32_16x16x32_bf16 v[6:9], v[150:153], v[200:203], v[6:9]
	v_mfma_f32_16x16x32_bf16 v[2:5], v[168:171], v[200:203], v[2:5]
	s_barrier
	v_add_u32_e32 v78, 0x18000, v161
	v_add_u32_e32 v154, 0x1c000, v161
	ds_read_b128 v[66:69], v78
	ds_read_b128 v[70:73], v78 offset:1024
	ds_read_b128 v[74:77], v78 offset:2048
	ds_read_b128 v[78:81], v78 offset:3072
	ds_read_b128 v[146:149], v154
	ds_read_b128 v[150:153], v154 offset:1024
	ds_read_b128 v[164:167], v154 offset:2048
	ds_read_b128 v[168:171], v154 offset:3072
	ds_read_b128 v[172:175], v162 offset:32768
	ds_read_b128 v[176:179], v162 offset:33792
	ds_read_b128 v[180:183], v162 offset:34816
	ds_read_b128 v[184:187], v162 offset:35840
	ds_read_b128 v[188:191], v162 offset:36864
	ds_read_b128 v[192:195], v162 offset:37888
	ds_read_b128 v[196:199], v162 offset:38912
	ds_read_b128 v[200:203], v162 offset:39936
	s_add_u32 s34, s44, 0x40000
	s_addc_u32 s35, s45, 0
	s_mov_b32 s44, m0
	s_mov_b32 m0, s58
	s_nop 3
	global_load_lds_dwordx4 v0, s[34:35]
	s_mov_b32 m0, s44
	s_nop 0
	s_mov_b32 s44, m0
	s_mov_b32 m0, s59
	s_nop 3
	global_load_lds_dwordx4 v157, s[34:35]
	s_mov_b32 m0, s44
	s_waitcnt vmcnt(8)
	s_waitcnt lgkmcnt(0)
	s_barrier
	s_waitcnt lgkmcnt(7)
	v_mfma_f32_16x16x32_bf16 v[142:145], v[66:69], v[172:175], v[142:145]
	v_mfma_f32_16x16x32_bf16 v[138:141], v[74:77], v[172:175], v[138:141]
	s_waitcnt lgkmcnt(5)
	v_mfma_f32_16x16x32_bf16 v[126:129], v[66:69], v[180:183], v[126:129]
	v_mfma_f32_16x16x32_bf16 v[122:125], v[74:77], v[180:183], v[122:125]
	s_waitcnt lgkmcnt(3)
	v_mfma_f32_16x16x32_bf16 v[110:113], v[66:69], v[188:191], v[110:113]
	v_mfma_f32_16x16x32_bf16 v[106:109], v[74:77], v[188:191], v[106:109]
	s_waitcnt lgkmcnt(1)
	v_mfma_f32_16x16x32_bf16 v[94:97], v[66:69], v[196:199], v[94:97]
	v_mfma_f32_16x16x32_bf16 v[90:93], v[74:77], v[196:199], v[90:93]
	v_mfma_f32_16x16x32_bf16 v[142:145], v[70:73], v[176:179], v[142:145]
	v_mfma_f32_16x16x32_bf16 v[138:141], v[78:81], v[176:179], v[138:141]
	v_mfma_f32_16x16x32_bf16 v[126:129], v[70:73], v[184:187], v[126:129]
	v_mfma_f32_16x16x32_bf16 v[122:125], v[78:81], v[184:187], v[122:125]
	v_mfma_f32_16x16x32_bf16 v[110:113], v[70:73], v[192:195], v[110:113]
	v_mfma_f32_16x16x32_bf16 v[106:109], v[78:81], v[192:195], v[106:109]
	s_waitcnt lgkmcnt(0)
	v_mfma_f32_16x16x32_bf16 v[94:97], v[70:73], v[200:203], v[94:97]
	v_mfma_f32_16x16x32_bf16 v[90:93], v[78:81], v[200:203], v[90:93]
	v_mfma_f32_16x16x32_bf16 v[134:137], v[146:149], v[172:175], v[134:137]
	v_mfma_f32_16x16x32_bf16 v[130:133], v[164:167], v[172:175], v[130:133]
	v_mfma_f32_16x16x32_bf16 v[118:121], v[146:149], v[180:183], v[118:121]
	v_mfma_f32_16x16x32_bf16 v[114:117], v[164:167], v[180:183], v[114:117]
	v_mfma_f32_16x16x32_bf16 v[102:105], v[146:149], v[188:191], v[102:105]
	v_mfma_f32_16x16x32_bf16 v[98:101], v[164:167], v[188:191], v[98:101]
	v_mfma_f32_16x16x32_bf16 v[86:89], v[146:149], v[196:199], v[86:89]
	v_mfma_f32_16x16x32_bf16 v[82:85], v[164:167], v[196:199], v[82:85]
	v_mfma_f32_16x16x32_bf16 v[134:137], v[150:153], v[176:179], v[134:137]
	v_mfma_f32_16x16x32_bf16 v[130:133], v[168:171], v[176:179], v[130:133]
	v_mfma_f32_16x16x32_bf16 v[118:121], v[150:153], v[184:187], v[118:121]
	v_mfma_f32_16x16x32_bf16 v[114:117], v[168:171], v[184:187], v[114:117]
	v_mfma_f32_16x16x32_bf16 v[102:105], v[150:153], v[192:195], v[102:105]
	v_mfma_f32_16x16x32_bf16 v[98:101], v[168:171], v[192:195], v[98:101]
	v_mfma_f32_16x16x32_bf16 v[86:89], v[150:153], v[200:203], v[86:89]
	v_mfma_f32_16x16x32_bf16 v[82:85], v[168:171], v[200:203], v[82:85]
	s_barrier
	ds_read_b128 v[172:175], v162 offset:49152
	ds_read_b128 v[176:179], v162 offset:50176
	ds_read_b128 v[180:183], v162 offset:51200
	ds_read_b128 v[184:187], v162 offset:52224
	ds_read_b128 v[188:191], v162 offset:53248
	ds_read_b128 v[192:195], v162 offset:54272
	ds_read_b128 v[196:199], v162 offset:55296
	ds_read_b128 v[200:203], v162 offset:56320
	s_add_u32 s34, s42, 0x80
	s_addc_u32 s35, s43, 0
	s_mov_b32 s44, m0
	s_mov_b32 m0, s62
	s_nop 3
	global_load_lds_dwordx4 v156, s[34:35]
	s_mov_b32 m0, s44
	s_nop 0
	s_mov_b32 s44, m0
	s_mov_b32 m0, s63
	s_nop 3
	global_load_lds_dwordx4 v158, s[34:35]
	s_mov_b32 m0, s44
	s_add_u32 s34, s42, 0x40080
	s_addc_u32 s35, s43, 0
	s_mov_b32 s42, m0
	s_mov_b32 m0, s66
	s_nop 3
	global_load_lds_dwordx4 v156, s[34:35]
	s_mov_b32 m0, s42
	s_nop 0
	s_mov_b32 s42, m0
	s_mov_b32 m0, s67
	s_nop 3
	global_load_lds_dwordx4 v158, s[34:35]
	s_mov_b32 m0, s42
	s_mov_b32 s34, m0
	s_mov_b32 m0, s64
	s_nop 3
	global_load_lds_dwordx4 v0, s[40:41]
	s_mov_b32 m0, s34
	s_nop 0
	s_mov_b32 s34, m0
	s_mov_b32 m0, s65
	s_nop 3
	global_load_lds_dwordx4 v157, s[40:41]
	s_mov_b32 m0, s34
	s_waitcnt vmcnt(8)
	s_waitcnt lgkmcnt(0)
	s_barrier
	s_waitcnt lgkmcnt(7)
	v_mfma_f32_16x16x32_bf16 v[62:65], v[66:69], v[172:175], v[62:65]
	v_mfma_f32_16x16x32_bf16 v[58:61], v[74:77], v[172:175], v[58:61]
	s_waitcnt lgkmcnt(5)
	v_mfma_f32_16x16x32_bf16 v[46:49], v[66:69], v[180:183], v[46:49]
	v_mfma_f32_16x16x32_bf16 v[42:45], v[74:77], v[180:183], v[42:45]
	s_waitcnt lgkmcnt(3)
	v_mfma_f32_16x16x32_bf16 v[30:33], v[66:69], v[188:191], v[30:33]
	v_mfma_f32_16x16x32_bf16 v[26:29], v[74:77], v[188:191], v[26:29]
	s_waitcnt lgkmcnt(1)
	v_mfma_f32_16x16x32_bf16 v[22:25], v[66:69], v[196:199], v[22:25]
	v_mfma_f32_16x16x32_bf16 v[18:21], v[74:77], v[196:199], v[18:21]
	v_mfma_f32_16x16x32_bf16 v[62:65], v[70:73], v[176:179], v[62:65]
	v_mfma_f32_16x16x32_bf16 v[58:61], v[78:81], v[176:179], v[58:61]
	v_mfma_f32_16x16x32_bf16 v[46:49], v[70:73], v[184:187], v[46:49]
	v_mfma_f32_16x16x32_bf16 v[42:45], v[78:81], v[184:187], v[42:45]
	v_mfma_f32_16x16x32_bf16 v[30:33], v[70:73], v[192:195], v[30:33]
	v_mfma_f32_16x16x32_bf16 v[26:29], v[78:81], v[192:195], v[26:29]
	s_waitcnt lgkmcnt(0)
	v_mfma_f32_16x16x32_bf16 v[22:25], v[70:73], v[200:203], v[22:25]
	v_mfma_f32_16x16x32_bf16 v[18:21], v[78:81], v[200:203], v[18:21]
	v_mfma_f32_16x16x32_bf16 v[54:57], v[146:149], v[172:175], v[54:57]
	v_mfma_f32_16x16x32_bf16 v[50:53], v[164:167], v[172:175], v[50:53]
	v_mfma_f32_16x16x32_bf16 v[38:41], v[146:149], v[180:183], v[38:41]
	v_mfma_f32_16x16x32_bf16 v[34:37], v[164:167], v[180:183], v[34:37]
	v_mfma_f32_16x16x32_bf16 v[14:17], v[146:149], v[188:191], v[14:17]
	v_mfma_f32_16x16x32_bf16 v[10:13], v[164:167], v[188:191], v[10:13]
	v_mfma_f32_16x16x32_bf16 v[6:9], v[146:149], v[196:199], v[6:9]
	v_mfma_f32_16x16x32_bf16 v[2:5], v[164:167], v[196:199], v[2:5]
	v_mfma_f32_16x16x32_bf16 v[54:57], v[150:153], v[176:179], v[54:57]
	v_mfma_f32_16x16x32_bf16 v[50:53], v[168:171], v[176:179], v[50:53]
	v_mfma_f32_16x16x32_bf16 v[38:41], v[150:153], v[184:187], v[38:41]
	v_mfma_f32_16x16x32_bf16 v[34:37], v[168:171], v[184:187], v[34:37]
	v_mfma_f32_16x16x32_bf16 v[14:17], v[150:153], v[192:195], v[14:17]
	v_mfma_f32_16x16x32_bf16 v[10:13], v[168:171], v[192:195], v[10:13]
	v_mfma_f32_16x16x32_bf16 v[6:9], v[150:153], v[200:203], v[6:9]
	v_mfma_f32_16x16x32_bf16 v[2:5], v[168:171], v[200:203], v[2:5]
	s_barrier
	s_add_i32 s73, s73, 2
	s_add_u32 s71, s71, 0x100
	s_addc_u32 s72, s72, 0
	s_cmp_gt_u32 s73, 13
	s_mov_b64 s[34:35], s[36:37]
	s_cbranch_scc0 .LBB0_909
	s_and_b64 vcc, exec, s[16:17]
	s_cbranch_vccz .LBB0_912
	s_barrier
.LBB0_912:
	s_setprio 0
	v_readlane_b32 s72, v253, 37
	v_readlane_b32 s74, v253, 39
	v_readlane_b32 s44, v253, 43
	s_mov_b64 s[36:37], 0xc800
	s_cmpk_gt_i32 s30, 0xff
	s_mov_b64 s[34:35], s[18:19]
	v_readlane_b32 s73, v253, 38
	v_readlane_b32 s75, v253, 40
	v_readlane_b32 s45, v253, 44
	v_readlane_b32 s71, v253, 51
	s_mov_b32 s70, 0xe000
	s_cbranch_scc1 .LBB0_914
	s_ashr_i32 s21, s30, 31
	s_lshr_b32 s21, s21, 27
	s_add_i32 s21, s30, s21
	s_ashr_i32 s21, s21, 5
	s_mul_i32 s34, s21, 6
	s_ashr_i32 s35, s34, 31
	s_lshl_b64 s[34:35], s[34:35], 10
	s_add_u32 s36, s34, 0x800
	s_addc_u32 s37, s35, 0
	s_mov_b64 s[34:35], s[8:9]

.Lprio_1226:
	v_add_u32_e32 v2, 0x10000, v171
	v_add_u32_e32 v6, 0x14000, v171
	ds_read_b128 v[26:29], v2
	ds_read_b128 v[30:33], v2 offset:1024
	ds_read_b128 v[18:21], v2 offset:2048
	ds_read_b128 v[22:25], v2 offset:3072
	ds_read_b128 v[10:13], v6
	ds_read_b128 v[14:17], v6 offset:1024
	ds_read_b128 v[2:5], v6 offset:2048
	ds_read_b128 v[6:9], v6 offset:3072
	s_add_u32 s26, s34, 0x100
	s_addc_u32 s27, s35, 0
	s_cmp_eq_u32 s64, 4
	s_cselect_b32 s36, s17, s26
	s_cselect_b32 s37, s14, s27
	s_cselect_b32 s30, s61, s62
	s_cselect_b32 s31, s13, s63
	s_add_u32 s28, s36, 0x80
	s_addc_u32 s29, s37, 0
	ds_read_b128 v[174:177], v172
	ds_read_b128 v[178:181], v172 offset:1024
	ds_read_b128 v[182:185], v172 offset:2048
	ds_read_b128 v[186:189], v172 offset:3072
	ds_read_b128 v[190:193], v172 offset:4096
	ds_read_b128 v[194:197], v172 offset:5120
	ds_read_b128 v[198:201], v172 offset:6144
	ds_read_b128 v[202:205], v172 offset:7168
	s_add_u32 s34, s34, 0x80
	s_addc_u32 s35, s35, 0
	s_mov_b32 s65, m0
	s_mov_b32 m0, s59
	s_nop 3
	global_load_lds_dwordx4 v232, s[34:35]
	s_mov_b32 m0, s65
	s_add_i32 s65, s33, 0xe000
	s_mov_b32 s66, m0
	s_mov_b32 m0, s65
	s_nop 3
	global_load_lds_dwordx4 v233, s[34:35]
	s_mov_b32 m0, s66
	s_waitcnt vmcnt(8)
	s_waitcnt lgkmcnt(0)
	s_barrier
	s_waitcnt lgkmcnt(6)
	v_mfma_scale_f32_16x16x128_f8f6f4 v[154:157], v[26:33], v[174:181], v[154:157], v168, v169 op_sel_hi:[0,0,0]
	v_mfma_scale_f32_16x16x128_f8f6f4 v[146:149], v[18:25], v[174:181], v[146:149], v168, v169 op_sel_hi:[0,0,0]
	s_waitcnt lgkmcnt(4)
	v_mfma_scale_f32_16x16x128_f8f6f4 v[138:141], v[26:33], v[182:189], v[138:141], v168, v169 op_sel_hi:[0,0,0]
	v_mfma_scale_f32_16x16x128_f8f6f4 v[130:133], v[18:25], v[182:189], v[130:133], v168, v169 op_sel_hi:[0,0,0]
	s_waitcnt lgkmcnt(2)
	v_mfma_scale_f32_16x16x128_f8f6f4 v[122:125], v[26:33], v[190:197], v[122:125], v168, v169 op_sel_hi:[0,0,0]
	v_mfma_scale_f32_16x16x128_f8f6f4 v[114:117], v[18:25], v[190:197], v[114:117], v168, v169 op_sel_hi:[0,0,0]
	s_waitcnt lgkmcnt(0)
	v_mfma_scale_f32_16x16x128_f8f6f4 v[106:109], v[26:33], v[198:205], v[106:109], v168, v169 op_sel_hi:[0,0,0]
	v_mfma_scale_f32_16x16x128_f8f6f4 v[98:101], v[18:25], v[198:205], v[98:101], v168, v169 op_sel_hi:[0,0,0]
	v_mfma_scale_f32_16x16x128_f8f6f4 v[158:161], v[10:17], v[174:181], v[158:161], v168, v169 op_sel_hi:[0,0,0]
	v_mfma_scale_f32_16x16x128_f8f6f4 v[150:153], v[2:9], v[174:181], v[150:153], v168, v169 op_sel_hi:[0,0,0]
	v_mfma_scale_f32_16x16x128_f8f6f4 v[142:145], v[10:17], v[182:189], v[142:145], v168, v169 op_sel_hi:[0,0,0]
	v_mfma_scale_f32_16x16x128_f8f6f4 v[134:137], v[2:9], v[182:189], v[134:137], v168, v169 op_sel_hi:[0,0,0]
	v_mfma_scale_f32_16x16x128_f8f6f4 v[126:129], v[10:17], v[190:197], v[126:129], v168, v169 op_sel_hi:[0,0,0]
	v_mfma_scale_f32_16x16x128_f8f6f4 v[118:121], v[2:9], v[190:197], v[118:121], v168, v169 op_sel_hi:[0,0,0]
	v_mfma_scale_f32_16x16x128_f8f6f4 v[110:113], v[10:17], v[198:205], v[110:113], v168, v169 op_sel_hi:[0,0,0]
	v_mfma_scale_f32_16x16x128_f8f6f4 v[102:105], v[2:9], v[198:205], v[102:105], v168, v169 op_sel_hi:[0,0,0]
	s_barrier
	ds_read_b128 v[174:177], v172 offset:16384
	ds_read_b128 v[178:181], v172 offset:17408
	ds_read_b128 v[182:185], v172 offset:18432
	ds_read_b128 v[186:189], v172 offset:19456
	ds_read_b128 v[190:193], v172 offset:20480
	ds_read_b128 v[194:197], v172 offset:21504
	ds_read_b128 v[198:201], v172 offset:22528
	ds_read_b128 v[202:205], v172 offset:23552
	s_mov_b32 s34, m0
	s_mov_b32 m0, s43
	s_nop 3
	global_load_lds_dwordx4 v165, s[30:31]
	s_mov_b32 m0, s34
	s_nop 0
	s_mov_b32 s34, m0
	s_mov_b32 m0, s44
	s_nop 3
	global_load_lds_dwordx4 v167, s[30:31]
	s_mov_b32 m0, s34
	s_add_u32 s34, s30, 0x20000
	s_addc_u32 s35, s31, 0
	s_mov_b32 s65, m0
	s_mov_b32 m0, s45
	s_nop 3
	global_load_lds_dwordx4 v165, s[34:35]
	s_mov_b32 m0, s65
	s_nop 0
	s_mov_b32 s65, m0
	s_mov_b32 m0, s47
	s_nop 3
	global_load_lds_dwordx4 v167, s[34:35]
	s_mov_b32 m0, s65
	s_cmp_lg_u32 s64, 4
	s_cbranch_scc1 .Lp8_noswap
	v_lshl_or_b32 v164, v238, 10, v234
	v_lshl_or_b32 v166, v239, 10, v235
	v_lshl_or_b32 v232, v240, 10, v234
	v_lshl_or_b32 v233, v241, 10, v235
.Lp8_noswap:
	s_mov_b32 s34, m0
	s_mov_b32 m0, s33
	s_nop 3
	global_load_lds_dwordx4 v164, s[36:37]
	s_mov_b32 m0, s34
	s_nop 0
	s_mov_b32 s34, m0
	s_mov_b32 m0, s48
	s_nop 3
	global_load_lds_dwordx4 v166, s[36:37]
	s_mov_b32 m0, s34
	s_waitcnt vmcnt(8)
	s_waitcnt lgkmcnt(0)
	s_barrier
	s_waitcnt lgkmcnt(6)
	v_mfma_scale_f32_16x16x128_f8f6f4 v[90:93], v[26:33], v[174:181], v[90:93], v168, v169 op_sel_hi:[0,0,0]
	v_mfma_scale_f32_16x16x128_f8f6f4 v[82:85], v[18:25], v[174:181], v[82:85], v168, v169 op_sel_hi:[0,0,0]
	s_waitcnt lgkmcnt(4)
	v_mfma_scale_f32_16x16x128_f8f6f4 v[74:77], v[26:33], v[182:189], v[74:77], v168, v169 op_sel_hi:[0,0,0]
	v_mfma_scale_f32_16x16x128_f8f6f4 v[66:69], v[18:25], v[182:189], v[66:69], v168, v169 op_sel_hi:[0,0,0]
	s_waitcnt lgkmcnt(2)
	v_mfma_scale_f32_16x16x128_f8f6f4 v[58:61], v[26:33], v[190:197], v[58:61], v168, v169 op_sel_hi:[0,0,0]
	v_mfma_scale_f32_16x16x128_f8f6f4 v[50:53], v[18:25], v[190:197], v[50:53], v168, v169 op_sel_hi:[0,0,0]
	s_waitcnt lgkmcnt(0)
	v_mfma_scale_f32_16x16x128_f8f6f4 v[42:45], v[26:33], v[198:205], v[42:45], v168, v169 op_sel_hi:[0,0,0]
	v_mfma_scale_f32_16x16x128_f8f6f4 v[38:41], v[18:25], v[198:205], v[38:41], v168, v169 op_sel_hi:[0,0,0]
	v_mfma_scale_f32_16x16x128_f8f6f4 v[94:97], v[10:17], v[174:181], v[94:97], v168, v169 op_sel_hi:[0,0,0]
	v_mfma_scale_f32_16x16x128_f8f6f4 v[86:89], v[2:9], v[174:181], v[86:89], v168, v169 op_sel_hi:[0,0,0]
	v_mfma_scale_f32_16x16x128_f8f6f4 v[78:81], v[10:17], v[182:189], v[78:81], v168, v169 op_sel_hi:[0,0,0]
	v_mfma_scale_f32_16x16x128_f8f6f4 v[70:73], v[2:9], v[182:189], v[70:73], v168, v169 op_sel_hi:[0,0,0]
	v_mfma_scale_f32_16x16x128_f8f6f4 v[62:65], v[10:17], v[190:197], v[62:65], v168, v169 op_sel_hi:[0,0,0]
	v_mfma_scale_f32_16x16x128_f8f6f4 v[54:57], v[2:9], v[190:197], v[54:57], v168, v169 op_sel_hi:[0,0,0]
	v_mfma_scale_f32_16x16x128_f8f6f4 v[46:49], v[10:17], v[198:205], v[46:49], v168, v169 op_sel_hi:[0,0,0]
	v_mfma_scale_f32_16x16x128_f8f6f4 v[34:37], v[2:9], v[198:205], v[34:37], v168, v169 op_sel_hi:[0,0,0]
	s_barrier
	v_add_u32_e32 v2, 0x18000, v171
	v_add_u32_e32 v6, 0x1c000, v171
	ds_read_b128 v[26:29], v2
	ds_read_b128 v[30:33], v2 offset:1024
	ds_read_b128 v[18:21], v2 offset:2048
	ds_read_b128 v[22:25], v2 offset:3072
	ds_read_b128 v[10:13], v6
	ds_read_b128 v[14:17], v6 offset:1024
	ds_read_b128 v[2:5], v6 offset:2048
	ds_read_b128 v[6:9], v6 offset:3072
	ds_read_b128 v[174:177], v172 offset:32768
	ds_read_b128 v[178:181], v172 offset:33792
	ds_read_b128 v[182:185], v172 offset:34816
	ds_read_b128 v[186:189], v172 offset:35840
	ds_read_b128 v[190:193], v172 offset:36864
	ds_read_b128 v[194:197], v172 offset:37888
	ds_read_b128 v[198:201], v172 offset:38912
	ds_read_b128 v[202:205], v172 offset:39936
	s_add_u32 s34, s36, 0
	s_addc_u32 s35, s37, 0
	s_mov_b32 s36, m0
	s_mov_b32 m0, s49
	s_nop 3
	global_load_lds_dwordx4 v232, s[34:35]
	s_mov_b32 m0, s36
	s_nop 0
	s_mov_b32 s36, m0
	s_mov_b32 m0, s50
	s_nop 3
	global_load_lds_dwordx4 v233, s[34:35]
	s_mov_b32 m0, s36
	s_waitcnt vmcnt(8)
	s_waitcnt lgkmcnt(0)
	s_barrier
	s_waitcnt lgkmcnt(6)
	v_mfma_scale_f32_16x16x128_f8f6f4 v[154:157], v[26:33], v[174:181], v[154:157], v168, v169 op_sel_hi:[0,0,0]
	v_mfma_scale_f32_16x16x128_f8f6f4 v[146:149], v[18:25], v[174:181], v[146:149], v168, v169 op_sel_hi:[0,0,0]
	s_waitcnt lgkmcnt(4)
	v_mfma_scale_f32_16x16x128_f8f6f4 v[138:141], v[26:33], v[182:189], v[138:141], v168, v169 op_sel_hi:[0,0,0]
	v_mfma_scale_f32_16x16x128_f8f6f4 v[130:133], v[18:25], v[182:189], v[130:133], v168, v169 op_sel_hi:[0,0,0]
	s_waitcnt lgkmcnt(2)
	v_mfma_scale_f32_16x16x128_f8f6f4 v[122:125], v[26:33], v[190:197], v[122:125], v168, v169 op_sel_hi:[0,0,0]
	v_mfma_scale_f32_16x16x128_f8f6f4 v[114:117], v[18:25], v[190:197], v[114:117], v168, v169 op_sel_hi:[0,0,0]
	s_waitcnt lgkmcnt(0)
	v_mfma_scale_f32_16x16x128_f8f6f4 v[106:109], v[26:33], v[198:205], v[106:109], v168, v169 op_sel_hi:[0,0,0]
	v_mfma_scale_f32_16x16x128_f8f6f4 v[98:101], v[18:25], v[198:205], v[98:101], v168, v169 op_sel_hi:[0,0,0]
	v_mfma_scale_f32_16x16x128_f8f6f4 v[158:161], v[10:17], v[174:181], v[158:161], v168, v169 op_sel_hi:[0,0,0]
	v_mfma_scale_f32_16x16x128_f8f6f4 v[150:153], v[2:9], v[174:181], v[150:153], v168, v169 op_sel_hi:[0,0,0]
	v_mfma_scale_f32_16x16x128_f8f6f4 v[142:145], v[10:17], v[182:189], v[142:145], v168, v169 op_sel_hi:[0,0,0]
	v_mfma_scale_f32_16x16x128_f8f6f4 v[134:137], v[2:9], v[182:189], v[134:137], v168, v169 op_sel_hi:[0,0,0]
	v_mfma_scale_f32_16x16x128_f8f6f4 v[126:129], v[10:17], v[190:197], v[126:129], v168, v169 op_sel_hi:[0,0,0]
	v_mfma_scale_f32_16x16x128_f8f6f4 v[118:121], v[2:9], v[190:197], v[118:121], v168, v169 op_sel_hi:[0,0,0]
	v_mfma_scale_f32_16x16x128_f8f6f4 v[110:113], v[10:17], v[198:205], v[110:113], v168, v169 op_sel_hi:[0,0,0]
	v_mfma_scale_f32_16x16x128_f8f6f4 v[102:105], v[2:9], v[198:205], v[102:105], v168, v169 op_sel_hi:[0,0,0]
	s_barrier
	ds_read_b128 v[174:177], v172 offset:49152
	ds_read_b128 v[178:181], v172 offset:50176
	ds_read_b128 v[182:185], v172 offset:51200
	ds_read_b128 v[186:189], v172 offset:52224
	ds_read_b128 v[190:193], v172 offset:53248
	ds_read_b128 v[194:197], v172 offset:54272
	ds_read_b128 v[198:201], v172 offset:55296
	ds_read_b128 v[202:205], v172 offset:56320
	s_add_u32 s34, s30, 0x80
	s_addc_u32 s35, s31, 0
	s_mov_b32 s36, m0
	s_mov_b32 m0, s53
	s_nop 3
	global_load_lds_dwordx4 v165, s[34:35]
	s_mov_b32 m0, s36
	s_add_u32 s30, s30, 0x20080
	s_mov_b32 s36, m0
	s_mov_b32 m0, s54
	s_nop 3
	global_load_lds_dwordx4 v167, s[34:35]
	s_mov_b32 m0, s36
	s_addc_u32 s31, s31, 0
	s_mov_b32 s34, m0
	s_mov_b32 m0, s57
	s_nop 3
	global_load_lds_dwordx4 v165, s[30:31]
	s_mov_b32 m0, s34
	s_nop 0
	s_mov_b32 s34, m0
	s_mov_b32 m0, s58
	s_nop 3
	global_load_lds_dwordx4 v167, s[30:31]
	s_mov_b32 m0, s34
	s_mov_b32 s30, m0
	s_mov_b32 m0, s55
	s_nop 3
	global_load_lds_dwordx4 v164, s[28:29]
	s_mov_b32 m0, s30
	s_nop 0
	s_mov_b32 s30, m0
	s_mov_b32 m0, s56
	s_nop 3
	global_load_lds_dwordx4 v166, s[28:29]
	s_mov_b32 m0, s30
	s_waitcnt vmcnt(8)
	s_waitcnt lgkmcnt(0)
	s_barrier
	s_waitcnt lgkmcnt(6)
	v_mfma_scale_f32_16x16x128_f8f6f4 v[90:93], v[26:33], v[174:181], v[90:93], v168, v169 op_sel_hi:[0,0,0]
	v_mfma_scale_f32_16x16x128_f8f6f4 v[82:85], v[18:25], v[174:181], v[82:85], v168, v169 op_sel_hi:[0,0,0]
	s_waitcnt lgkmcnt(4)
	v_mfma_scale_f32_16x16x128_f8f6f4 v[74:77], v[26:33], v[182:189], v[74:77], v168, v169 op_sel_hi:[0,0,0]
	v_mfma_scale_f32_16x16x128_f8f6f4 v[66:69], v[18:25], v[182:189], v[66:69], v168, v169 op_sel_hi:[0,0,0]
	s_waitcnt lgkmcnt(2)
	v_mfma_scale_f32_16x16x128_f8f6f4 v[58:61], v[26:33], v[190:197], v[58:61], v168, v169 op_sel_hi:[0,0,0]
	v_mfma_scale_f32_16x16x128_f8f6f4 v[50:53], v[18:25], v[190:197], v[50:53], v168, v169 op_sel_hi:[0,0,0]
	s_waitcnt lgkmcnt(0)
	v_mfma_scale_f32_16x16x128_f8f6f4 v[42:45], v[26:33], v[198:205], v[42:45], v168, v169 op_sel_hi:[0,0,0]
	v_mfma_scale_f32_16x16x128_f8f6f4 v[38:41], v[18:25], v[198:205], v[38:41], v168, v169 op_sel_hi:[0,0,0]
	v_mfma_scale_f32_16x16x128_f8f6f4 v[94:97], v[10:17], v[174:181], v[94:97], v168, v169 op_sel_hi:[0,0,0]
	v_mfma_scale_f32_16x16x128_f8f6f4 v[86:89], v[2:9], v[174:181], v[86:89], v168, v169 op_sel_hi:[0,0,0]
	v_mfma_scale_f32_16x16x128_f8f6f4 v[78:81], v[10:17], v[182:189], v[78:81], v168, v169 op_sel_hi:[0,0,0]
	v_mfma_scale_f32_16x16x128_f8f6f4 v[70:73], v[2:9], v[182:189], v[70:73], v168, v169 op_sel_hi:[0,0,0]
	v_mfma_scale_f32_16x16x128_f8f6f4 v[62:65], v[10:17], v[190:197], v[62:65], v168, v169 op_sel_hi:[0,0,0]
	v_mfma_scale_f32_16x16x128_f8f6f4 v[54:57], v[2:9], v[190:197], v[54:57], v168, v169 op_sel_hi:[0,0,0]
	v_mfma_scale_f32_16x16x128_f8f6f4 v[46:49], v[10:17], v[198:205], v[46:49], v168, v169 op_sel_hi:[0,0,0]
	v_mfma_scale_f32_16x16x128_f8f6f4 v[34:37], v[2:9], v[198:205], v[34:37], v168, v169 op_sel_hi:[0,0,0]
	s_barrier
	s_add_i32 s64, s64, 2
	s_add_u32 s62, s62, 0x100
	s_addc_u32 s63, s63, 0
	s_cmp_gt_u32 s64, 5
	s_mov_b64 s[34:35], s[26:27]
	s_cbranch_scc0 .LBB0_1226
	s_and_b64 vcc, exec, s[10:11]
	s_cbranch_vccz .LBB0_1229
	s_barrier
.LBB0_1229:
	s_setprio 0
	s_lshl_b32 s13, s24, 8
	s_and_b32 s26, s13, 0xfffff800
	s_ashr_i32 s27, s26, 31
	s_lshl_b64 s[26:27], s[26:27], 2
	s_add_u32 s13, s51, s26
	s_addc_u32 s17, s52, s27
	s_lshl_b32 s14, s24, 7
	s_and_b32 s14, s14, 0x380
	s_lshl_b32 s24, s14, 2
	s_add_u32 s26, s13, s24
	s_addc_u32 s27, s17, 0
	s_nop 15
	s_nop 3
	v_lshl_add_u64 v[6:7], s[26:27], 0, v[0:1]
	s_mov_b64 s[28:29], 0x1000
	s_movk_i32 s13, 0x1000
	v_lshl_add_u64 v[8:9], v[6:7], 0, s[28:29]
	v_add_co_u32_e32 v6, vcc, s13, v6
	s_mov_b32 s17, 0xc0e00000
	s_nop 0
	v_addc_co_u32_e32 v7, vcc, 0, v7, vcc
	s_nop 0
	v_lshl_add_u32 v20, s25, 8, v170
	v_ashrrev_i32_e32 v21, 31, v20
	v_mov_b32_e32 v27, v1
	s_mov_b32 s13, 0x20000
	s_mov_b64 s[24:25], -1
	s_movk_i32 s66, 0x1800
	s_mov_b32 s64, 0x1f000
	s_mov_b32 s30, 0x3fd9db23
	s_mov_b32 s34, 0xbfb8aa3b
	s_mov_b32 s37, 0
	v_lshlrev_b64 v[18:19], 10, v[20:21]
	v_lshl_add_u64 v[18:19], s[8:9], 0, v[18:19]
	v_lshl_add_u64 v[18:19], v[18:19], 0, s[14:15]
	v_lshl_add_u64 v[18:19], v[18:19], 0, v[162:163]
	v_pk_add_f32 v[154:155], v[154:155], v[206:207]
	v_pk_add_f32 v[156:157], v[156:157], v[208:209]
	v_pk_add_f32 v[146:147], v[146:147], v[216:217]
	v_pk_add_f32 v[148:149], v[148:149], v[218:219]
	v_pk_add_f32 v[158:159], v[158:159], v[224:225]
	v_pk_add_f32 v[160:161], v[160:161], v[226:227]
	v_pk_add_f32 v[150:151], v[150:151], v[228:229]
	v_pk_add_f32 v[152:153], v[152:153], v[230:231]
	v_min_f32_e32 v154, 0x40e00000, v154
	v_min_f32_e32 v155, 0x40e00000, v155
	v_min_f32_e32 v156, 0x40e00000, v156
	v_min_f32_e32 v157, 0x40e00000, v157
	v_min_f32_e32 v146, 0x40e00000, v146
	v_min_f32_e32 v147, 0x40e00000, v147
	v_min_f32_e32 v148, 0x40e00000, v148
	v_min_f32_e32 v149, 0x40e00000, v149
	v_med3_f32 v158, v158, s17, v223
	v_med3_f32 v159, v159, s17, v223
	v_med3_f32 v160, v160, s17, v223
	v_med3_f32 v161, v161, s17, v223
	v_med3_f32 v150, v150, s17, v223
	v_med3_f32 v151, v151, s17, v223
	v_med3_f32 v152, v152, s17, v223
	v_med3_f32 v153, v153, s17, v223
	v_pk_mul_f32 v[24:25], v[154:155], s[30:31] op_sel_hi:[1,0]
	v_pk_mul_f32 v[26:27], v[156:157], s[30:31] op_sel_hi:[1,0]
	v_pk_mul_f32 v[28:29], v[146:147], s[30:31] op_sel_hi:[1,0]
	v_pk_mul_f32 v[30:31], v[148:149], s[30:31] op_sel_hi:[1,0]
	v_pk_mul_f32 v[24:25], v[24:25], s[34:35] op_sel_hi:[1,0]
	v_pk_mul_f32 v[26:27], v[26:27], s[34:35] op_sel_hi:[1,0]
	v_pk_mul_f32 v[28:29], v[28:29], s[34:35] op_sel_hi:[1,0]
	v_pk_mul_f32 v[30:31], v[30:31], s[34:35] op_sel_hi:[1,0]
	v_exp_f32_e32 v24, v24
	v_exp_f32_e32 v25, v25
	v_exp_f32_e32 v26, v26
	v_exp_f32_e32 v27, v27
	v_exp_f32_e32 v28, v28
	v_exp_f32_e32 v29, v29
	v_exp_f32_e32 v30, v30
	v_exp_f32_e32 v31, v31
	v_pk_add_f32 v[24:25], v[24:25], 1.0 op_sel_hi:[1,0]
	v_pk_add_f32 v[26:27], v[26:27], 1.0 op_sel_hi:[1,0]
	v_pk_add_f32 v[28:29], v[28:29], 1.0 op_sel_hi:[1,0]
	v_pk_add_f32 v[30:31], v[30:31], 1.0 op_sel_hi:[1,0]
	v_rcp_f32_e32 v24, v24
	v_rcp_f32_e32 v25, v25
	v_rcp_f32_e32 v26, v26
	v_rcp_f32_e32 v27, v27
	v_rcp_f32_e32 v28, v28
	v_rcp_f32_e32 v29, v29
	v_rcp_f32_e32 v30, v30
	v_rcp_f32_e32 v31, v31
	v_pk_add_f32 v[158:159], v[158:159], 1.0 op_sel_hi:[1,0]
	v_pk_add_f32 v[160:161], v[160:161], 1.0 op_sel_hi:[1,0]
	v_pk_add_f32 v[150:151], v[150:151], 1.0 op_sel_hi:[1,0]
	v_pk_add_f32 v[152:153], v[152:153], 1.0 op_sel_hi:[1,0]
	v_pk_mul_f32 v[154:155], v[154:155], v[24:25]
	v_pk_mul_f32 v[156:157], v[156:157], v[26:27]
	v_pk_mul_f32 v[146:147], v[146:147], v[28:29]
	v_pk_mul_f32 v[148:149], v[148:149], v[30:31]
	v_pk_mul_f32 v[154:155], v[158:159], v[154:155]
	v_pk_mul_f32 v[156:157], v[160:161], v[156:157]
	v_pk_mul_f32 v[146:147], v[150:151], v[146:147]
	v_pk_mul_f32 v[148:149], v[152:153], v[148:149]
	v_cvt_pk_fp8_f32 v32, v154, v155
	v_cvt_pk_fp8_f32 v33, v146, v147
	v_cvt_pk_fp8_f32 v32, v156, v157 op_sel:[0,0,1]
	v_cvt_pk_fp8_f32 v33, v148, v149 op_sel:[0,0,1]
	s_nop 0
	global_store_dwordx2 v[18:19], v[32:33], off
	v_pk_add_f32 v[138:139], v[138:139], v[206:207]
	v_pk_add_f32 v[140:141], v[140:141], v[208:209]
	v_pk_add_f32 v[130:131], v[130:131], v[216:217]
	v_pk_add_f32 v[132:133], v[132:133], v[218:219]
	v_pk_add_f32 v[142:143], v[142:143], v[224:225]
	v_pk_add_f32 v[144:145], v[144:145], v[226:227]
	v_pk_add_f32 v[134:135], v[134:135], v[228:229]
	v_pk_add_f32 v[136:137], v[136:137], v[230:231]
	v_min_f32_e32 v138, 0x40e00000, v138
	v_min_f32_e32 v139, 0x40e00000, v139
	v_min_f32_e32 v140, 0x40e00000, v140
	v_min_f32_e32 v141, 0x40e00000, v141
	v_min_f32_e32 v130, 0x40e00000, v130
	v_min_f32_e32 v131, 0x40e00000, v131
	v_min_f32_e32 v132, 0x40e00000, v132
	v_min_f32_e32 v133, 0x40e00000, v133
	v_med3_f32 v142, v142, s17, v223
	v_med3_f32 v143, v143, s17, v223
	v_med3_f32 v144, v144, s17, v223
	v_med3_f32 v145, v145, s17, v223
	v_med3_f32 v134, v134, s17, v223
	v_med3_f32 v135, v135, s17, v223
	v_med3_f32 v136, v136, s17, v223
	v_med3_f32 v137, v137, s17, v223
	v_pk_mul_f32 v[24:25], v[138:139], s[30:31] op_sel_hi:[1,0]
	v_pk_mul_f32 v[26:27], v[140:141], s[30:31] op_sel_hi:[1,0]
	v_pk_mul_f32 v[28:29], v[130:131], s[30:31] op_sel_hi:[1,0]
	v_pk_mul_f32 v[30:31], v[132:133], s[30:31] op_sel_hi:[1,0]
	v_pk_mul_f32 v[24:25], v[24:25], s[34:35] op_sel_hi:[1,0]
	v_pk_mul_f32 v[26:27], v[26:27], s[34:35] op_sel_hi:[1,0]
	v_pk_mul_f32 v[28:29], v[28:29], s[34:35] op_sel_hi:[1,0]
	v_pk_mul_f32 v[30:31], v[30:31], s[34:35] op_sel_hi:[1,0]
	v_exp_f32_e32 v24, v24
	v_exp_f32_e32 v25, v25
	v_exp_f32_e32 v26, v26
	v_exp_f32_e32 v27, v27
	v_exp_f32_e32 v28, v28
	v_exp_f32_e32 v29, v29
	v_exp_f32_e32 v30, v30
	v_exp_f32_e32 v31, v31
	v_pk_add_f32 v[24:25], v[24:25], 1.0 op_sel_hi:[1,0]
	v_pk_add_f32 v[26:27], v[26:27], 1.0 op_sel_hi:[1,0]
	v_pk_add_f32 v[28:29], v[28:29], 1.0 op_sel_hi:[1,0]
	v_pk_add_f32 v[30:31], v[30:31], 1.0 op_sel_hi:[1,0]
	v_rcp_f32_e32 v24, v24
	v_rcp_f32_e32 v25, v25
	v_rcp_f32_e32 v26, v26
	v_rcp_f32_e32 v27, v27
	v_rcp_f32_e32 v28, v28
	v_rcp_f32_e32 v29, v29
	v_rcp_f32_e32 v30, v30
	v_rcp_f32_e32 v31, v31
	v_pk_add_f32 v[142:143], v[142:143], 1.0 op_sel_hi:[1,0]
	v_pk_add_f32 v[144:145], v[144:145], 1.0 op_sel_hi:[1,0]
	v_pk_add_f32 v[134:135], v[134:135], 1.0 op_sel_hi:[1,0]
	v_pk_add_f32 v[136:137], v[136:137], 1.0 op_sel_hi:[1,0]
	v_pk_mul_f32 v[138:139], v[138:139], v[24:25]
	v_pk_mul_f32 v[140:141], v[140:141], v[26:27]
	v_pk_mul_f32 v[130:131], v[130:131], v[28:29]
	v_pk_mul_f32 v[132:133], v[132:133], v[30:31]
	v_pk_mul_f32 v[138:139], v[142:143], v[138:139]
	v_pk_mul_f32 v[140:141], v[144:145], v[140:141]
	v_pk_mul_f32 v[130:131], v[134:135], v[130:131]
	v_pk_mul_f32 v[132:133], v[136:137], v[132:133]
	v_cvt_pk_fp8_f32 v32, v138, v139
	v_cvt_pk_fp8_f32 v33, v130, v131
	v_cvt_pk_fp8_f32 v32, v140, v141 op_sel:[0,0,1]
	v_cvt_pk_fp8_f32 v33, v132, v133 op_sel:[0,0,1]
	s_mov_b32 s36, 0x4000
	v_lshl_add_u64 v[22:23], v[18:19], 0, s[36:37]
	global_store_dwordx2 v[22:23], v[32:33], off
	v_pk_add_f32 v[122:123], v[122:123], v[206:207]
	v_pk_add_f32 v[124:125], v[124:125], v[208:209]
	v_pk_add_f32 v[114:115], v[114:115], v[216:217]
	v_pk_add_f32 v[116:117], v[116:117], v[218:219]
	v_pk_add_f32 v[126:127], v[126:127], v[224:225]
	v_pk_add_f32 v[128:129], v[128:129], v[226:227]
	v_pk_add_f32 v[118:119], v[118:119], v[228:229]
	v_pk_add_f32 v[120:121], v[120:121], v[230:231]
	v_min_f32_e32 v122, 0x40e00000, v122
	v_min_f32_e32 v123, 0x40e00000, v123
	v_min_f32_e32 v124, 0x40e00000, v124
	v_min_f32_e32 v125, 0x40e00000, v125
	v_min_f32_e32 v114, 0x40e00000, v114
	v_min_f32_e32 v115, 0x40e00000, v115
	v_min_f32_e32 v116, 0x40e00000, v116
	v_min_f32_e32 v117, 0x40e00000, v117
	v_med3_f32 v126, v126, s17, v223
	v_med3_f32 v127, v127, s17, v223
	v_med3_f32 v128, v128, s17, v223
	v_med3_f32 v129, v129, s17, v223
	v_med3_f32 v118, v118, s17, v223
	v_med3_f32 v119, v119, s17, v223
	v_med3_f32 v120, v120, s17, v223
	v_med3_f32 v121, v121, s17, v223
	v_pk_mul_f32 v[24:25], v[122:123], s[30:31] op_sel_hi:[1,0]
	v_pk_mul_f32 v[26:27], v[124:125], s[30:31] op_sel_hi:[1,0]
	v_pk_mul_f32 v[28:29], v[114:115], s[30:31] op_sel_hi:[1,0]
	v_pk_mul_f32 v[30:31], v[116:117], s[30:31] op_sel_hi:[1,0]
	v_pk_mul_f32 v[24:25], v[24:25], s[34:35] op_sel_hi:[1,0]
	v_pk_mul_f32 v[26:27], v[26:27], s[34:35] op_sel_hi:[1,0]
	v_pk_mul_f32 v[28:29], v[28:29], s[34:35] op_sel_hi:[1,0]
	v_pk_mul_f32 v[30:31], v[30:31], s[34:35] op_sel_hi:[1,0]
	v_exp_f32_e32 v24, v24
	v_exp_f32_e32 v25, v25
	v_exp_f32_e32 v26, v26
	v_exp_f32_e32 v27, v27
	v_exp_f32_e32 v28, v28
	v_exp_f32_e32 v29, v29
	v_exp_f32_e32 v30, v30
	v_exp_f32_e32 v31, v31
	v_pk_add_f32 v[24:25], v[24:25], 1.0 op_sel_hi:[1,0]
	v_pk_add_f32 v[26:27], v[26:27], 1.0 op_sel_hi:[1,0]
	v_pk_add_f32 v[28:29], v[28:29], 1.0 op_sel_hi:[1,0]
	v_pk_add_f32 v[30:31], v[30:31], 1.0 op_sel_hi:[1,0]
	v_rcp_f32_e32 v24, v24
	v_rcp_f32_e32 v25, v25
	v_rcp_f32_e32 v26, v26
	v_rcp_f32_e32 v27, v27
	v_rcp_f32_e32 v28, v28
	v_rcp_f32_e32 v29, v29
	v_rcp_f32_e32 v30, v30
	v_rcp_f32_e32 v31, v31
	v_pk_add_f32 v[126:127], v[126:127], 1.0 op_sel_hi:[1,0]
	v_pk_add_f32 v[128:129], v[128:129], 1.0 op_sel_hi:[1,0]
	v_pk_add_f32 v[118:119], v[118:119], 1.0 op_sel_hi:[1,0]
	v_pk_add_f32 v[120:121], v[120:121], 1.0 op_sel_hi:[1,0]
	v_pk_mul_f32 v[122:123], v[122:123], v[24:25]
	v_pk_mul_f32 v[124:125], v[124:125], v[26:27]
	v_pk_mul_f32 v[114:115], v[114:115], v[28:29]
	v_pk_mul_f32 v[116:117], v[116:117], v[30:31]
	v_pk_mul_f32 v[122:123], v[126:127], v[122:123]
	v_pk_mul_f32 v[124:125], v[128:129], v[124:125]
	v_pk_mul_f32 v[114:115], v[118:119], v[114:115]
	v_pk_mul_f32 v[116:117], v[120:121], v[116:117]
	v_cvt_pk_fp8_f32 v32, v122, v123
	v_cvt_pk_fp8_f32 v33, v114, v115
	v_cvt_pk_fp8_f32 v32, v124, v125 op_sel:[0,0,1]
	v_cvt_pk_fp8_f32 v33, v116, v117 op_sel:[0,0,1]
	s_mov_b32 s36, 0x8000
	v_lshl_add_u64 v[22:23], v[18:19], 0, s[36:37]
	global_store_dwordx2 v[22:23], v[32:33], off
	v_pk_add_f32 v[106:107], v[106:107], v[206:207]
	v_pk_add_f32 v[108:109], v[108:109], v[208:209]
	v_pk_add_f32 v[98:99], v[98:99], v[216:217]
	v_pk_add_f32 v[100:101], v[100:101], v[218:219]
	v_pk_add_f32 v[110:111], v[110:111], v[224:225]
	v_pk_add_f32 v[112:113], v[112:113], v[226:227]
	v_pk_add_f32 v[102:103], v[102:103], v[228:229]
	v_pk_add_f32 v[104:105], v[104:105], v[230:231]
	v_min_f32_e32 v106, 0x40e00000, v106
	v_min_f32_e32 v107, 0x40e00000, v107
	v_min_f32_e32 v108, 0x40e00000, v108
	v_min_f32_e32 v109, 0x40e00000, v109
	v_min_f32_e32 v98, 0x40e00000, v98
	v_min_f32_e32 v99, 0x40e00000, v99
	v_min_f32_e32 v100, 0x40e00000, v100
	v_min_f32_e32 v101, 0x40e00000, v101
	v_med3_f32 v110, v110, s17, v223
	v_med3_f32 v111, v111, s17, v223
	v_med3_f32 v112, v112, s17, v223
	v_med3_f32 v113, v113, s17, v223
	v_med3_f32 v102, v102, s17, v223
	v_med3_f32 v103, v103, s17, v223
	v_med3_f32 v104, v104, s17, v223
	v_med3_f32 v105, v105, s17, v223
	v_pk_mul_f32 v[24:25], v[106:107], s[30:31] op_sel_hi:[1,0]
	v_pk_mul_f32 v[26:27], v[108:109], s[30:31] op_sel_hi:[1,0]
	v_pk_mul_f32 v[28:29], v[98:99], s[30:31] op_sel_hi:[1,0]
	v_pk_mul_f32 v[30:31], v[100:101], s[30:31] op_sel_hi:[1,0]
	v_pk_mul_f32 v[24:25], v[24:25], s[34:35] op_sel_hi:[1,0]
	v_pk_mul_f32 v[26:27], v[26:27], s[34:35] op_sel_hi:[1,0]
	v_pk_mul_f32 v[28:29], v[28:29], s[34:35] op_sel_hi:[1,0]
	v_pk_mul_f32 v[30:31], v[30:31], s[34:35] op_sel_hi:[1,0]
	v_exp_f32_e32 v24, v24
	v_exp_f32_e32 v25, v25
	v_exp_f32_e32 v26, v26
	v_exp_f32_e32 v27, v27
	v_exp_f32_e32 v28, v28
	v_exp_f32_e32 v29, v29
	v_exp_f32_e32 v30, v30
	v_exp_f32_e32 v31, v31
	v_pk_add_f32 v[24:25], v[24:25], 1.0 op_sel_hi:[1,0]
	v_pk_add_f32 v[26:27], v[26:27], 1.0 op_sel_hi:[1,0]
	v_pk_add_f32 v[28:29], v[28:29], 1.0 op_sel_hi:[1,0]
	v_pk_add_f32 v[30:31], v[30:31], 1.0 op_sel_hi:[1,0]
	v_rcp_f32_e32 v24, v24
	v_rcp_f32_e32 v25, v25
	v_rcp_f32_e32 v26, v26
	v_rcp_f32_e32 v27, v27
	v_rcp_f32_e32 v28, v28
	v_rcp_f32_e32 v29, v29
	v_rcp_f32_e32 v30, v30
	v_rcp_f32_e32 v31, v31
	v_pk_add_f32 v[110:111], v[110:111], 1.0 op_sel_hi:[1,0]
	v_pk_add_f32 v[112:113], v[112:113], 1.0 op_sel_hi:[1,0]
	v_pk_add_f32 v[102:103], v[102:103], 1.0 op_sel_hi:[1,0]
	v_pk_add_f32 v[104:105], v[104:105], 1.0 op_sel_hi:[1,0]
	v_pk_mul_f32 v[106:107], v[106:107], v[24:25]
	v_pk_mul_f32 v[108:109], v[108:109], v[26:27]
	v_pk_mul_f32 v[98:99], v[98:99], v[28:29]
	v_pk_mul_f32 v[100:101], v[100:101], v[30:31]
	v_pk_mul_f32 v[106:107], v[110:111], v[106:107]
	v_pk_mul_f32 v[108:109], v[112:113], v[108:109]
	v_pk_mul_f32 v[98:99], v[102:103], v[98:99]
	v_pk_mul_f32 v[100:101], v[104:105], v[100:101]
	v_cvt_pk_fp8_f32 v32, v106, v107
	v_cvt_pk_fp8_f32 v33, v98, v99
	v_cvt_pk_fp8_f32 v32, v108, v109 op_sel:[0,0,1]
	v_cvt_pk_fp8_f32 v33, v100, v101 op_sel:[0,0,1]
	s_mov_b32 s36, 0xc000
	v_lshl_add_u64 v[22:23], v[18:19], 0, s[36:37]
	global_store_dwordx2 v[22:23], v[32:33], off
	v_pk_add_f32 v[90:91], v[90:91], v[206:207]
	v_pk_add_f32 v[92:93], v[92:93], v[208:209]
	v_pk_add_f32 v[82:83], v[82:83], v[216:217]
	v_pk_add_f32 v[84:85], v[84:85], v[218:219]
	v_pk_add_f32 v[94:95], v[94:95], v[224:225]
	v_pk_add_f32 v[96:97], v[96:97], v[226:227]
	v_pk_add_f32 v[86:87], v[86:87], v[228:229]
	v_pk_add_f32 v[88:89], v[88:89], v[230:231]
	v_min_f32_e32 v90, 0x40e00000, v90
	v_min_f32_e32 v91, 0x40e00000, v91
	v_min_f32_e32 v92, 0x40e00000, v92
	v_min_f32_e32 v93, 0x40e00000, v93
	v_min_f32_e32 v82, 0x40e00000, v82
	v_min_f32_e32 v83, 0x40e00000, v83
	v_min_f32_e32 v84, 0x40e00000, v84
	v_min_f32_e32 v85, 0x40e00000, v85
	v_med3_f32 v94, v94, s17, v223
	v_med3_f32 v95, v95, s17, v223
	v_med3_f32 v96, v96, s17, v223
	v_med3_f32 v97, v97, s17, v223
	v_med3_f32 v86, v86, s17, v223
	v_med3_f32 v87, v87, s17, v223
	v_med3_f32 v88, v88, s17, v223
	v_med3_f32 v89, v89, s17, v223
	v_pk_mul_f32 v[24:25], v[90:91], s[30:31] op_sel_hi:[1,0]
	v_pk_mul_f32 v[26:27], v[92:93], s[30:31] op_sel_hi:[1,0]
	v_pk_mul_f32 v[28:29], v[82:83], s[30:31] op_sel_hi:[1,0]
	v_pk_mul_f32 v[30:31], v[84:85], s[30:31] op_sel_hi:[1,0]
	v_pk_mul_f32 v[24:25], v[24:25], s[34:35] op_sel_hi:[1,0]
	v_pk_mul_f32 v[26:27], v[26:27], s[34:35] op_sel_hi:[1,0]
	v_pk_mul_f32 v[28:29], v[28:29], s[34:35] op_sel_hi:[1,0]
	v_pk_mul_f32 v[30:31], v[30:31], s[34:35] op_sel_hi:[1,0]
	v_exp_f32_e32 v24, v24
	v_exp_f32_e32 v25, v25
	v_exp_f32_e32 v26, v26
	v_exp_f32_e32 v27, v27
	v_exp_f32_e32 v28, v28
	v_exp_f32_e32 v29, v29
	v_exp_f32_e32 v30, v30
	v_exp_f32_e32 v31, v31
	v_pk_add_f32 v[24:25], v[24:25], 1.0 op_sel_hi:[1,0]
	v_pk_add_f32 v[26:27], v[26:27], 1.0 op_sel_hi:[1,0]
	v_pk_add_f32 v[28:29], v[28:29], 1.0 op_sel_hi:[1,0]
	v_pk_add_f32 v[30:31], v[30:31], 1.0 op_sel_hi:[1,0]
	v_rcp_f32_e32 v24, v24
	v_rcp_f32_e32 v25, v25
	v_rcp_f32_e32 v26, v26
	v_rcp_f32_e32 v27, v27
	v_rcp_f32_e32 v28, v28
	v_rcp_f32_e32 v29, v29
	v_rcp_f32_e32 v30, v30
	v_rcp_f32_e32 v31, v31
	v_pk_add_f32 v[94:95], v[94:95], 1.0 op_sel_hi:[1,0]
	v_pk_add_f32 v[96:97], v[96:97], 1.0 op_sel_hi:[1,0]
	v_pk_add_f32 v[86:87], v[86:87], 1.0 op_sel_hi:[1,0]
	v_pk_add_f32 v[88:89], v[88:89], 1.0 op_sel_hi:[1,0]
	v_pk_mul_f32 v[90:91], v[90:91], v[24:25]
	v_pk_mul_f32 v[92:93], v[92:93], v[26:27]
	v_pk_mul_f32 v[82:83], v[82:83], v[28:29]
	v_pk_mul_f32 v[84:85], v[84:85], v[30:31]
	v_pk_mul_f32 v[90:91], v[94:95], v[90:91]
	v_pk_mul_f32 v[92:93], v[96:97], v[92:93]
	v_pk_mul_f32 v[82:83], v[86:87], v[82:83]
	v_pk_mul_f32 v[84:85], v[88:89], v[84:85]
	v_cvt_pk_fp8_f32 v32, v90, v91
	v_cvt_pk_fp8_f32 v33, v82, v83
	v_cvt_pk_fp8_f32 v32, v92, v93 op_sel:[0,0,1]
	v_cvt_pk_fp8_f32 v33, v84, v85 op_sel:[0,0,1]
	s_mov_b32 s36, 0x20000
	v_lshl_add_u64 v[22:23], v[18:19], 0, s[36:37]
	global_store_dwordx2 v[22:23], v[32:33], off
	v_pk_add_f32 v[74:75], v[74:75], v[206:207]
	v_pk_add_f32 v[76:77], v[76:77], v[208:209]
	v_pk_add_f32 v[66:67], v[66:67], v[216:217]
	v_pk_add_f32 v[68:69], v[68:69], v[218:219]
	v_pk_add_f32 v[78:79], v[78:79], v[224:225]
	v_pk_add_f32 v[80:81], v[80:81], v[226:227]
	v_pk_add_f32 v[70:71], v[70:71], v[228:229]
	v_pk_add_f32 v[72:73], v[72:73], v[230:231]
	v_min_f32_e32 v74, 0x40e00000, v74
	v_min_f32_e32 v75, 0x40e00000, v75
	v_min_f32_e32 v76, 0x40e00000, v76
	v_min_f32_e32 v77, 0x40e00000, v77
	v_min_f32_e32 v66, 0x40e00000, v66
	v_min_f32_e32 v67, 0x40e00000, v67
	v_min_f32_e32 v68, 0x40e00000, v68
	v_min_f32_e32 v69, 0x40e00000, v69
	v_med3_f32 v78, v78, s17, v223
	v_med3_f32 v79, v79, s17, v223
	v_med3_f32 v80, v80, s17, v223
	v_med3_f32 v81, v81, s17, v223
	v_med3_f32 v70, v70, s17, v223
	v_med3_f32 v71, v71, s17, v223
	v_med3_f32 v72, v72, s17, v223
	v_med3_f32 v73, v73, s17, v223
	v_pk_mul_f32 v[24:25], v[74:75], s[30:31] op_sel_hi:[1,0]
	v_pk_mul_f32 v[26:27], v[76:77], s[30:31] op_sel_hi:[1,0]
	v_pk_mul_f32 v[28:29], v[66:67], s[30:31] op_sel_hi:[1,0]
	v_pk_mul_f32 v[30:31], v[68:69], s[30:31] op_sel_hi:[1,0]
	v_pk_mul_f32 v[24:25], v[24:25], s[34:35] op_sel_hi:[1,0]
	v_pk_mul_f32 v[26:27], v[26:27], s[34:35] op_sel_hi:[1,0]
	v_pk_mul_f32 v[28:29], v[28:29], s[34:35] op_sel_hi:[1,0]
	v_pk_mul_f32 v[30:31], v[30:31], s[34:35] op_sel_hi:[1,0]
	v_exp_f32_e32 v24, v24
	v_exp_f32_e32 v25, v25
	v_exp_f32_e32 v26, v26
	v_exp_f32_e32 v27, v27
	v_exp_f32_e32 v28, v28
	v_exp_f32_e32 v29, v29
	v_exp_f32_e32 v30, v30
	v_exp_f32_e32 v31, v31
	v_pk_add_f32 v[24:25], v[24:25], 1.0 op_sel_hi:[1,0]
	v_pk_add_f32 v[26:27], v[26:27], 1.0 op_sel_hi:[1,0]
	v_pk_add_f32 v[28:29], v[28:29], 1.0 op_sel_hi:[1,0]
	v_pk_add_f32 v[30:31], v[30:31], 1.0 op_sel_hi:[1,0]
	v_rcp_f32_e32 v24, v24
	v_rcp_f32_e32 v25, v25
	v_rcp_f32_e32 v26, v26
	v_rcp_f32_e32 v27, v27
	v_rcp_f32_e32 v28, v28
	v_rcp_f32_e32 v29, v29
	v_rcp_f32_e32 v30, v30
	v_rcp_f32_e32 v31, v31
	v_pk_add_f32 v[78:79], v[78:79], 1.0 op_sel_hi:[1,0]
	v_pk_add_f32 v[80:81], v[80:81], 1.0 op_sel_hi:[1,0]
	v_pk_add_f32 v[70:71], v[70:71], 1.0 op_sel_hi:[1,0]
	v_pk_add_f32 v[72:73], v[72:73], 1.0 op_sel_hi:[1,0]
	v_pk_mul_f32 v[74:75], v[74:75], v[24:25]
	v_pk_mul_f32 v[76:77], v[76:77], v[26:27]
	v_pk_mul_f32 v[66:67], v[66:67], v[28:29]
	v_pk_mul_f32 v[68:69], v[68:69], v[30:31]
	v_pk_mul_f32 v[74:75], v[78:79], v[74:75]
	v_pk_mul_f32 v[76:77], v[80:81], v[76:77]
	v_pk_mul_f32 v[66:67], v[70:71], v[66:67]
	v_pk_mul_f32 v[68:69], v[72:73], v[68:69]
	v_cvt_pk_fp8_f32 v32, v74, v75
	v_cvt_pk_fp8_f32 v33, v66, v67
	v_cvt_pk_fp8_f32 v32, v76, v77 op_sel:[0,0,1]
	v_cvt_pk_fp8_f32 v33, v68, v69 op_sel:[0,0,1]
	s_mov_b32 s36, 0x24000
	v_lshl_add_u64 v[22:23], v[18:19], 0, s[36:37]
	global_store_dwordx2 v[22:23], v[32:33], off
	v_pk_add_f32 v[58:59], v[58:59], v[206:207]
	v_pk_add_f32 v[60:61], v[60:61], v[208:209]
	v_pk_add_f32 v[50:51], v[50:51], v[216:217]
	v_pk_add_f32 v[52:53], v[52:53], v[218:219]
	v_pk_add_f32 v[62:63], v[62:63], v[224:225]
	v_pk_add_f32 v[64:65], v[64:65], v[226:227]
	v_pk_add_f32 v[54:55], v[54:55], v[228:229]
	v_pk_add_f32 v[56:57], v[56:57], v[230:231]
	v_min_f32_e32 v58, 0x40e00000, v58
	v_min_f32_e32 v59, 0x40e00000, v59
	v_min_f32_e32 v60, 0x40e00000, v60
	v_min_f32_e32 v61, 0x40e00000, v61
	v_min_f32_e32 v50, 0x40e00000, v50
	v_min_f32_e32 v51, 0x40e00000, v51
	v_min_f32_e32 v52, 0x40e00000, v52
	v_min_f32_e32 v53, 0x40e00000, v53
	v_med3_f32 v62, v62, s17, v223
	v_med3_f32 v63, v63, s17, v223
	v_med3_f32 v64, v64, s17, v223
	v_med3_f32 v65, v65, s17, v223
	v_med3_f32 v54, v54, s17, v223
	v_med3_f32 v55, v55, s17, v223
	v_med3_f32 v56, v56, s17, v223
	v_med3_f32 v57, v57, s17, v223
	v_pk_mul_f32 v[24:25], v[58:59], s[30:31] op_sel_hi:[1,0]
	v_pk_mul_f32 v[26:27], v[60:61], s[30:31] op_sel_hi:[1,0]
	v_pk_mul_f32 v[28:29], v[50:51], s[30:31] op_sel_hi:[1,0]
	v_pk_mul_f32 v[30:31], v[52:53], s[30:31] op_sel_hi:[1,0]
	v_pk_mul_f32 v[24:25], v[24:25], s[34:35] op_sel_hi:[1,0]
	v_pk_mul_f32 v[26:27], v[26:27], s[34:35] op_sel_hi:[1,0]
	v_pk_mul_f32 v[28:29], v[28:29], s[34:35] op_sel_hi:[1,0]
	v_pk_mul_f32 v[30:31], v[30:31], s[34:35] op_sel_hi:[1,0]
	v_exp_f32_e32 v24, v24
	v_exp_f32_e32 v25, v25
	v_exp_f32_e32 v26, v26
	v_exp_f32_e32 v27, v27
	v_exp_f32_e32 v28, v28
	v_exp_f32_e32 v29, v29
	v_exp_f32_e32 v30, v30
	v_exp_f32_e32 v31, v31
	v_pk_add_f32 v[24:25], v[24:25], 1.0 op_sel_hi:[1,0]
	v_pk_add_f32 v[26:27], v[26:27], 1.0 op_sel_hi:[1,0]
	v_pk_add_f32 v[28:29], v[28:29], 1.0 op_sel_hi:[1,0]
	v_pk_add_f32 v[30:31], v[30:31], 1.0 op_sel_hi:[1,0]
	v_rcp_f32_e32 v24, v24
	v_rcp_f32_e32 v25, v25
	v_rcp_f32_e32 v26, v26
	v_rcp_f32_e32 v27, v27
	v_rcp_f32_e32 v28, v28
	v_rcp_f32_e32 v29, v29
	v_rcp_f32_e32 v30, v30
	v_rcp_f32_e32 v31, v31
	v_pk_add_f32 v[62:63], v[62:63], 1.0 op_sel_hi:[1,0]
	v_pk_add_f32 v[64:65], v[64:65], 1.0 op_sel_hi:[1,0]
	v_pk_add_f32 v[54:55], v[54:55], 1.0 op_sel_hi:[1,0]
	v_pk_add_f32 v[56:57], v[56:57], 1.0 op_sel_hi:[1,0]
	v_pk_mul_f32 v[58:59], v[58:59], v[24:25]
	v_pk_mul_f32 v[60:61], v[60:61], v[26:27]
	v_pk_mul_f32 v[50:51], v[50:51], v[28:29]
	v_pk_mul_f32 v[52:53], v[52:53], v[30:31]
	v_pk_mul_f32 v[58:59], v[62:63], v[58:59]
	v_pk_mul_f32 v[60:61], v[64:65], v[60:61]
	v_pk_mul_f32 v[50:51], v[54:55], v[50:51]
	v_pk_mul_f32 v[52:53], v[56:57], v[52:53]
	v_cvt_pk_fp8_f32 v32, v58, v59
	v_cvt_pk_fp8_f32 v33, v50, v51
	v_cvt_pk_fp8_f32 v32, v60, v61 op_sel:[0,0,1]
	v_cvt_pk_fp8_f32 v33, v52, v53 op_sel:[0,0,1]
	s_mov_b32 s36, 0x28000
	v_lshl_add_u64 v[22:23], v[18:19], 0, s[36:37]
	global_store_dwordx2 v[22:23], v[32:33], off
	v_pk_add_f32 v[42:43], v[42:43], v[206:207]
	v_pk_add_f32 v[44:45], v[44:45], v[208:209]
	v_pk_add_f32 v[38:39], v[38:39], v[216:217]
	v_pk_add_f32 v[40:41], v[40:41], v[218:219]
	v_pk_add_f32 v[46:47], v[46:47], v[224:225]
	v_pk_add_f32 v[48:49], v[48:49], v[226:227]
	v_pk_add_f32 v[34:35], v[34:35], v[228:229]
	v_pk_add_f32 v[36:37], v[36:37], v[230:231]
	v_min_f32_e32 v42, 0x40e00000, v42
	v_min_f32_e32 v43, 0x40e00000, v43
	v_min_f32_e32 v44, 0x40e00000, v44
	v_min_f32_e32 v45, 0x40e00000, v45
	v_min_f32_e32 v38, 0x40e00000, v38
	v_min_f32_e32 v39, 0x40e00000, v39
	v_min_f32_e32 v40, 0x40e00000, v40
	v_min_f32_e32 v41, 0x40e00000, v41
	v_med3_f32 v46, v46, s17, v223
	v_med3_f32 v47, v47, s17, v223
	v_med3_f32 v48, v48, s17, v223
	v_med3_f32 v49, v49, s17, v223
	v_med3_f32 v34, v34, s17, v223
	v_med3_f32 v35, v35, s17, v223
	v_med3_f32 v36, v36, s17, v223
	v_med3_f32 v37, v37, s17, v223
	v_pk_mul_f32 v[24:25], v[42:43], s[30:31] op_sel_hi:[1,0]
	v_pk_mul_f32 v[26:27], v[44:45], s[30:31] op_sel_hi:[1,0]
	v_pk_mul_f32 v[28:29], v[38:39], s[30:31] op_sel_hi:[1,0]
	v_pk_mul_f32 v[30:31], v[40:41], s[30:31] op_sel_hi:[1,0]
	v_pk_mul_f32 v[24:25], v[24:25], s[34:35] op_sel_hi:[1,0]
	v_pk_mul_f32 v[26:27], v[26:27], s[34:35] op_sel_hi:[1,0]
	v_pk_mul_f32 v[28:29], v[28:29], s[34:35] op_sel_hi:[1,0]
	v_pk_mul_f32 v[30:31], v[30:31], s[34:35] op_sel_hi:[1,0]
	v_exp_f32_e32 v24, v24
	v_exp_f32_e32 v25, v25
	v_exp_f32_e32 v26, v26
	v_exp_f32_e32 v27, v27
	v_exp_f32_e32 v28, v28
	v_exp_f32_e32 v29, v29
	v_exp_f32_e32 v30, v30
	v_exp_f32_e32 v31, v31
	v_pk_add_f32 v[24:25], v[24:25], 1.0 op_sel_hi:[1,0]
	v_pk_add_f32 v[26:27], v[26:27], 1.0 op_sel_hi:[1,0]
	v_pk_add_f32 v[28:29], v[28:29], 1.0 op_sel_hi:[1,0]
	v_pk_add_f32 v[30:31], v[30:31], 1.0 op_sel_hi:[1,0]
	v_rcp_f32_e32 v24, v24
	v_rcp_f32_e32 v25, v25
	v_rcp_f32_e32 v26, v26
	v_rcp_f32_e32 v27, v27
	v_rcp_f32_e32 v28, v28
	v_rcp_f32_e32 v29, v29
	v_rcp_f32_e32 v30, v30
	v_rcp_f32_e32 v31, v31
	v_pk_add_f32 v[46:47], v[46:47], 1.0 op_sel_hi:[1,0]
	v_pk_add_f32 v[48:49], v[48:49], 1.0 op_sel_hi:[1,0]
	v_pk_add_f32 v[34:35], v[34:35], 1.0 op_sel_hi:[1,0]
	v_pk_add_f32 v[36:37], v[36:37], 1.0 op_sel_hi:[1,0]
	v_pk_mul_f32 v[42:43], v[42:43], v[24:25]
	v_pk_mul_f32 v[44:45], v[44:45], v[26:27]
	v_pk_mul_f32 v[38:39], v[38:39], v[28:29]
	v_pk_mul_f32 v[40:41], v[40:41], v[30:31]
	v_pk_mul_f32 v[42:43], v[46:47], v[42:43]
	v_pk_mul_f32 v[44:45], v[48:49], v[44:45]
	v_pk_mul_f32 v[38:39], v[34:35], v[38:39]
	v_pk_mul_f32 v[40:41], v[36:37], v[40:41]
	v_cvt_pk_fp8_f32 v32, v42, v43
	v_cvt_pk_fp8_f32 v33, v38, v39
	v_cvt_pk_fp8_f32 v32, v44, v45 op_sel:[0,0,1]
	v_cvt_pk_fp8_f32 v33, v40, v41 op_sel:[0,0,1]
	s_mov_b32 s36, 0x2c000
	v_lshl_add_u64 v[22:23], v[18:19], 0, s[36:37]
	s_mov_b32 s13, 0x28000
	s_and_b64 vcc, exec, s[22:23]
	global_store_dwordx2 v[22:23], v[32:33], off
	s_cbranch_vccz .LBB0_1222
	v_readlane_b32 s24, v253, 4
	v_readlane_b32 s26, v253, 6
	v_readlane_b32 s27, v253, 7
	v_readlane_b32 s25, v253, 5
	s_and_b64 vcc, exec, s[0:1]
	v_mov_b64_e32 v[36:37], s[26:27]
	v_mov_b64_e32 v[156:157], s[26:27]
	v_mov_b64_e32 v[148:149], s[26:27]
	v_mov_b64_e32 v[140:141], s[26:27]
	v_mov_b64_e32 v[132:133], s[26:27]
	v_mov_b64_e32 v[124:125], s[26:27]
	v_mov_b64_e32 v[116:117], s[26:27]
	v_mov_b64_e32 v[108:109], s[26:27]
	v_mov_b64_e32 v[100:101], s[26:27]
	v_mov_b64_e32 v[160:161], s[26:27]
	v_mov_b64_e32 v[152:153], s[26:27]
	v_mov_b64_e32 v[144:145], s[26:27]
	v_mov_b64_e32 v[136:137], s[26:27]
	v_mov_b64_e32 v[128:129], s[26:27]
	v_mov_b64_e32 v[120:121], s[26:27]
	v_mov_b64_e32 v[112:113], s[26:27]
	v_mov_b64_e32 v[104:105], s[26:27]
	v_mov_b64_e32 v[92:93], s[26:27]
	v_mov_b64_e32 v[84:85], s[26:27]
	v_mov_b64_e32 v[76:77], s[26:27]
	v_mov_b64_e32 v[68:69], s[26:27]
	v_mov_b64_e32 v[60:61], s[26:27]
	v_mov_b64_e32 v[52:53], s[26:27]
	v_mov_b64_e32 v[44:45], s[26:27]
	v_mov_b64_e32 v[40:41], s[26:27]
	v_mov_b64_e32 v[96:97], s[26:27]
	v_mov_b64_e32 v[88:89], s[26:27]
	v_mov_b64_e32 v[80:81], s[26:27]
	v_mov_b64_e32 v[72:73], s[26:27]
	v_mov_b64_e32 v[64:65], s[26:27]
	v_mov_b64_e32 v[56:57], s[26:27]
	v_mov_b64_e32 v[48:49], s[26:27]
	v_mov_b64_e32 v[34:35], s[24:25]
	v_mov_b64_e32 v[154:155], s[24:25]
	v_mov_b64_e32 v[146:147], s[24:25]
	v_mov_b64_e32 v[138:139], s[24:25]
	v_mov_b64_e32 v[130:131], s[24:25]
	v_mov_b64_e32 v[122:123], s[24:25]
	v_mov_b64_e32 v[114:115], s[24:25]
	v_mov_b64_e32 v[106:107], s[24:25]
	v_mov_b64_e32 v[98:99], s[24:25]
	v_mov_b64_e32 v[158:159], s[24:25]
	v_mov_b64_e32 v[150:151], s[24:25]
	v_mov_b64_e32 v[142:143], s[24:25]
	v_mov_b64_e32 v[134:135], s[24:25]
	v_mov_b64_e32 v[126:127], s[24:25]
	v_mov_b64_e32 v[118:119], s[24:25]
	v_mov_b64_e32 v[110:111], s[24:25]
	v_mov_b64_e32 v[102:103], s[24:25]
	v_mov_b64_e32 v[90:91], s[24:25]
	v_mov_b64_e32 v[82:83], s[24:25]
	v_mov_b64_e32 v[74:75], s[24:25]
	v_mov_b64_e32 v[66:67], s[24:25]
	v_mov_b64_e32 v[58:59], s[24:25]
	v_mov_b64_e32 v[50:51], s[24:25]
	v_mov_b64_e32 v[42:43], s[24:25]
	v_mov_b64_e32 v[38:39], s[24:25]
	v_mov_b64_e32 v[94:95], s[24:25]
	v_mov_b64_e32 v[86:87], s[24:25]
	v_mov_b64_e32 v[78:79], s[24:25]
	v_mov_b64_e32 v[70:71], s[24:25]
	v_mov_b64_e32 v[62:63], s[24:25]
	v_mov_b64_e32 v[54:55], s[24:25]
	v_mov_b64_e32 v[46:47], s[24:25]
	s_cbranch_vccz .LBB0_1221
	s_barrier
	s_branch .LBB0_1221

.LBB0_1326:
	s_setprio 0
	v_lshl_or_b32 v18, s0, 8, v168
	v_ashrrev_i32_e32 v19, 31, v18
	s_mov_b32 s64, 0x1f000
	s_nop 15
	s_nop 3
